# GEMM K-loops: counter/pointer updates and exit compare moved in front of the loop-back barrier (on v11)
# baseline (speedup 1.0000x reference)
; #define PG8_STAGE(bufoff, gbase, voff) do { _Pragma("unroll") for (int _i = 0; _i < 2; ++_i) \
;         __builtin_amdgcn_global_load_lds((const unsigned*)((const char*)(gbase) + (voff)[_i]), (LAS unsigned*)(lds + (bufoff) + ldsw + _i * 8192), 16, 0, 0); } while (0)
; #define PG8_STAGE_A(bufoff, kptr, half, VO) do { if constexpr (GATHER) { _Pragma("unroll") for (int _i = 0; _i < 2; ++_i) \
;         __builtin_amdgcn_global_load_lds((const unsigned*)((const char*)(kptr) + (VO)[half][_i]), (LAS unsigned*)(lds + (bufoff) + ldsw + _i * 8192), 16, 0, 0); } \
;         else { PG8_STAGE(bufoff, (kptr) + (half) * hstepA, voffA); } } while (0)
; #define PG8_LDA(dst, b, h) do { _Pragma("unroll") for (int m = 0; m < 4; ++m) _Pragma("unroll") for (int k = 0; k < 2; ++k) dst[m][k] = *(const LAS bf16x8*)(lds + PG8_SA(b, h) + aoff + m * 2048 + k * 1024); } while (0)
; #define PG8_LDB(dst, b, h) do { _Pragma("unroll") for (int n = 0; n < 2; ++n) _Pragma("unroll") for (int k = 0; k < 2; ++k) dst[n][k] = *(const LAS bf16x8*)(lds + PG8_SB(b, h) + boff + n * 2048 + k * 1024); } while (0)
; #define PG8_WAIT_V(n) asm volatile("s_waitcnt vmcnt(" #n ")" ::: "memory")
; #define PG8_WAIT_L(n) asm volatile("s_waitcnt lgkmcnt(" #n ")" ::: "memory")
;     ...
;         for (int t = 0; t < nt; t += 2) {
;             const bool last = (t == nt - 2);
;             const char* a1 = cA + (size_t)(t + 1) * kstep;
;             const char* a2 = last ? nA : cA + (size_t)(t + 2) * kstep; const char* b2 = last ? nB : cB + (size_t)(t + 2) * kstep;
;             const char* a3 = a2 + kstep; const char* b3 = b2 + kstep;
;             unsigned g2[2][2];
;             if constexpr (GATHER) {
; #pragma unroll
;                 for (int _h = 0; _h < 2; ++_h)
; #pragma unroll
;                     for (int _i = 0; _i < 2; ++_i) g2[_h][_i] = last ? gN[_h][_i] : gC[_h][_i]; }
;             if constexpr (SP2) {
;             PG8_LDB(B0, 0, 0); PG8_LDB(B1, 0, 1); PG8_SCHED; PG8_LDA(At, 0, 0); PG8_STAGE_A(PG8_SA(1, 1), a1, 1, gC);
;             PG8_WAIT_V(8); PG8_WAIT_L(0); PG8_BAR; PG8_MMA(0, 0, At, B0); PG8_MMA(0, 1, At, B1); PG8_BAR; PG8_SCHED;
;             PG8_LDA(At, 0, 1); PG8_STAGE(PG8_SB(0, 0), b2, voffB); PG8_STAGE(PG8_SB(0, 1), b2 + hstepB, voffB); PG8_STAGE_A(PG8_SA(0, 0), a2, 0, g2);
;             PG8_WAIT_V(8); PG8_WAIT_L(0); PG8_BAR; PG8_MMA(1, 0, At, B0); PG8_MMA(1, 1, At, B1); PG8_BAR; PG8_SCHED;
.LBB0_224:
	s_add_u32 s0, s24, 0xfff80080
	s_addc_u32 s1, s25, -1
	s_add_i32 s20, 0, 0x10000
	s_cmp_eq_u32 s19, 28
	s_cselect_b32 s31, s4, s1
	s_cselect_b32 s30, s14, s0
	s_cselect_b32 s1, s15, s18
	s_cselect_b32 s0, s16, s17
	s_add_i32 s22, 0, 0x14000
	v_add_u32_e32 v160, s20, v143
	v_add_u32_e32 v176, s22, v143
	ds_read_b128 v[148:151], v160
	ds_read_b128 v[152:155], v160 offset:1024
	ds_read_b128 v[156:159], v160 offset:2048
	ds_read_b128 v[160:163], v160 offset:3072
	ds_read_b128 v[164:167], v176
	ds_read_b128 v[168:171], v176 offset:1024
	ds_read_b128 v[172:175], v176 offset:2048
	ds_read_b128 v[176:179], v176 offset:3072
	v_lshl_add_u64 v[204:205], s[24:25], 0, v[138:139]
	s_add_i32 m0, s13, 0xc000
	ds_read_b128 v[180:183], v147
	ds_read_b128 v[184:187], v147 offset:1024
	ds_read_b128 v[188:191], v147 offset:2048
	ds_read_b128 v[192:195], v147 offset:3072
	ds_read_b128 v[196:199], v147 offset:4096
	ds_read_b128 v[200:203], v147 offset:5120
	ds_read_b128 v[216:219], v147 offset:6144
	ds_read_b128 v[220:223], v147 offset:7168
	global_load_lds_dwordx4 v[204:205], off
	v_lshl_add_u64 v[204:205], s[24:25], 0, v[140:141]
	s_add_i32 m0, s13, 0xe000
	s_nop 0
	global_load_lds_dwordx4 v[204:205], off
	s_waitcnt vmcnt(8)
	s_waitcnt lgkmcnt(0)
	s_barrier
	s_setprio 1
	s_waitcnt lgkmcnt(0)
	v_mfma_f32_16x16x32_bf16 v[126:129], v[148:151], v[180:183], v[126:129]
	v_mfma_f32_16x16x32_bf16 v[122:125], v[156:159], v[180:183], v[122:125]
	v_mfma_f32_16x16x32_bf16 v[118:121], v[148:151], v[188:191], v[118:121]
	v_mfma_f32_16x16x32_bf16 v[114:117], v[156:159], v[188:191], v[114:117]
	v_mfma_f32_16x16x32_bf16 v[102:105], v[148:151], v[196:199], v[102:105]
	v_mfma_f32_16x16x32_bf16 v[98:101], v[156:159], v[196:199], v[98:101]
	v_mfma_f32_16x16x32_bf16 v[86:89], v[148:151], v[216:219], v[86:89]
	v_mfma_f32_16x16x32_bf16 v[82:85], v[156:159], v[216:219], v[82:85]
	v_mfma_f32_16x16x32_bf16 v[126:129], v[152:155], v[184:187], v[126:129]
	v_mfma_f32_16x16x32_bf16 v[122:125], v[160:163], v[184:187], v[122:125]
	v_mfma_f32_16x16x32_bf16 v[118:121], v[152:155], v[192:195], v[118:121]
	v_mfma_f32_16x16x32_bf16 v[114:117], v[160:163], v[192:195], v[114:117]
	v_mfma_f32_16x16x32_bf16 v[102:105], v[152:155], v[200:203], v[102:105]
	v_mfma_f32_16x16x32_bf16 v[98:101], v[160:163], v[200:203], v[98:101]
	v_mfma_f32_16x16x32_bf16 v[86:89], v[152:155], v[220:223], v[86:89]
	v_mfma_f32_16x16x32_bf16 v[82:85], v[160:163], v[220:223], v[82:85]
	s_setprio 0
	s_setprio 1
	v_mfma_f32_16x16x32_bf16 v[110:113], v[164:167], v[180:183], v[110:113]
	v_mfma_f32_16x16x32_bf16 v[106:109], v[172:175], v[180:183], v[106:109]
	v_mfma_f32_16x16x32_bf16 v[94:97], v[164:167], v[188:191], v[94:97]
	v_mfma_f32_16x16x32_bf16 v[90:93], v[172:175], v[188:191], v[90:93]
	v_mfma_f32_16x16x32_bf16 v[78:81], v[164:167], v[196:199], v[78:81]
	v_mfma_f32_16x16x32_bf16 v[74:77], v[172:175], v[196:199], v[74:77]
	v_mfma_f32_16x16x32_bf16 v[70:73], v[164:167], v[216:219], v[70:73]
	v_mfma_f32_16x16x32_bf16 v[66:69], v[172:175], v[216:219], v[66:69]
	v_mfma_f32_16x16x32_bf16 v[110:113], v[168:171], v[184:187], v[110:113]
	v_mfma_f32_16x16x32_bf16 v[106:109], v[176:179], v[184:187], v[106:109]
	v_mfma_f32_16x16x32_bf16 v[94:97], v[168:171], v[192:195], v[94:97]
	v_mfma_f32_16x16x32_bf16 v[90:93], v[176:179], v[192:195], v[90:93]
	v_mfma_f32_16x16x32_bf16 v[78:81], v[168:171], v[200:203], v[78:81]
	v_mfma_f32_16x16x32_bf16 v[74:77], v[176:179], v[200:203], v[74:77]
	v_mfma_f32_16x16x32_bf16 v[70:73], v[168:171], v[220:223], v[70:73]
	v_mfma_f32_16x16x32_bf16 v[66:69], v[176:179], v[220:223], v[66:69]
	s_setprio 0
	s_barrier
	s_add_i32 s20, s20, s12
	v_lshl_add_u64 v[204:205], s[0:1], 0, v[132:133]
	s_mov_b32 m0, s20
	ds_read_b128 v[180:183], v147 offset:16384
	ds_read_b128 v[184:187], v147 offset:17408
	ds_read_b128 v[188:191], v147 offset:18432
	ds_read_b128 v[192:195], v147 offset:19456
	ds_read_b128 v[196:199], v147 offset:20480
	ds_read_b128 v[200:203], v147 offset:21504
	ds_read_b128 v[216:219], v147 offset:22528
	ds_read_b128 v[220:223], v147 offset:23552
	global_load_lds_dwordx4 v[204:205], off
	s_add_i32 m0, s20, 0x2000
	s_add_u32 s20, s0, 0x80000
	v_lshl_add_u64 v[208:209], s[0:1], 0, v[136:137]
	s_addc_u32 s21, s1, 0
	s_add_i32 s22, s22, s12
	global_load_lds_dwordx4 v[208:209], off
	v_lshl_add_u64 v[210:211], s[20:21], 0, v[132:133]
	s_mov_b32 m0, s22
	v_lshl_add_u64 v[212:213], s[30:31], 0, v[134:135]
	global_load_lds_dwordx4 v[210:211], off
	v_lshl_add_u64 v[210:211], s[20:21], 0, v[136:137]
	s_add_i32 m0, s22, 0x2000
	s_nop 0
	global_load_lds_dwordx4 v[210:211], off
	v_lshl_add_u64 v[210:211], s[30:31], 0, v[130:131]
	s_mov_b32 m0, s13
	s_nop 0
	global_load_lds_dwordx4 v[210:211], off
	s_mov_b32 m0, s26
	s_nop 0
	global_load_lds_dwordx4 v[212:213], off
	s_waitcnt vmcnt(8)
	s_waitcnt lgkmcnt(0)
	s_barrier
; #define PG8_STAGE_A(bufoff, kptr, half, VO) do { if constexpr (GATHER) { _Pragma("unroll") for (int _i = 0; _i < 2; ++_i) \
;         __builtin_amdgcn_global_load_lds((const unsigned*)((const char*)(kptr) + (VO)[half][_i]), (LAS unsigned*)(lds + (bufoff) + ldsw + _i * 8192), 16, 0, 0); } \
;         else { PG8_STAGE(bufoff, (kptr) + (half) * hstepA, voffA); } } while (0)
; #define PG8_LDA(dst, b, h) do { _Pragma("unroll") for (int m = 0; m < 4; ++m) _Pragma("unroll") for (int k = 0; k < 2; ++k) dst[m][k] = *(const LAS bf16x8*)(lds + PG8_SA(b, h) + aoff + m * 2048 + k * 1024); } while (0)
; #define PG8_LDB(dst, b, h) do { _Pragma("unroll") for (int n = 0; n < 2; ++n) _Pragma("unroll") for (int k = 0; k < 2; ++k) dst[n][k] = *(const LAS bf16x8*)(lds + PG8_SB(b, h) + boff + n * 2048 + k * 1024); } while (0)
; #define PG8_MMA(ai, bj, At, Bt) do { __builtin_amdgcn_s_setprio(1); _Pragma("unroll") for (int m = 0; m < 4; ++m) _Pragma("unroll") for (int n = 0; n < 2; ++n) _Pragma("unroll") for (int k = 0; k < 2; ++k) \
;         acc[ai][bj][m][n] = __builtin_amdgcn_mfma_f32_16x16x32_bf16(Bt[n][k], At[m][k], acc[ai][bj][m][n], 0, 0, 0); __builtin_amdgcn_s_setprio(0); } while (0)
; #define PG8_WAIT_V(n) asm volatile("s_waitcnt vmcnt(" #n ")" ::: "memory")
; #define PG8_WAIT_L(n) asm volatile("s_waitcnt lgkmcnt(" #n ")" ::: "memory")
; #define PG8_BAR __builtin_amdgcn_s_barrier()
; #define PG8_SCHED __builtin_amdgcn_sched_barrier(0)
;     ...
;             PG8_WAIT_V(8); PG8_WAIT_L(0); PG8_BAR; PG8_MMA(1, 0, At, B0); PG8_MMA(1, 1, At, B1); PG8_BAR; PG8_SCHED;
;             PG8_LDB(B0, 1, 0); PG8_LDB(B1, 1, 1); PG8_SCHED; PG8_LDA(At, 1, 0); PG8_STAGE_A(PG8_SA(0, 1), a2, 1, g2);
;             PG8_WAIT_V(8); PG8_WAIT_L(0); PG8_BAR; PG8_MMA(0, 0, At, B0); PG8_MMA(0, 1, At, B1); PG8_BAR; PG8_SCHED;
	s_setprio 1
	s_waitcnt lgkmcnt(0)
	v_mfma_f32_16x16x32_bf16 v[62:65], v[148:151], v[180:183], v[62:65]
	v_mfma_f32_16x16x32_bf16 v[58:61], v[156:159], v[180:183], v[58:61]
	v_mfma_f32_16x16x32_bf16 v[54:57], v[148:151], v[188:191], v[54:57]
	v_mfma_f32_16x16x32_bf16 v[50:53], v[156:159], v[188:191], v[50:53]
	v_mfma_f32_16x16x32_bf16 v[38:41], v[148:151], v[196:199], v[38:41]
	v_mfma_f32_16x16x32_bf16 v[34:37], v[156:159], v[196:199], v[34:37]
	v_mfma_f32_16x16x32_bf16 v[22:25], v[148:151], v[216:219], v[22:25]
	v_mfma_f32_16x16x32_bf16 v[18:21], v[156:159], v[216:219], v[18:21]
	v_mfma_f32_16x16x32_bf16 v[62:65], v[152:155], v[184:187], v[62:65]
	v_mfma_f32_16x16x32_bf16 v[58:61], v[160:163], v[184:187], v[58:61]
	v_mfma_f32_16x16x32_bf16 v[54:57], v[152:155], v[192:195], v[54:57]
	v_mfma_f32_16x16x32_bf16 v[50:53], v[160:163], v[192:195], v[50:53]
	v_mfma_f32_16x16x32_bf16 v[38:41], v[152:155], v[200:203], v[38:41]
	v_mfma_f32_16x16x32_bf16 v[34:37], v[160:163], v[200:203], v[34:37]
	v_mfma_f32_16x16x32_bf16 v[22:25], v[152:155], v[220:223], v[22:25]
	v_mfma_f32_16x16x32_bf16 v[18:21], v[160:163], v[220:223], v[18:21]
	s_setprio 0
	s_setprio 1
	v_mfma_f32_16x16x32_bf16 v[46:49], v[164:167], v[180:183], v[46:49]
	v_mfma_f32_16x16x32_bf16 v[42:45], v[172:175], v[180:183], v[42:45]
	v_mfma_f32_16x16x32_bf16 v[30:33], v[164:167], v[188:191], v[30:33]
	v_mfma_f32_16x16x32_bf16 v[26:29], v[172:175], v[188:191], v[26:29]
	v_mfma_f32_16x16x32_bf16 v[14:17], v[164:167], v[196:199], v[14:17]
	v_mfma_f32_16x16x32_bf16 v[10:13], v[172:175], v[196:199], v[10:13]
	v_mfma_f32_16x16x32_bf16 v[6:9], v[164:167], v[216:219], v[6:9]
	v_mfma_f32_16x16x32_bf16 v[2:5], v[172:175], v[216:219], v[2:5]
	v_mfma_f32_16x16x32_bf16 v[46:49], v[168:171], v[184:187], v[46:49]
	v_mfma_f32_16x16x32_bf16 v[42:45], v[176:179], v[184:187], v[42:45]
	v_mfma_f32_16x16x32_bf16 v[30:33], v[168:171], v[192:195], v[30:33]
	v_mfma_f32_16x16x32_bf16 v[26:29], v[176:179], v[192:195], v[26:29]
	v_mfma_f32_16x16x32_bf16 v[14:17], v[168:171], v[200:203], v[14:17]
	v_mfma_f32_16x16x32_bf16 v[10:13], v[176:179], v[200:203], v[10:13]
	v_mfma_f32_16x16x32_bf16 v[6:9], v[168:171], v[220:223], v[6:9]
	v_mfma_f32_16x16x32_bf16 v[2:5], v[176:179], v[220:223], v[2:5]
	s_setprio 0
	s_barrier
	s_add_i32 s22, 0, 0x18000
	s_add_i32 s23, 0, 0x1c000
	v_add_u32_e32 v160, s22, v143
	v_add_u32_e32 v176, s23, v143
	ds_read_b128 v[148:151], v160
	ds_read_b128 v[152:155], v160 offset:1024
	ds_read_b128 v[156:159], v160 offset:2048
	ds_read_b128 v[160:163], v160 offset:3072
	ds_read_b128 v[164:167], v176
	ds_read_b128 v[168:171], v176 offset:1024
	ds_read_b128 v[172:175], v176 offset:2048
	ds_read_b128 v[176:179], v176 offset:3072
	s_add_u32 s20, s30, 0x80000
	s_addc_u32 s21, s31, 0
	s_mov_b32 m0, s27
	v_lshl_add_u64 v[224:225], s[20:21], 0, v[130:131]
	ds_read_b128 v[180:183], v147 offset:32768
	ds_read_b128 v[184:187], v147 offset:33792
	ds_read_b128 v[188:191], v147 offset:34816
	ds_read_b128 v[192:195], v147 offset:35840
	ds_read_b128 v[196:199], v147 offset:36864
	ds_read_b128 v[200:203], v147 offset:37888
	ds_read_b128 v[216:219], v147 offset:38912
	ds_read_b128 v[220:223], v147 offset:39936
	global_load_lds_dwordx4 v[224:225], off
	v_lshl_add_u64 v[224:225], s[20:21], 0, v[134:135]
	s_mov_b32 m0, s48
	s_nop 0
	global_load_lds_dwordx4 v[224:225], off
	s_waitcnt vmcnt(8)
	s_waitcnt lgkmcnt(0)
	s_barrier
	s_setprio 1
	s_waitcnt lgkmcnt(0)
	v_mfma_f32_16x16x32_bf16 v[126:129], v[148:151], v[180:183], v[126:129]
	v_mfma_f32_16x16x32_bf16 v[122:125], v[156:159], v[180:183], v[122:125]
	v_mfma_f32_16x16x32_bf16 v[118:121], v[148:151], v[188:191], v[118:121]
	v_mfma_f32_16x16x32_bf16 v[114:117], v[156:159], v[188:191], v[114:117]
	v_mfma_f32_16x16x32_bf16 v[102:105], v[148:151], v[196:199], v[102:105]
	v_mfma_f32_16x16x32_bf16 v[98:101], v[156:159], v[196:199], v[98:101]
	v_mfma_f32_16x16x32_bf16 v[86:89], v[148:151], v[216:219], v[86:89]
	v_mfma_f32_16x16x32_bf16 v[82:85], v[156:159], v[216:219], v[82:85]
	v_mfma_f32_16x16x32_bf16 v[126:129], v[152:155], v[184:187], v[126:129]
	v_mfma_f32_16x16x32_bf16 v[122:125], v[160:163], v[184:187], v[122:125]
	v_mfma_f32_16x16x32_bf16 v[118:121], v[152:155], v[192:195], v[118:121]
	v_mfma_f32_16x16x32_bf16 v[114:117], v[160:163], v[192:195], v[114:117]
	v_mfma_f32_16x16x32_bf16 v[102:105], v[152:155], v[200:203], v[102:105]
	v_mfma_f32_16x16x32_bf16 v[98:101], v[160:163], v[200:203], v[98:101]
	v_mfma_f32_16x16x32_bf16 v[86:89], v[152:155], v[220:223], v[86:89]
	v_mfma_f32_16x16x32_bf16 v[82:85], v[160:163], v[220:223], v[82:85]
	s_setprio 0
	s_setprio 1
	v_mfma_f32_16x16x32_bf16 v[110:113], v[164:167], v[180:183], v[110:113]
	v_mfma_f32_16x16x32_bf16 v[106:109], v[172:175], v[180:183], v[106:109]
	v_mfma_f32_16x16x32_bf16 v[94:97], v[164:167], v[188:191], v[94:97]
	v_mfma_f32_16x16x32_bf16 v[90:93], v[172:175], v[188:191], v[90:93]
	v_mfma_f32_16x16x32_bf16 v[78:81], v[164:167], v[196:199], v[78:81]
	v_mfma_f32_16x16x32_bf16 v[74:77], v[172:175], v[196:199], v[74:77]
	v_mfma_f32_16x16x32_bf16 v[70:73], v[164:167], v[216:219], v[70:73]
	v_mfma_f32_16x16x32_bf16 v[66:69], v[172:175], v[216:219], v[66:69]
	v_mfma_f32_16x16x32_bf16 v[110:113], v[168:171], v[184:187], v[110:113]
	v_mfma_f32_16x16x32_bf16 v[106:109], v[176:179], v[184:187], v[106:109]
	v_mfma_f32_16x16x32_bf16 v[94:97], v[168:171], v[192:195], v[94:97]
	v_mfma_f32_16x16x32_bf16 v[90:93], v[176:179], v[192:195], v[90:93]
	v_mfma_f32_16x16x32_bf16 v[78:81], v[168:171], v[200:203], v[78:81]
	v_mfma_f32_16x16x32_bf16 v[74:77], v[176:179], v[200:203], v[74:77]
	v_mfma_f32_16x16x32_bf16 v[70:73], v[168:171], v[220:223], v[70:73]
	v_mfma_f32_16x16x32_bf16 v[66:69], v[176:179], v[220:223], v[66:69]
	s_setprio 0
	s_barrier
; #define PG8_STAGE(bufoff, gbase, voff) do { _Pragma("unroll") for (int _i = 0; _i < 2; ++_i) \
;         __builtin_amdgcn_global_load_lds((const unsigned*)((const char*)(gbase) + (voff)[_i]), (LAS unsigned*)(lds + (bufoff) + ldsw + _i * 8192), 16, 0, 0); } while (0)
; #define PG8_STAGE_A(bufoff, kptr, half, VO) do { if constexpr (GATHER) { _Pragma("unroll") for (int _i = 0; _i < 2; ++_i) \
;         __builtin_amdgcn_global_load_lds((const unsigned*)((const char*)(kptr) + (VO)[half][_i]), (LAS unsigned*)(lds + (bufoff) + ldsw + _i * 8192), 16, 0, 0); } \
;         else { PG8_STAGE(bufoff, (kptr) + (half) * hstepA, voffA); } } while (0)
; #define PG8_LDA(dst, b, h) do { _Pragma("unroll") for (int m = 0; m < 4; ++m) _Pragma("unroll") for (int k = 0; k < 2; ++k) dst[m][k] = *(const LAS bf16x8*)(lds + PG8_SA(b, h) + aoff + m * 2048 + k * 1024); } while (0)
; #define PG8_MMA(ai, bj, At, Bt) do { __builtin_amdgcn_s_setprio(1); _Pragma("unroll") for (int m = 0; m < 4; ++m) _Pragma("unroll") for (int n = 0; n < 2; ++n) _Pragma("unroll") for (int k = 0; k < 2; ++k) \
;         acc[ai][bj][m][n] = __builtin_amdgcn_mfma_f32_16x16x32_bf16(Bt[n][k], At[m][k], acc[ai][bj][m][n], 0, 0, 0); __builtin_amdgcn_s_setprio(0); } while (0)
; #define PG8_WAIT_V(n) asm volatile("s_waitcnt vmcnt(" #n ")" ::: "memory")
; #define PG8_WAIT_L(n) asm volatile("s_waitcnt lgkmcnt(" #n ")" ::: "memory")
; #define PG8_BAR __builtin_amdgcn_s_barrier()
; #define PG8_SCHED __builtin_amdgcn_sched_barrier(0)
;     ...
;         for (int t = 0; t < nt; t += 2) {
;     ...
;             PG8_LDA(At, 1, 1); PG8_STAGE(PG8_SB(1, 0), b3, voffB); PG8_STAGE(PG8_SB(1, 1), b3 + hstepB, voffB); PG8_STAGE_A(PG8_SA(1, 0), a3, 0, g2);
;             PG8_WAIT_V(8); PG8_WAIT_L(0); PG8_BAR; PG8_MMA(1, 0, At, B0); PG8_MMA(1, 1, At, B1); PG8_BAR; PG8_SCHED;
	s_add_i32 s20, s22, s12
	v_lshl_add_u64 v[204:205], v[204:205], 0, s[8:9]
	s_mov_b32 m0, s20
	ds_read_b128 v[180:183], v147 offset:49152
	ds_read_b128 v[184:187], v147 offset:50176
	ds_read_b128 v[188:191], v147 offset:51200
	ds_read_b128 v[192:195], v147 offset:52224
	ds_read_b128 v[196:199], v147 offset:53248
	ds_read_b128 v[200:203], v147 offset:54272
	ds_read_b128 v[216:219], v147 offset:55296
	ds_read_b128 v[220:223], v147 offset:56320
	global_load_lds_dwordx4 v[204:205], off
	s_add_i32 m0, s20, 0x2000
	s_add_u32 s0, s0, 0x80080
	v_lshl_add_u64 v[204:205], v[208:209], 0, s[8:9]
	s_addc_u32 s1, s1, 0
	s_add_i32 s20, s23, s12
	global_load_lds_dwordx4 v[204:205], off
	v_lshl_add_u64 v[204:205], s[0:1], 0, v[132:133]
	s_mov_b32 m0, s20
	s_nop 0
	global_load_lds_dwordx4 v[204:205], off
	v_lshl_add_u64 v[204:205], s[0:1], 0, v[136:137]
	s_add_i32 m0, s20, 0x2000
	s_nop 0
	global_load_lds_dwordx4 v[204:205], off
	v_lshl_add_u64 v[204:205], v[210:211], 0, s[8:9]
	s_mov_b32 m0, s49
	s_nop 0
	global_load_lds_dwordx4 v[204:205], off
	v_lshl_add_u64 v[204:205], v[212:213], 0, s[8:9]
	s_mov_b32 m0, s50
	s_nop 0
	global_load_lds_dwordx4 v[204:205], off
	s_waitcnt vmcnt(8)
	s_waitcnt lgkmcnt(0)
	s_barrier
	s_setprio 1
	s_waitcnt lgkmcnt(0)
	v_mfma_f32_16x16x32_bf16 v[62:65], v[148:151], v[180:183], v[62:65]
	v_mfma_f32_16x16x32_bf16 v[58:61], v[156:159], v[180:183], v[58:61]
	v_mfma_f32_16x16x32_bf16 v[54:57], v[148:151], v[188:191], v[54:57]
	v_mfma_f32_16x16x32_bf16 v[50:53], v[156:159], v[188:191], v[50:53]
	v_mfma_f32_16x16x32_bf16 v[38:41], v[148:151], v[196:199], v[38:41]
	v_mfma_f32_16x16x32_bf16 v[34:37], v[156:159], v[196:199], v[34:37]
	v_mfma_f32_16x16x32_bf16 v[22:25], v[148:151], v[216:219], v[22:25]
	v_mfma_f32_16x16x32_bf16 v[18:21], v[156:159], v[216:219], v[18:21]
	v_mfma_f32_16x16x32_bf16 v[62:65], v[152:155], v[184:187], v[62:65]
	v_mfma_f32_16x16x32_bf16 v[58:61], v[160:163], v[184:187], v[58:61]
	v_mfma_f32_16x16x32_bf16 v[54:57], v[152:155], v[192:195], v[54:57]
	v_mfma_f32_16x16x32_bf16 v[50:53], v[160:163], v[192:195], v[50:53]
	v_mfma_f32_16x16x32_bf16 v[38:41], v[152:155], v[200:203], v[38:41]
	v_mfma_f32_16x16x32_bf16 v[34:37], v[160:163], v[200:203], v[34:37]
	v_mfma_f32_16x16x32_bf16 v[22:25], v[152:155], v[220:223], v[22:25]
	v_mfma_f32_16x16x32_bf16 v[18:21], v[160:163], v[220:223], v[18:21]
	s_setprio 0
	s_setprio 1
	v_mfma_f32_16x16x32_bf16 v[46:49], v[164:167], v[180:183], v[46:49]
	v_mfma_f32_16x16x32_bf16 v[42:45], v[172:175], v[180:183], v[42:45]
	v_mfma_f32_16x16x32_bf16 v[30:33], v[164:167], v[188:191], v[30:33]
	v_mfma_f32_16x16x32_bf16 v[26:29], v[172:175], v[188:191], v[26:29]
	v_mfma_f32_16x16x32_bf16 v[14:17], v[164:167], v[196:199], v[14:17]
	v_mfma_f32_16x16x32_bf16 v[10:13], v[172:175], v[196:199], v[10:13]
	v_mfma_f32_16x16x32_bf16 v[6:9], v[164:167], v[216:219], v[6:9]
	v_mfma_f32_16x16x32_bf16 v[2:5], v[172:175], v[216:219], v[2:5]
	v_mfma_f32_16x16x32_bf16 v[46:49], v[168:171], v[184:187], v[46:49]
	v_mfma_f32_16x16x32_bf16 v[42:45], v[176:179], v[184:187], v[42:45]
	v_mfma_f32_16x16x32_bf16 v[30:33], v[168:171], v[192:195], v[30:33]
	v_mfma_f32_16x16x32_bf16 v[26:29], v[176:179], v[192:195], v[26:29]
	v_mfma_f32_16x16x32_bf16 v[14:17], v[168:171], v[200:203], v[14:17]
	v_mfma_f32_16x16x32_bf16 v[10:13], v[176:179], v[200:203], v[10:13]
	v_mfma_f32_16x16x32_bf16 v[6:9], v[168:171], v[220:223], v[6:9]
	v_mfma_f32_16x16x32_bf16 v[2:5], v[176:179], v[220:223], v[2:5]
	s_add_i32 s19, s19, 2
	s_add_u32 s24, s24, 0x100
	s_addc_u32 s25, s25, 0
	s_add_u32 s17, s17, 0x100
	s_addc_u32 s18, s18, 0
	s_cmp_gt_u32 s19, 29
	s_setprio 0
	s_barrier
	s_cbranch_scc0 .LBB0_224
	s_and_b64 vcc, exec, s[36:37]
	s_cbranch_vccz .LBB0_227
	s_barrier

; #define PG8_STAGE(bufoff, gbase, voff) do { _Pragma("unroll") for (int _i = 0; _i < 2; ++_i) \
;         __builtin_amdgcn_global_load_lds((const unsigned*)((const char*)(gbase) + (voff)[_i]), (LAS unsigned*)(lds + (bufoff) + ldsw + _i * 8192), 16, 0, 0); } while (0)
; #define PG8_STAGE_A(bufoff, kptr, half, VO) do { if constexpr (GATHER) { _Pragma("unroll") for (int _i = 0; _i < 2; ++_i) \
;         __builtin_amdgcn_global_load_lds((const unsigned*)((const char*)(kptr) + (VO)[half][_i]), (LAS unsigned*)(lds + (bufoff) + ldsw + _i * 8192), 16, 0, 0); } \
;         else { PG8_STAGE(bufoff, (kptr) + (half) * hstepA, voffA); } } while (0)
; #define PG8_LDA(dst, b, h) do { _Pragma("unroll") for (int m = 0; m < 4; ++m) _Pragma("unroll") for (int k = 0; k < 2; ++k) dst[m][k] = *(const LAS bf16x8*)(lds + PG8_SA(b, h) + aoff + m * 2048 + k * 1024); } while (0)
; #define PG8_LDB(dst, b, h) do { _Pragma("unroll") for (int n = 0; n < 2; ++n) _Pragma("unroll") for (int k = 0; k < 2; ++k) dst[n][k] = *(const LAS bf16x8*)(lds + PG8_SB(b, h) + boff + n * 2048 + k * 1024); } while (0)
; #define PG8_WAIT_V(n) asm volatile("s_waitcnt vmcnt(" #n ")" ::: "memory")
; #define PG8_WAIT_L(n) asm volatile("s_waitcnt lgkmcnt(" #n ")" ::: "memory")
;     ...
;         for (int t = 0; t < nt; t += 2) {
;             const bool last = (t == nt - 2);
;             const char* a1 = cA + (size_t)(t + 1) * kstep;
;             const char* a2 = last ? nA : cA + (size_t)(t + 2) * kstep; const char* b2 = last ? nB : cB + (size_t)(t + 2) * kstep;
;             const char* a3 = a2 + kstep; const char* b3 = b2 + kstep;
;             unsigned g2[2][2];
;             if constexpr (GATHER) {
; #pragma unroll
;                 for (int _h = 0; _h < 2; ++_h)
; #pragma unroll
;                     for (int _i = 0; _i < 2; ++_i) g2[_h][_i] = last ? gN[_h][_i] : gC[_h][_i]; }
;             if constexpr (SP2) {
;             PG8_LDB(B0, 0, 0); PG8_LDB(B1, 0, 1); PG8_SCHED; PG8_LDA(At, 0, 0); PG8_STAGE_A(PG8_SA(1, 1), a1, 1, gC);
;             PG8_WAIT_V(8); PG8_WAIT_L(0); PG8_BAR; PG8_MMA(0, 0, At, B0); PG8_MMA(0, 1, At, B1); PG8_BAR; PG8_SCHED;
;             PG8_LDA(At, 0, 1); PG8_STAGE(PG8_SB(0, 0), b2, voffB); PG8_STAGE(PG8_SB(0, 1), b2 + hstepB, voffB); PG8_STAGE_A(PG8_SA(0, 0), a2, 0, g2);
;             PG8_WAIT_V(8); PG8_WAIT_L(0); PG8_BAR; PG8_MMA(1, 0, At, B0); PG8_MMA(1, 1, At, B1); PG8_BAR; PG8_SCHED;
.LBB0_402:
	s_add_u32 s0, s24, 0xfff80080
	s_addc_u32 s1, s25, -1
	s_add_i32 s16, 0, 0x10000
	s_cmp_eq_u32 s15, 28
	s_cselect_b32 s31, s45, s1
	s_cselect_b32 s30, s44, s0
	s_cselect_b32 s1, s47, s14
	s_cselect_b32 s0, s46, s13
	s_add_i32 s18, 0, 0x14000
	v_add_u32_e32 v160, s16, v143
	v_add_u32_e32 v176, s18, v143
	ds_read_b128 v[148:151], v160
	ds_read_b128 v[152:155], v160 offset:1024
	ds_read_b128 v[156:159], v160 offset:2048
	ds_read_b128 v[160:163], v160 offset:3072
	ds_read_b128 v[164:167], v176
	ds_read_b128 v[168:171], v176 offset:1024
	ds_read_b128 v[172:175], v176 offset:2048
	ds_read_b128 v[176:179], v176 offset:3072
	v_lshl_add_u64 v[204:205], s[24:25], 0, v[138:139]
	s_add_i32 m0, s27, 0xc000
	ds_read_b128 v[180:183], v147
	ds_read_b128 v[184:187], v147 offset:1024
	ds_read_b128 v[188:191], v147 offset:2048
	ds_read_b128 v[192:195], v147 offset:3072
	ds_read_b128 v[196:199], v147 offset:4096
	ds_read_b128 v[200:203], v147 offset:5120
	ds_read_b128 v[216:219], v147 offset:6144
	ds_read_b128 v[220:223], v147 offset:7168
	global_load_lds_dwordx4 v[204:205], off
	v_lshl_add_u64 v[204:205], s[24:25], 0, v[140:141]
	s_add_i32 m0, s27, 0xe000
	s_nop 0
	global_load_lds_dwordx4 v[204:205], off
	s_waitcnt vmcnt(8)
	s_waitcnt lgkmcnt(0)
	s_barrier
	s_setprio 1
	s_waitcnt lgkmcnt(0)
	v_mfma_f32_16x16x32_bf16 v[126:129], v[148:151], v[180:183], v[126:129]
	v_mfma_f32_16x16x32_bf16 v[122:125], v[156:159], v[180:183], v[122:125]
	v_mfma_f32_16x16x32_bf16 v[118:121], v[148:151], v[188:191], v[118:121]
	v_mfma_f32_16x16x32_bf16 v[114:117], v[156:159], v[188:191], v[114:117]
	v_mfma_f32_16x16x32_bf16 v[102:105], v[148:151], v[196:199], v[102:105]
	v_mfma_f32_16x16x32_bf16 v[98:101], v[156:159], v[196:199], v[98:101]
	v_mfma_f32_16x16x32_bf16 v[86:89], v[148:151], v[216:219], v[86:89]
	v_mfma_f32_16x16x32_bf16 v[82:85], v[156:159], v[216:219], v[82:85]
	v_mfma_f32_16x16x32_bf16 v[126:129], v[152:155], v[184:187], v[126:129]
	v_mfma_f32_16x16x32_bf16 v[122:125], v[160:163], v[184:187], v[122:125]
	v_mfma_f32_16x16x32_bf16 v[118:121], v[152:155], v[192:195], v[118:121]
	v_mfma_f32_16x16x32_bf16 v[114:117], v[160:163], v[192:195], v[114:117]
	v_mfma_f32_16x16x32_bf16 v[102:105], v[152:155], v[200:203], v[102:105]
	v_mfma_f32_16x16x32_bf16 v[98:101], v[160:163], v[200:203], v[98:101]
	v_mfma_f32_16x16x32_bf16 v[86:89], v[152:155], v[220:223], v[86:89]
	v_mfma_f32_16x16x32_bf16 v[82:85], v[160:163], v[220:223], v[82:85]
	s_setprio 0
	s_setprio 1
	v_mfma_f32_16x16x32_bf16 v[110:113], v[164:167], v[180:183], v[110:113]
	v_mfma_f32_16x16x32_bf16 v[106:109], v[172:175], v[180:183], v[106:109]
	v_mfma_f32_16x16x32_bf16 v[94:97], v[164:167], v[188:191], v[94:97]
	v_mfma_f32_16x16x32_bf16 v[90:93], v[172:175], v[188:191], v[90:93]
	v_mfma_f32_16x16x32_bf16 v[78:81], v[164:167], v[196:199], v[78:81]
	v_mfma_f32_16x16x32_bf16 v[74:77], v[172:175], v[196:199], v[74:77]
	v_mfma_f32_16x16x32_bf16 v[70:73], v[164:167], v[216:219], v[70:73]
	v_mfma_f32_16x16x32_bf16 v[66:69], v[172:175], v[216:219], v[66:69]
	v_mfma_f32_16x16x32_bf16 v[110:113], v[168:171], v[184:187], v[110:113]
	v_mfma_f32_16x16x32_bf16 v[106:109], v[176:179], v[184:187], v[106:109]
	v_mfma_f32_16x16x32_bf16 v[94:97], v[168:171], v[192:195], v[94:97]
	v_mfma_f32_16x16x32_bf16 v[90:93], v[176:179], v[192:195], v[90:93]
	v_mfma_f32_16x16x32_bf16 v[78:81], v[168:171], v[200:203], v[78:81]
	v_mfma_f32_16x16x32_bf16 v[74:77], v[176:179], v[200:203], v[74:77]
	v_mfma_f32_16x16x32_bf16 v[70:73], v[168:171], v[220:223], v[70:73]
	v_mfma_f32_16x16x32_bf16 v[66:69], v[176:179], v[220:223], v[66:69]
	s_setprio 0
	s_barrier
	s_add_i32 s16, s16, s26
	v_lshl_add_u64 v[204:205], s[0:1], 0, v[132:133]
	s_mov_b32 m0, s16
	ds_read_b128 v[180:183], v147 offset:16384
	ds_read_b128 v[184:187], v147 offset:17408
	ds_read_b128 v[188:191], v147 offset:18432
	ds_read_b128 v[192:195], v147 offset:19456
	ds_read_b128 v[196:199], v147 offset:20480
	ds_read_b128 v[200:203], v147 offset:21504
	ds_read_b128 v[216:219], v147 offset:22528
	ds_read_b128 v[220:223], v147 offset:23552
	global_load_lds_dwordx4 v[204:205], off
	s_add_i32 m0, s16, 0x2000
	s_add_u32 s16, s0, 0x80000
	v_lshl_add_u64 v[208:209], s[0:1], 0, v[136:137]
	s_addc_u32 s17, s1, 0
	s_add_i32 s18, s18, s26
	global_load_lds_dwordx4 v[208:209], off
	v_lshl_add_u64 v[210:211], s[16:17], 0, v[132:133]
	s_mov_b32 m0, s18
	v_lshl_add_u64 v[212:213], s[30:31], 0, v[134:135]
	global_load_lds_dwordx4 v[210:211], off
	v_lshl_add_u64 v[210:211], s[16:17], 0, v[136:137]
	s_add_i32 m0, s18, 0x2000
	s_nop 0
	global_load_lds_dwordx4 v[210:211], off
	v_lshl_add_u64 v[210:211], s[30:31], 0, v[130:131]
	s_mov_b32 m0, s27
	s_nop 0
	global_load_lds_dwordx4 v[210:211], off
	s_mov_b32 m0, s41
	s_nop 0
	global_load_lds_dwordx4 v[212:213], off
	s_waitcnt vmcnt(8)
	s_waitcnt lgkmcnt(0)
	s_barrier
; #define PG8_STAGE_A(bufoff, kptr, half, VO) do { if constexpr (GATHER) { _Pragma("unroll") for (int _i = 0; _i < 2; ++_i) \
;         __builtin_amdgcn_global_load_lds((const unsigned*)((const char*)(kptr) + (VO)[half][_i]), (LAS unsigned*)(lds + (bufoff) + ldsw + _i * 8192), 16, 0, 0); } \
;         else { PG8_STAGE(bufoff, (kptr) + (half) * hstepA, voffA); } } while (0)
; #define PG8_LDA(dst, b, h) do { _Pragma("unroll") for (int m = 0; m < 4; ++m) _Pragma("unroll") for (int k = 0; k < 2; ++k) dst[m][k] = *(const LAS bf16x8*)(lds + PG8_SA(b, h) + aoff + m * 2048 + k * 1024); } while (0)
; #define PG8_LDB(dst, b, h) do { _Pragma("unroll") for (int n = 0; n < 2; ++n) _Pragma("unroll") for (int k = 0; k < 2; ++k) dst[n][k] = *(const LAS bf16x8*)(lds + PG8_SB(b, h) + boff + n * 2048 + k * 1024); } while (0)
; #define PG8_MMA(ai, bj, At, Bt) do { __builtin_amdgcn_s_setprio(1); _Pragma("unroll") for (int m = 0; m < 4; ++m) _Pragma("unroll") for (int n = 0; n < 2; ++n) _Pragma("unroll") for (int k = 0; k < 2; ++k) \
;         acc[ai][bj][m][n] = __builtin_amdgcn_mfma_f32_16x16x32_bf16(Bt[n][k], At[m][k], acc[ai][bj][m][n], 0, 0, 0); __builtin_amdgcn_s_setprio(0); } while (0)
; #define PG8_WAIT_V(n) asm volatile("s_waitcnt vmcnt(" #n ")" ::: "memory")
; #define PG8_WAIT_L(n) asm volatile("s_waitcnt lgkmcnt(" #n ")" ::: "memory")
; #define PG8_BAR __builtin_amdgcn_s_barrier()
; #define PG8_SCHED __builtin_amdgcn_sched_barrier(0)
;     ...
;             PG8_WAIT_V(8); PG8_WAIT_L(0); PG8_BAR; PG8_MMA(1, 0, At, B0); PG8_MMA(1, 1, At, B1); PG8_BAR; PG8_SCHED;
;             PG8_LDB(B0, 1, 0); PG8_LDB(B1, 1, 1); PG8_SCHED; PG8_LDA(At, 1, 0); PG8_STAGE_A(PG8_SA(0, 1), a2, 1, g2);
;             PG8_WAIT_V(8); PG8_WAIT_L(0); PG8_BAR; PG8_MMA(0, 0, At, B0); PG8_MMA(0, 1, At, B1); PG8_BAR; PG8_SCHED;
	s_setprio 1
	s_waitcnt lgkmcnt(0)
	v_mfma_f32_16x16x32_bf16 v[62:65], v[148:151], v[180:183], v[62:65]
	v_mfma_f32_16x16x32_bf16 v[58:61], v[156:159], v[180:183], v[58:61]
	v_mfma_f32_16x16x32_bf16 v[54:57], v[148:151], v[188:191], v[54:57]
	v_mfma_f32_16x16x32_bf16 v[50:53], v[156:159], v[188:191], v[50:53]
	v_mfma_f32_16x16x32_bf16 v[38:41], v[148:151], v[196:199], v[38:41]
	v_mfma_f32_16x16x32_bf16 v[34:37], v[156:159], v[196:199], v[34:37]
	v_mfma_f32_16x16x32_bf16 v[22:25], v[148:151], v[216:219], v[22:25]
	v_mfma_f32_16x16x32_bf16 v[18:21], v[156:159], v[216:219], v[18:21]
	v_mfma_f32_16x16x32_bf16 v[62:65], v[152:155], v[184:187], v[62:65]
	v_mfma_f32_16x16x32_bf16 v[58:61], v[160:163], v[184:187], v[58:61]
	v_mfma_f32_16x16x32_bf16 v[54:57], v[152:155], v[192:195], v[54:57]
	v_mfma_f32_16x16x32_bf16 v[50:53], v[160:163], v[192:195], v[50:53]
	v_mfma_f32_16x16x32_bf16 v[38:41], v[152:155], v[200:203], v[38:41]
	v_mfma_f32_16x16x32_bf16 v[34:37], v[160:163], v[200:203], v[34:37]
	v_mfma_f32_16x16x32_bf16 v[22:25], v[152:155], v[220:223], v[22:25]
	v_mfma_f32_16x16x32_bf16 v[18:21], v[160:163], v[220:223], v[18:21]
	s_setprio 0
	s_setprio 1
	v_mfma_f32_16x16x32_bf16 v[46:49], v[164:167], v[180:183], v[46:49]
	v_mfma_f32_16x16x32_bf16 v[42:45], v[172:175], v[180:183], v[42:45]
	v_mfma_f32_16x16x32_bf16 v[30:33], v[164:167], v[188:191], v[30:33]
	v_mfma_f32_16x16x32_bf16 v[26:29], v[172:175], v[188:191], v[26:29]
	v_mfma_f32_16x16x32_bf16 v[14:17], v[164:167], v[196:199], v[14:17]
	v_mfma_f32_16x16x32_bf16 v[10:13], v[172:175], v[196:199], v[10:13]
	v_mfma_f32_16x16x32_bf16 v[6:9], v[164:167], v[216:219], v[6:9]
	v_mfma_f32_16x16x32_bf16 v[2:5], v[172:175], v[216:219], v[2:5]
	v_mfma_f32_16x16x32_bf16 v[46:49], v[168:171], v[184:187], v[46:49]
	v_mfma_f32_16x16x32_bf16 v[42:45], v[176:179], v[184:187], v[42:45]
	v_mfma_f32_16x16x32_bf16 v[30:33], v[168:171], v[192:195], v[30:33]
	v_mfma_f32_16x16x32_bf16 v[26:29], v[176:179], v[192:195], v[26:29]
	v_mfma_f32_16x16x32_bf16 v[14:17], v[168:171], v[200:203], v[14:17]
	v_mfma_f32_16x16x32_bf16 v[10:13], v[176:179], v[200:203], v[10:13]
	v_mfma_f32_16x16x32_bf16 v[6:9], v[168:171], v[220:223], v[6:9]
	v_mfma_f32_16x16x32_bf16 v[2:5], v[176:179], v[220:223], v[2:5]
	s_setprio 0
	s_barrier
	s_add_i32 s18, 0, 0x18000
	s_add_i32 s19, 0, 0x1c000
	v_add_u32_e32 v160, s18, v143
	v_add_u32_e32 v176, s19, v143
	ds_read_b128 v[148:151], v160
	ds_read_b128 v[152:155], v160 offset:1024
	ds_read_b128 v[156:159], v160 offset:2048
	ds_read_b128 v[160:163], v160 offset:3072
	ds_read_b128 v[164:167], v176
	ds_read_b128 v[168:171], v176 offset:1024
	ds_read_b128 v[172:175], v176 offset:2048
	ds_read_b128 v[176:179], v176 offset:3072
	s_add_u32 s16, s30, 0x80000
	s_addc_u32 s17, s31, 0
	s_mov_b32 m0, s48
	v_lshl_add_u64 v[224:225], s[16:17], 0, v[130:131]
	ds_read_b128 v[180:183], v147 offset:32768
	ds_read_b128 v[184:187], v147 offset:33792
	ds_read_b128 v[188:191], v147 offset:34816
	ds_read_b128 v[192:195], v147 offset:35840
	ds_read_b128 v[196:199], v147 offset:36864
	ds_read_b128 v[200:203], v147 offset:37888
	ds_read_b128 v[216:219], v147 offset:38912
	ds_read_b128 v[220:223], v147 offset:39936
	global_load_lds_dwordx4 v[224:225], off
	v_lshl_add_u64 v[224:225], s[16:17], 0, v[134:135]
	s_mov_b32 m0, s49
	s_nop 0
	global_load_lds_dwordx4 v[224:225], off
	s_waitcnt vmcnt(8)
	s_waitcnt lgkmcnt(0)
	s_barrier
	s_setprio 1
	s_waitcnt lgkmcnt(0)
	v_mfma_f32_16x16x32_bf16 v[126:129], v[148:151], v[180:183], v[126:129]
	v_mfma_f32_16x16x32_bf16 v[122:125], v[156:159], v[180:183], v[122:125]
	v_mfma_f32_16x16x32_bf16 v[118:121], v[148:151], v[188:191], v[118:121]
	v_mfma_f32_16x16x32_bf16 v[114:117], v[156:159], v[188:191], v[114:117]
	v_mfma_f32_16x16x32_bf16 v[102:105], v[148:151], v[196:199], v[102:105]
	v_mfma_f32_16x16x32_bf16 v[98:101], v[156:159], v[196:199], v[98:101]
	v_mfma_f32_16x16x32_bf16 v[86:89], v[148:151], v[216:219], v[86:89]
	v_mfma_f32_16x16x32_bf16 v[82:85], v[156:159], v[216:219], v[82:85]
	v_mfma_f32_16x16x32_bf16 v[126:129], v[152:155], v[184:187], v[126:129]
	v_mfma_f32_16x16x32_bf16 v[122:125], v[160:163], v[184:187], v[122:125]
	v_mfma_f32_16x16x32_bf16 v[118:121], v[152:155], v[192:195], v[118:121]
	v_mfma_f32_16x16x32_bf16 v[114:117], v[160:163], v[192:195], v[114:117]
	v_mfma_f32_16x16x32_bf16 v[102:105], v[152:155], v[200:203], v[102:105]
	v_mfma_f32_16x16x32_bf16 v[98:101], v[160:163], v[200:203], v[98:101]
	v_mfma_f32_16x16x32_bf16 v[86:89], v[152:155], v[220:223], v[86:89]
	v_mfma_f32_16x16x32_bf16 v[82:85], v[160:163], v[220:223], v[82:85]
	s_setprio 0
	s_setprio 1
	v_mfma_f32_16x16x32_bf16 v[110:113], v[164:167], v[180:183], v[110:113]
	v_mfma_f32_16x16x32_bf16 v[106:109], v[172:175], v[180:183], v[106:109]
	v_mfma_f32_16x16x32_bf16 v[94:97], v[164:167], v[188:191], v[94:97]
	v_mfma_f32_16x16x32_bf16 v[90:93], v[172:175], v[188:191], v[90:93]
	v_mfma_f32_16x16x32_bf16 v[78:81], v[164:167], v[196:199], v[78:81]
	v_mfma_f32_16x16x32_bf16 v[74:77], v[172:175], v[196:199], v[74:77]
	v_mfma_f32_16x16x32_bf16 v[70:73], v[164:167], v[216:219], v[70:73]
	v_mfma_f32_16x16x32_bf16 v[66:69], v[172:175], v[216:219], v[66:69]
	v_mfma_f32_16x16x32_bf16 v[110:113], v[168:171], v[184:187], v[110:113]
	v_mfma_f32_16x16x32_bf16 v[106:109], v[176:179], v[184:187], v[106:109]
	v_mfma_f32_16x16x32_bf16 v[94:97], v[168:171], v[192:195], v[94:97]
	v_mfma_f32_16x16x32_bf16 v[90:93], v[176:179], v[192:195], v[90:93]
	v_mfma_f32_16x16x32_bf16 v[78:81], v[168:171], v[200:203], v[78:81]
	v_mfma_f32_16x16x32_bf16 v[74:77], v[176:179], v[200:203], v[74:77]
	v_mfma_f32_16x16x32_bf16 v[70:73], v[168:171], v[220:223], v[70:73]
	v_mfma_f32_16x16x32_bf16 v[66:69], v[176:179], v[220:223], v[66:69]
	s_setprio 0
	s_barrier
; #define PG8_STAGE(bufoff, gbase, voff) do { _Pragma("unroll") for (int _i = 0; _i < 2; ++_i) \
;         __builtin_amdgcn_global_load_lds((const unsigned*)((const char*)(gbase) + (voff)[_i]), (LAS unsigned*)(lds + (bufoff) + ldsw + _i * 8192), 16, 0, 0); } while (0)
; #define PG8_STAGE_A(bufoff, kptr, half, VO) do { if constexpr (GATHER) { _Pragma("unroll") for (int _i = 0; _i < 2; ++_i) \
;         __builtin_amdgcn_global_load_lds((const unsigned*)((const char*)(kptr) + (VO)[half][_i]), (LAS unsigned*)(lds + (bufoff) + ldsw + _i * 8192), 16, 0, 0); } \
;         else { PG8_STAGE(bufoff, (kptr) + (half) * hstepA, voffA); } } while (0)
; #define PG8_LDA(dst, b, h) do { _Pragma("unroll") for (int m = 0; m < 4; ++m) _Pragma("unroll") for (int k = 0; k < 2; ++k) dst[m][k] = *(const LAS bf16x8*)(lds + PG8_SA(b, h) + aoff + m * 2048 + k * 1024); } while (0)
; #define PG8_MMA(ai, bj, At, Bt) do { __builtin_amdgcn_s_setprio(1); _Pragma("unroll") for (int m = 0; m < 4; ++m) _Pragma("unroll") for (int n = 0; n < 2; ++n) _Pragma("unroll") for (int k = 0; k < 2; ++k) \
;         acc[ai][bj][m][n] = __builtin_amdgcn_mfma_f32_16x16x32_bf16(Bt[n][k], At[m][k], acc[ai][bj][m][n], 0, 0, 0); __builtin_amdgcn_s_setprio(0); } while (0)
; #define PG8_WAIT_V(n) asm volatile("s_waitcnt vmcnt(" #n ")" ::: "memory")
; #define PG8_WAIT_L(n) asm volatile("s_waitcnt lgkmcnt(" #n ")" ::: "memory")
; #define PG8_BAR __builtin_amdgcn_s_barrier()
; #define PG8_SCHED __builtin_amdgcn_sched_barrier(0)
;     ...
;         for (int t = 0; t < nt; t += 2) {
;     ...
;             PG8_LDA(At, 1, 1); PG8_STAGE(PG8_SB(1, 0), b3, voffB); PG8_STAGE(PG8_SB(1, 1), b3 + hstepB, voffB); PG8_STAGE_A(PG8_SA(1, 0), a3, 0, g2);
;             PG8_WAIT_V(8); PG8_WAIT_L(0); PG8_BAR; PG8_MMA(1, 0, At, B0); PG8_MMA(1, 1, At, B1); PG8_BAR; PG8_SCHED;
	s_add_i32 s16, s18, s26
	v_lshl_add_u64 v[204:205], v[204:205], 0, s[8:9]
	s_mov_b32 m0, s16
	ds_read_b128 v[180:183], v147 offset:49152
	ds_read_b128 v[184:187], v147 offset:50176
	ds_read_b128 v[188:191], v147 offset:51200
	ds_read_b128 v[192:195], v147 offset:52224
	ds_read_b128 v[196:199], v147 offset:53248
	ds_read_b128 v[200:203], v147 offset:54272
	ds_read_b128 v[216:219], v147 offset:55296
	ds_read_b128 v[220:223], v147 offset:56320
	global_load_lds_dwordx4 v[204:205], off
	s_add_i32 m0, s16, 0x2000
	s_add_u32 s0, s0, 0x80080
	v_lshl_add_u64 v[204:205], v[208:209], 0, s[8:9]
	s_addc_u32 s1, s1, 0
	s_add_i32 s16, s19, s26
	global_load_lds_dwordx4 v[204:205], off
	v_lshl_add_u64 v[204:205], s[0:1], 0, v[132:133]
	s_mov_b32 m0, s16
	s_nop 0
	global_load_lds_dwordx4 v[204:205], off
	v_lshl_add_u64 v[204:205], s[0:1], 0, v[136:137]
	s_add_i32 m0, s16, 0x2000
	s_nop 0
	global_load_lds_dwordx4 v[204:205], off
	v_lshl_add_u64 v[204:205], v[210:211], 0, s[8:9]
	s_mov_b32 m0, s50
	s_nop 0
	global_load_lds_dwordx4 v[204:205], off
	v_lshl_add_u64 v[204:205], v[212:213], 0, s[8:9]
	s_mov_b32 m0, s51
	s_nop 0
	global_load_lds_dwordx4 v[204:205], off
	s_waitcnt vmcnt(8)
	s_waitcnt lgkmcnt(0)
	s_barrier
	s_setprio 1
	s_waitcnt lgkmcnt(0)
	v_mfma_f32_16x16x32_bf16 v[62:65], v[148:151], v[180:183], v[62:65]
	v_mfma_f32_16x16x32_bf16 v[58:61], v[156:159], v[180:183], v[58:61]
	v_mfma_f32_16x16x32_bf16 v[54:57], v[148:151], v[188:191], v[54:57]
	v_mfma_f32_16x16x32_bf16 v[50:53], v[156:159], v[188:191], v[50:53]
	v_mfma_f32_16x16x32_bf16 v[38:41], v[148:151], v[196:199], v[38:41]
	v_mfma_f32_16x16x32_bf16 v[34:37], v[156:159], v[196:199], v[34:37]
	v_mfma_f32_16x16x32_bf16 v[22:25], v[148:151], v[216:219], v[22:25]
	v_mfma_f32_16x16x32_bf16 v[18:21], v[156:159], v[216:219], v[18:21]
	v_mfma_f32_16x16x32_bf16 v[62:65], v[152:155], v[184:187], v[62:65]
	v_mfma_f32_16x16x32_bf16 v[58:61], v[160:163], v[184:187], v[58:61]
	v_mfma_f32_16x16x32_bf16 v[54:57], v[152:155], v[192:195], v[54:57]
	v_mfma_f32_16x16x32_bf16 v[50:53], v[160:163], v[192:195], v[50:53]
	v_mfma_f32_16x16x32_bf16 v[38:41], v[152:155], v[200:203], v[38:41]
	v_mfma_f32_16x16x32_bf16 v[34:37], v[160:163], v[200:203], v[34:37]
	v_mfma_f32_16x16x32_bf16 v[22:25], v[152:155], v[220:223], v[22:25]
	v_mfma_f32_16x16x32_bf16 v[18:21], v[160:163], v[220:223], v[18:21]
	s_setprio 0
	s_setprio 1
	v_mfma_f32_16x16x32_bf16 v[46:49], v[164:167], v[180:183], v[46:49]
	v_mfma_f32_16x16x32_bf16 v[42:45], v[172:175], v[180:183], v[42:45]
	v_mfma_f32_16x16x32_bf16 v[30:33], v[164:167], v[188:191], v[30:33]
	v_mfma_f32_16x16x32_bf16 v[26:29], v[172:175], v[188:191], v[26:29]
	v_mfma_f32_16x16x32_bf16 v[14:17], v[164:167], v[196:199], v[14:17]
	v_mfma_f32_16x16x32_bf16 v[10:13], v[172:175], v[196:199], v[10:13]
	v_mfma_f32_16x16x32_bf16 v[6:9], v[164:167], v[216:219], v[6:9]
	v_mfma_f32_16x16x32_bf16 v[2:5], v[172:175], v[216:219], v[2:5]
	v_mfma_f32_16x16x32_bf16 v[46:49], v[168:171], v[184:187], v[46:49]
	v_mfma_f32_16x16x32_bf16 v[42:45], v[176:179], v[184:187], v[42:45]
	v_mfma_f32_16x16x32_bf16 v[30:33], v[168:171], v[192:195], v[30:33]
	v_mfma_f32_16x16x32_bf16 v[26:29], v[176:179], v[192:195], v[26:29]
	v_mfma_f32_16x16x32_bf16 v[14:17], v[168:171], v[200:203], v[14:17]
	v_mfma_f32_16x16x32_bf16 v[10:13], v[176:179], v[200:203], v[10:13]
	v_mfma_f32_16x16x32_bf16 v[6:9], v[168:171], v[220:223], v[6:9]
	v_mfma_f32_16x16x32_bf16 v[2:5], v[176:179], v[220:223], v[2:5]
	s_add_i32 s15, s15, 2
	s_add_u32 s24, s24, 0x100
	s_addc_u32 s25, s25, 0
	s_add_u32 s13, s13, 0x100
	s_addc_u32 s14, s14, 0
	s_cmp_gt_u32 s15, 29
	s_setprio 0
	s_barrier
	s_cbranch_scc0 .LBB0_402
	s_and_b64 vcc, exec, s[38:39]
	s_cbranch_vccz .LBB0_405
	s_barrier

; #define PG8_STAGE(bufoff, gbase, voff) do { _Pragma("unroll") for (int _i = 0; _i < 2; ++_i) \
;         __builtin_amdgcn_global_load_lds((const unsigned*)((const char*)(gbase) + (voff)[_i]), (LAS unsigned*)(lds + (bufoff) + ldsw + _i * 8192), 16, 0, 0); } while (0)
; #define PG8_STAGE_A(bufoff, kptr, half, VO) do { if constexpr (GATHER) { _Pragma("unroll") for (int _i = 0; _i < 2; ++_i) \
;         __builtin_amdgcn_global_load_lds((const unsigned*)((const char*)(kptr) + (VO)[half][_i]), (LAS unsigned*)(lds + (bufoff) + ldsw + _i * 8192), 16, 0, 0); } \
;         else { PG8_STAGE(bufoff, (kptr) + (half) * hstepA, voffA); } } while (0)
; #define PG8_LDA(dst, b, h) do { _Pragma("unroll") for (int m = 0; m < 4; ++m) _Pragma("unroll") for (int k = 0; k < 2; ++k) dst[m][k] = *(const LAS bf16x8*)(lds + PG8_SA(b, h) + aoff + m * 2048 + k * 1024); } while (0)
; #define PG8_LDB(dst, b, h) do { _Pragma("unroll") for (int n = 0; n < 2; ++n) _Pragma("unroll") for (int k = 0; k < 2; ++k) dst[n][k] = *(const LAS bf16x8*)(lds + PG8_SB(b, h) + boff + n * 2048 + k * 1024); } while (0)
; #define PG8_WAIT_V(n) asm volatile("s_waitcnt vmcnt(" #n ")" ::: "memory")
; #define PG8_WAIT_L(n) asm volatile("s_waitcnt lgkmcnt(" #n ")" ::: "memory")
;     ...
;         for (int t = 0; t < nt; t += 2) {
;             const bool last = (t == nt - 2);
;             const char* a1 = cA + (size_t)(t + 1) * kstep;
;             const char* a2 = last ? nA : cA + (size_t)(t + 2) * kstep; const char* b2 = last ? nB : cB + (size_t)(t + 2) * kstep;
;             const char* a3 = a2 + kstep; const char* b3 = b2 + kstep;
;             unsigned g2[2][2];
;             if constexpr (GATHER) {
; #pragma unroll
;                 for (int _h = 0; _h < 2; ++_h)
; #pragma unroll
;                     for (int _i = 0; _i < 2; ++_i) g2[_h][_i] = last ? gN[_h][_i] : gC[_h][_i]; }
;             if constexpr (SP2) {
;             PG8_LDB(B0, 0, 0); PG8_LDB(B1, 0, 1); PG8_SCHED; PG8_LDA(At, 0, 0); PG8_STAGE_A(PG8_SA(1, 1), a1, 1, gC);
;             PG8_WAIT_V(8); PG8_WAIT_L(0); PG8_BAR; PG8_MMA(0, 0, At, B0); PG8_MMA(0, 1, At, B1); PG8_BAR; PG8_SCHED;
;             PG8_LDA(At, 0, 1); PG8_STAGE(PG8_SB(0, 0), b2, voffB); PG8_STAGE(PG8_SB(0, 1), b2 + hstepB, voffB); PG8_STAGE_A(PG8_SA(0, 0), a2, 0, g2);
;             PG8_WAIT_V(8); PG8_WAIT_L(0); PG8_BAR; PG8_MMA(1, 0, At, B0); PG8_MMA(1, 1, At, B1); PG8_BAR; PG8_SCHED;
.LBB0_1318:
	s_add_u32 s0, s24, 0xfffe0080
	s_addc_u32 s1, s25, -1
	s_add_i32 s17, 0, 0x10000
	s_cmp_eq_u32 s16, 4
	s_cselect_b32 s31, s45, s1
	s_cselect_b32 s30, s44, s0
	v_add_u32_e32 v147, s17, v144
	s_cselect_b32 s1, s47, s15
	s_cselect_b32 s0, s46, s14
	s_add_i32 s20, 0, 0x14000
	ds_read_b128 v[148:151], v147
	ds_read_b128 v[152:155], v147 offset:1024
	ds_read_b128 v[156:159], v147 offset:2048
	ds_read_b128 v[160:163], v147 offset:3072
	v_add_u32_e32 v147, s20, v144
	ds_read_b128 v[164:167], v147
	ds_read_b128 v[168:171], v147 offset:1024
	ds_read_b128 v[172:175], v147 offset:2048
	ds_read_b128 v[176:179], v147 offset:3072
	v_lshl_add_u64 v[204:205], s[24:25], 0, v[140:141]
	s_add_i32 m0, s51, 0xc000
	ds_read_b128 v[180:183], v146
	ds_read_b128 v[184:187], v146 offset:1024
	ds_read_b128 v[188:191], v146 offset:2048
	ds_read_b128 v[192:195], v146 offset:3072
	ds_read_b128 v[196:199], v146 offset:4096
	ds_read_b128 v[200:203], v146 offset:5120
	ds_read_b128 v[216:219], v146 offset:6144
	ds_read_b128 v[220:223], v146 offset:7168
	global_load_lds_dwordx4 v[204:205], off
	v_lshl_add_u64 v[204:205], s[24:25], 0, v[142:143]
	s_add_i32 m0, s51, 0xe000
	s_nop 0
	global_load_lds_dwordx4 v[204:205], off
	s_waitcnt vmcnt(8)
	s_waitcnt lgkmcnt(0)
	s_barrier
	s_setprio 1
	s_waitcnt lgkmcnt(0)
	v_mfma_f32_16x16x32_bf16 v[126:129], v[148:151], v[180:183], v[126:129]
	v_mfma_f32_16x16x32_bf16 v[122:125], v[156:159], v[180:183], v[122:125]
	v_mfma_f32_16x16x32_bf16 v[110:113], v[148:151], v[188:191], v[110:113]
	v_mfma_f32_16x16x32_bf16 v[106:109], v[156:159], v[188:191], v[106:109]
	v_mfma_f32_16x16x32_bf16 v[94:97], v[148:151], v[196:199], v[94:97]
	v_mfma_f32_16x16x32_bf16 v[90:93], v[156:159], v[196:199], v[90:93]
	v_mfma_f32_16x16x32_bf16 v[78:81], v[148:151], v[216:219], v[78:81]
	v_mfma_f32_16x16x32_bf16 v[74:77], v[156:159], v[216:219], v[74:77]
	v_mfma_f32_16x16x32_bf16 v[126:129], v[152:155], v[184:187], v[126:129]
	v_mfma_f32_16x16x32_bf16 v[122:125], v[160:163], v[184:187], v[122:125]
	v_mfma_f32_16x16x32_bf16 v[110:113], v[152:155], v[192:195], v[110:113]
	v_mfma_f32_16x16x32_bf16 v[106:109], v[160:163], v[192:195], v[106:109]
	v_mfma_f32_16x16x32_bf16 v[94:97], v[152:155], v[200:203], v[94:97]
	v_mfma_f32_16x16x32_bf16 v[90:93], v[160:163], v[200:203], v[90:93]
	v_mfma_f32_16x16x32_bf16 v[78:81], v[152:155], v[220:223], v[78:81]
	v_mfma_f32_16x16x32_bf16 v[74:77], v[160:163], v[220:223], v[74:77]
	s_setprio 0
	s_setprio 1
	v_mfma_f32_16x16x32_bf16 v[118:121], v[164:167], v[180:183], v[118:121]
	v_mfma_f32_16x16x32_bf16 v[114:117], v[172:175], v[180:183], v[114:117]
	v_mfma_f32_16x16x32_bf16 v[102:105], v[164:167], v[188:191], v[102:105]
	v_mfma_f32_16x16x32_bf16 v[98:101], v[172:175], v[188:191], v[98:101]
	v_mfma_f32_16x16x32_bf16 v[86:89], v[164:167], v[196:199], v[86:89]
	v_mfma_f32_16x16x32_bf16 v[82:85], v[172:175], v[196:199], v[82:85]
	v_mfma_f32_16x16x32_bf16 v[70:73], v[164:167], v[216:219], v[70:73]
	v_mfma_f32_16x16x32_bf16 v[66:69], v[172:175], v[216:219], v[66:69]
	v_mfma_f32_16x16x32_bf16 v[118:121], v[168:171], v[184:187], v[118:121]
	v_mfma_f32_16x16x32_bf16 v[114:117], v[176:179], v[184:187], v[114:117]
	v_mfma_f32_16x16x32_bf16 v[102:105], v[168:171], v[192:195], v[102:105]
	v_mfma_f32_16x16x32_bf16 v[98:101], v[176:179], v[192:195], v[98:101]
	v_mfma_f32_16x16x32_bf16 v[86:89], v[168:171], v[200:203], v[86:89]
	v_mfma_f32_16x16x32_bf16 v[82:85], v[176:179], v[200:203], v[82:85]
	v_mfma_f32_16x16x32_bf16 v[70:73], v[168:171], v[220:223], v[70:73]
	v_mfma_f32_16x16x32_bf16 v[66:69], v[176:179], v[220:223], v[66:69]
	s_setprio 0
	s_barrier
	s_add_i32 s17, s17, s27
	v_lshl_add_u64 v[204:205], s[0:1], 0, v[132:133]
	s_mov_b32 m0, s17
	ds_read_b128 v[180:183], v146 offset:16384
	ds_read_b128 v[184:187], v146 offset:17408
	ds_read_b128 v[188:191], v146 offset:18432
	ds_read_b128 v[192:195], v146 offset:19456
	ds_read_b128 v[196:199], v146 offset:20480
	ds_read_b128 v[200:203], v146 offset:21504
	ds_read_b128 v[216:219], v146 offset:22528
	ds_read_b128 v[220:223], v146 offset:23552
	global_load_lds_dwordx4 v[204:205], off
	s_add_i32 m0, s17, 0x2000
	s_add_u32 s18, s0, 0x20000
	v_lshl_add_u64 v[208:209], s[0:1], 0, v[136:137]
	s_addc_u32 s19, s1, 0
	s_add_i32 s17, s20, s27
	global_load_lds_dwordx4 v[208:209], off
	v_lshl_add_u64 v[210:211], s[18:19], 0, v[132:133]
	s_mov_b32 m0, s17
	v_lshl_add_u64 v[212:213], s[30:31], 0, v[134:135]
	global_load_lds_dwordx4 v[210:211], off
	v_lshl_add_u64 v[210:211], s[18:19], 0, v[136:137]
	s_add_i32 m0, s17, 0x2000
	s_nop 0
	global_load_lds_dwordx4 v[210:211], off
	v_lshl_add_u64 v[210:211], s[30:31], 0, v[130:131]
	s_mov_b32 m0, s51
	s_nop 0
	global_load_lds_dwordx4 v[210:211], off
	s_mov_b32 m0, s54
	s_nop 0
	global_load_lds_dwordx4 v[212:213], off
	s_waitcnt vmcnt(8)
	s_waitcnt lgkmcnt(0)
	s_barrier
; #define PG8_STAGE_A(bufoff, kptr, half, VO) do { if constexpr (GATHER) { _Pragma("unroll") for (int _i = 0; _i < 2; ++_i) \
;         __builtin_amdgcn_global_load_lds((const unsigned*)((const char*)(kptr) + (VO)[half][_i]), (LAS unsigned*)(lds + (bufoff) + ldsw + _i * 8192), 16, 0, 0); } \
;         else { PG8_STAGE(bufoff, (kptr) + (half) * hstepA, voffA); } } while (0)
; #define PG8_LDA(dst, b, h) do { _Pragma("unroll") for (int m = 0; m < 4; ++m) _Pragma("unroll") for (int k = 0; k < 2; ++k) dst[m][k] = *(const LAS bf16x8*)(lds + PG8_SA(b, h) + aoff + m * 2048 + k * 1024); } while (0)
; #define PG8_LDB(dst, b, h) do { _Pragma("unroll") for (int n = 0; n < 2; ++n) _Pragma("unroll") for (int k = 0; k < 2; ++k) dst[n][k] = *(const LAS bf16x8*)(lds + PG8_SB(b, h) + boff + n * 2048 + k * 1024); } while (0)
; #define PG8_MMA(ai, bj, At, Bt) do { __builtin_amdgcn_s_setprio(1); _Pragma("unroll") for (int m = 0; m < 4; ++m) _Pragma("unroll") for (int n = 0; n < 2; ++n) _Pragma("unroll") for (int k = 0; k < 2; ++k) \
;         acc[ai][bj][m][n] = __builtin_amdgcn_mfma_f32_16x16x32_bf16(Bt[n][k], At[m][k], acc[ai][bj][m][n], 0, 0, 0); __builtin_amdgcn_s_setprio(0); } while (0)
; #define PG8_WAIT_V(n) asm volatile("s_waitcnt vmcnt(" #n ")" ::: "memory")
; #define PG8_WAIT_L(n) asm volatile("s_waitcnt lgkmcnt(" #n ")" ::: "memory")
; #define PG8_BAR __builtin_amdgcn_s_barrier()
; #define PG8_SCHED __builtin_amdgcn_sched_barrier(0)
;     ...
;             PG8_WAIT_V(8); PG8_WAIT_L(0); PG8_BAR; PG8_MMA(1, 0, At, B0); PG8_MMA(1, 1, At, B1); PG8_BAR; PG8_SCHED;
;             PG8_LDB(B0, 1, 0); PG8_LDB(B1, 1, 1); PG8_SCHED; PG8_LDA(At, 1, 0); PG8_STAGE_A(PG8_SA(0, 1), a2, 1, g2);
;             PG8_WAIT_V(8); PG8_WAIT_L(0); PG8_BAR; PG8_MMA(0, 0, At, B0); PG8_MMA(0, 1, At, B1); PG8_BAR; PG8_SCHED;
	s_setprio 1
	s_waitcnt lgkmcnt(0)
	v_mfma_f32_16x16x32_bf16 v[62:65], v[148:151], v[180:183], v[62:65]
	v_mfma_f32_16x16x32_bf16 v[58:61], v[156:159], v[180:183], v[58:61]
	v_mfma_f32_16x16x32_bf16 v[46:49], v[148:151], v[188:191], v[46:49]
	v_mfma_f32_16x16x32_bf16 v[42:45], v[156:159], v[188:191], v[42:45]
	v_mfma_f32_16x16x32_bf16 v[30:33], v[148:151], v[196:199], v[30:33]
	v_mfma_f32_16x16x32_bf16 v[26:29], v[156:159], v[196:199], v[26:29]
	v_mfma_f32_16x16x32_bf16 v[14:17], v[148:151], v[216:219], v[14:17]
	v_mfma_f32_16x16x32_bf16 v[10:13], v[156:159], v[216:219], v[10:13]
	v_mfma_f32_16x16x32_bf16 v[62:65], v[152:155], v[184:187], v[62:65]
	v_mfma_f32_16x16x32_bf16 v[58:61], v[160:163], v[184:187], v[58:61]
	v_mfma_f32_16x16x32_bf16 v[46:49], v[152:155], v[192:195], v[46:49]
	v_mfma_f32_16x16x32_bf16 v[42:45], v[160:163], v[192:195], v[42:45]
	v_mfma_f32_16x16x32_bf16 v[30:33], v[152:155], v[200:203], v[30:33]
	v_mfma_f32_16x16x32_bf16 v[26:29], v[160:163], v[200:203], v[26:29]
	v_mfma_f32_16x16x32_bf16 v[14:17], v[152:155], v[220:223], v[14:17]
	v_mfma_f32_16x16x32_bf16 v[10:13], v[160:163], v[220:223], v[10:13]
	s_setprio 0
	s_setprio 1
	v_mfma_f32_16x16x32_bf16 v[54:57], v[164:167], v[180:183], v[54:57]
	v_mfma_f32_16x16x32_bf16 v[50:53], v[172:175], v[180:183], v[50:53]
	v_mfma_f32_16x16x32_bf16 v[38:41], v[164:167], v[188:191], v[38:41]
	v_mfma_f32_16x16x32_bf16 v[34:37], v[172:175], v[188:191], v[34:37]
	v_mfma_f32_16x16x32_bf16 v[22:25], v[164:167], v[196:199], v[22:25]
	v_mfma_f32_16x16x32_bf16 v[18:21], v[172:175], v[196:199], v[18:21]
	v_mfma_f32_16x16x32_bf16 v[6:9], v[164:167], v[216:219], v[6:9]
	v_mfma_f32_16x16x32_bf16 v[2:5], v[172:175], v[216:219], v[2:5]
	v_mfma_f32_16x16x32_bf16 v[54:57], v[168:171], v[184:187], v[54:57]
	v_mfma_f32_16x16x32_bf16 v[50:53], v[176:179], v[184:187], v[50:53]
	v_mfma_f32_16x16x32_bf16 v[38:41], v[168:171], v[192:195], v[38:41]
	v_mfma_f32_16x16x32_bf16 v[34:37], v[176:179], v[192:195], v[34:37]
	v_mfma_f32_16x16x32_bf16 v[22:25], v[168:171], v[200:203], v[22:25]
	v_mfma_f32_16x16x32_bf16 v[18:21], v[176:179], v[200:203], v[18:21]
	v_mfma_f32_16x16x32_bf16 v[6:9], v[168:171], v[220:223], v[6:9]
	v_mfma_f32_16x16x32_bf16 v[2:5], v[176:179], v[220:223], v[2:5]
	s_setprio 0
	s_barrier
	s_add_i32 s17, 0, 0x18000
	v_add_u32_e32 v147, s17, v144
	s_add_i32 s20, 0, 0x1c000
	ds_read_b128 v[148:151], v147
	ds_read_b128 v[152:155], v147 offset:1024
	ds_read_b128 v[156:159], v147 offset:2048
	ds_read_b128 v[160:163], v147 offset:3072
	v_add_u32_e32 v147, s20, v144
	ds_read_b128 v[164:167], v147
	ds_read_b128 v[168:171], v147 offset:1024
	ds_read_b128 v[172:175], v147 offset:2048
	ds_read_b128 v[176:179], v147 offset:3072
	s_add_u32 s18, s30, 0x20000
	s_addc_u32 s19, s31, 0
	s_mov_b32 m0, s55
	v_lshl_add_u64 v[224:225], s[18:19], 0, v[130:131]
	ds_read_b128 v[180:183], v146 offset:32768
	ds_read_b128 v[184:187], v146 offset:33792
	ds_read_b128 v[188:191], v146 offset:34816
	ds_read_b128 v[192:195], v146 offset:35840
	ds_read_b128 v[196:199], v146 offset:36864
	ds_read_b128 v[200:203], v146 offset:37888
	ds_read_b128 v[216:219], v146 offset:38912
	ds_read_b128 v[220:223], v146 offset:39936
	global_load_lds_dwordx4 v[224:225], off
	v_lshl_add_u64 v[224:225], s[18:19], 0, v[134:135]
	s_mov_b32 m0, s56
	s_nop 0
	global_load_lds_dwordx4 v[224:225], off
	s_waitcnt vmcnt(8)
	s_waitcnt lgkmcnt(0)
	s_barrier
	s_setprio 1
	s_waitcnt lgkmcnt(0)
	v_mfma_f32_16x16x32_bf16 v[126:129], v[148:151], v[180:183], v[126:129]
	v_mfma_f32_16x16x32_bf16 v[122:125], v[156:159], v[180:183], v[122:125]
	v_mfma_f32_16x16x32_bf16 v[110:113], v[148:151], v[188:191], v[110:113]
	v_mfma_f32_16x16x32_bf16 v[106:109], v[156:159], v[188:191], v[106:109]
	v_mfma_f32_16x16x32_bf16 v[94:97], v[148:151], v[196:199], v[94:97]
	v_mfma_f32_16x16x32_bf16 v[90:93], v[156:159], v[196:199], v[90:93]
	v_mfma_f32_16x16x32_bf16 v[78:81], v[148:151], v[216:219], v[78:81]
	v_mfma_f32_16x16x32_bf16 v[74:77], v[156:159], v[216:219], v[74:77]
	v_mfma_f32_16x16x32_bf16 v[126:129], v[152:155], v[184:187], v[126:129]
	v_mfma_f32_16x16x32_bf16 v[122:125], v[160:163], v[184:187], v[122:125]
	v_mfma_f32_16x16x32_bf16 v[110:113], v[152:155], v[192:195], v[110:113]
	v_mfma_f32_16x16x32_bf16 v[106:109], v[160:163], v[192:195], v[106:109]
	v_mfma_f32_16x16x32_bf16 v[94:97], v[152:155], v[200:203], v[94:97]
	v_mfma_f32_16x16x32_bf16 v[90:93], v[160:163], v[200:203], v[90:93]
	v_mfma_f32_16x16x32_bf16 v[78:81], v[152:155], v[220:223], v[78:81]
	v_mfma_f32_16x16x32_bf16 v[74:77], v[160:163], v[220:223], v[74:77]
	s_setprio 0
	s_setprio 1
	v_mfma_f32_16x16x32_bf16 v[118:121], v[164:167], v[180:183], v[118:121]
	v_mfma_f32_16x16x32_bf16 v[114:117], v[172:175], v[180:183], v[114:117]
	v_mfma_f32_16x16x32_bf16 v[102:105], v[164:167], v[188:191], v[102:105]
	v_mfma_f32_16x16x32_bf16 v[98:101], v[172:175], v[188:191], v[98:101]
	v_mfma_f32_16x16x32_bf16 v[86:89], v[164:167], v[196:199], v[86:89]
	v_mfma_f32_16x16x32_bf16 v[82:85], v[172:175], v[196:199], v[82:85]
	v_mfma_f32_16x16x32_bf16 v[70:73], v[164:167], v[216:219], v[70:73]
	v_mfma_f32_16x16x32_bf16 v[66:69], v[172:175], v[216:219], v[66:69]
	v_mfma_f32_16x16x32_bf16 v[118:121], v[168:171], v[184:187], v[118:121]
	v_mfma_f32_16x16x32_bf16 v[114:117], v[176:179], v[184:187], v[114:117]
	v_mfma_f32_16x16x32_bf16 v[102:105], v[168:171], v[192:195], v[102:105]
	v_mfma_f32_16x16x32_bf16 v[98:101], v[176:179], v[192:195], v[98:101]
	v_mfma_f32_16x16x32_bf16 v[86:89], v[168:171], v[200:203], v[86:89]
	v_mfma_f32_16x16x32_bf16 v[82:85], v[176:179], v[200:203], v[82:85]
	v_mfma_f32_16x16x32_bf16 v[70:73], v[168:171], v[220:223], v[70:73]
	v_mfma_f32_16x16x32_bf16 v[66:69], v[176:179], v[220:223], v[66:69]
	s_setprio 0
	s_barrier
; #define PG8_STAGE(bufoff, gbase, voff) do { _Pragma("unroll") for (int _i = 0; _i < 2; ++_i) \
;         __builtin_amdgcn_global_load_lds((const unsigned*)((const char*)(gbase) + (voff)[_i]), (LAS unsigned*)(lds + (bufoff) + ldsw + _i * 8192), 16, 0, 0); } while (0)
; #define PG8_STAGE_A(bufoff, kptr, half, VO) do { if constexpr (GATHER) { _Pragma("unroll") for (int _i = 0; _i < 2; ++_i) \
;         __builtin_amdgcn_global_load_lds((const unsigned*)((const char*)(kptr) + (VO)[half][_i]), (LAS unsigned*)(lds + (bufoff) + ldsw + _i * 8192), 16, 0, 0); } \
;         else { PG8_STAGE(bufoff, (kptr) + (half) * hstepA, voffA); } } while (0)
; #define PG8_LDA(dst, b, h) do { _Pragma("unroll") for (int m = 0; m < 4; ++m) _Pragma("unroll") for (int k = 0; k < 2; ++k) dst[m][k] = *(const LAS bf16x8*)(lds + PG8_SA(b, h) + aoff + m * 2048 + k * 1024); } while (0)
; #define PG8_MMA(ai, bj, At, Bt) do { __builtin_amdgcn_s_setprio(1); _Pragma("unroll") for (int m = 0; m < 4; ++m) _Pragma("unroll") for (int n = 0; n < 2; ++n) _Pragma("unroll") for (int k = 0; k < 2; ++k) \
;         acc[ai][bj][m][n] = __builtin_amdgcn_mfma_f32_16x16x32_bf16(Bt[n][k], At[m][k], acc[ai][bj][m][n], 0, 0, 0); __builtin_amdgcn_s_setprio(0); } while (0)
; #define PG8_WAIT_V(n) asm volatile("s_waitcnt vmcnt(" #n ")" ::: "memory")
; #define PG8_WAIT_L(n) asm volatile("s_waitcnt lgkmcnt(" #n ")" ::: "memory")
; #define PG8_BAR __builtin_amdgcn_s_barrier()
; #define PG8_SCHED __builtin_amdgcn_sched_barrier(0)
;     ...
;         for (int t = 0; t < nt; t += 2) {
;     ...
;             PG8_LDA(At, 1, 1); PG8_STAGE(PG8_SB(1, 0), b3, voffB); PG8_STAGE(PG8_SB(1, 1), b3 + hstepB, voffB); PG8_STAGE_A(PG8_SA(1, 0), a3, 0, g2);
;             PG8_WAIT_V(8); PG8_WAIT_L(0); PG8_BAR; PG8_MMA(1, 0, At, B0); PG8_MMA(1, 1, At, B1); PG8_BAR; PG8_SCHED;
	s_add_i32 s17, s17, s27
	v_lshl_add_u64 v[204:205], v[204:205], 0, s[8:9]
	s_mov_b32 m0, s17
	ds_read_b128 v[180:183], v146 offset:49152
	ds_read_b128 v[184:187], v146 offset:50176
	ds_read_b128 v[188:191], v146 offset:51200
	ds_read_b128 v[192:195], v146 offset:52224
	ds_read_b128 v[196:199], v146 offset:53248
	ds_read_b128 v[200:203], v146 offset:54272
	ds_read_b128 v[216:219], v146 offset:55296
	ds_read_b128 v[220:223], v146 offset:56320
	global_load_lds_dwordx4 v[204:205], off
	s_add_i32 m0, s17, 0x2000
	s_add_u32 s0, s0, 0x20080
	v_lshl_add_u64 v[204:205], v[208:209], 0, s[8:9]
	s_addc_u32 s1, s1, 0
	s_add_i32 s17, s20, s27
	global_load_lds_dwordx4 v[204:205], off
	v_lshl_add_u64 v[204:205], s[0:1], 0, v[132:133]
	s_mov_b32 m0, s17
	s_nop 0
	global_load_lds_dwordx4 v[204:205], off
	v_lshl_add_u64 v[204:205], s[0:1], 0, v[136:137]
	s_add_i32 m0, s17, 0x2000
	s_nop 0
	global_load_lds_dwordx4 v[204:205], off
	v_lshl_add_u64 v[204:205], v[210:211], 0, s[8:9]
	s_mov_b32 m0, s57
	s_nop 0
	global_load_lds_dwordx4 v[204:205], off
	v_lshl_add_u64 v[204:205], v[212:213], 0, s[8:9]
	s_mov_b32 m0, s58
	s_nop 0
	global_load_lds_dwordx4 v[204:205], off
	s_waitcnt vmcnt(8)
	s_waitcnt lgkmcnt(0)
	s_barrier
	s_setprio 1
	s_waitcnt lgkmcnt(0)
	v_mfma_f32_16x16x32_bf16 v[62:65], v[148:151], v[180:183], v[62:65]
	v_mfma_f32_16x16x32_bf16 v[58:61], v[156:159], v[180:183], v[58:61]
	v_mfma_f32_16x16x32_bf16 v[46:49], v[148:151], v[188:191], v[46:49]
	v_mfma_f32_16x16x32_bf16 v[42:45], v[156:159], v[188:191], v[42:45]
	v_mfma_f32_16x16x32_bf16 v[30:33], v[148:151], v[196:199], v[30:33]
	v_mfma_f32_16x16x32_bf16 v[26:29], v[156:159], v[196:199], v[26:29]
	v_mfma_f32_16x16x32_bf16 v[14:17], v[148:151], v[216:219], v[14:17]
	v_mfma_f32_16x16x32_bf16 v[10:13], v[156:159], v[216:219], v[10:13]
	v_mfma_f32_16x16x32_bf16 v[62:65], v[152:155], v[184:187], v[62:65]
	v_mfma_f32_16x16x32_bf16 v[58:61], v[160:163], v[184:187], v[58:61]
	v_mfma_f32_16x16x32_bf16 v[46:49], v[152:155], v[192:195], v[46:49]
	v_mfma_f32_16x16x32_bf16 v[42:45], v[160:163], v[192:195], v[42:45]
	v_mfma_f32_16x16x32_bf16 v[30:33], v[152:155], v[200:203], v[30:33]
	v_mfma_f32_16x16x32_bf16 v[26:29], v[160:163], v[200:203], v[26:29]
	v_mfma_f32_16x16x32_bf16 v[14:17], v[152:155], v[220:223], v[14:17]
	v_mfma_f32_16x16x32_bf16 v[10:13], v[160:163], v[220:223], v[10:13]
	s_setprio 0
	s_setprio 1
	v_mfma_f32_16x16x32_bf16 v[54:57], v[164:167], v[180:183], v[54:57]
	v_mfma_f32_16x16x32_bf16 v[50:53], v[172:175], v[180:183], v[50:53]
	v_mfma_f32_16x16x32_bf16 v[38:41], v[164:167], v[188:191], v[38:41]
	v_mfma_f32_16x16x32_bf16 v[34:37], v[172:175], v[188:191], v[34:37]
	v_mfma_f32_16x16x32_bf16 v[22:25], v[164:167], v[196:199], v[22:25]
	v_mfma_f32_16x16x32_bf16 v[18:21], v[172:175], v[196:199], v[18:21]
	v_mfma_f32_16x16x32_bf16 v[6:9], v[164:167], v[216:219], v[6:9]
	v_mfma_f32_16x16x32_bf16 v[2:5], v[172:175], v[216:219], v[2:5]
	v_mfma_f32_16x16x32_bf16 v[54:57], v[168:171], v[184:187], v[54:57]
	v_mfma_f32_16x16x32_bf16 v[50:53], v[176:179], v[184:187], v[50:53]
	v_mfma_f32_16x16x32_bf16 v[38:41], v[168:171], v[192:195], v[38:41]
	v_mfma_f32_16x16x32_bf16 v[34:37], v[176:179], v[192:195], v[34:37]
	v_mfma_f32_16x16x32_bf16 v[22:25], v[168:171], v[200:203], v[22:25]
	v_mfma_f32_16x16x32_bf16 v[18:21], v[176:179], v[200:203], v[18:21]
	v_mfma_f32_16x16x32_bf16 v[6:9], v[168:171], v[220:223], v[6:9]
	v_mfma_f32_16x16x32_bf16 v[2:5], v[176:179], v[220:223], v[2:5]
	s_add_i32 s16, s16, 2
	s_add_u32 s24, s24, 0x100
	s_addc_u32 s25, s25, 0
	s_add_u32 s14, s14, 0x100
	s_addc_u32 s15, s15, 0
	s_cmp_gt_u32 s16, 5
	s_setprio 0
	s_barrier
	s_cbranch_scc0 .LBB0_1318
	s_and_b64 vcc, exec, s[38:39]
	s_cbranch_vccz .LBB0_1321
	s_barrier

; #define PG8_STAGE(bufoff, gbase, voff) do { _Pragma("unroll") for (int _i = 0; _i < 2; ++_i) \
;         __builtin_amdgcn_global_load_lds((const unsigned*)((const char*)(gbase) + (voff)[_i]), (LAS unsigned*)(lds + (bufoff) + ldsw + _i * 8192), 16, 0, 0); } while (0)
; #define PG8_STAGE_A(bufoff, kptr, half, VO) do { if constexpr (GATHER) { _Pragma("unroll") for (int _i = 0; _i < 2; ++_i) \
;         __builtin_amdgcn_global_load_lds((const unsigned*)((const char*)(kptr) + (VO)[half][_i]), (LAS unsigned*)(lds + (bufoff) + ldsw + _i * 8192), 16, 0, 0); } \
;         else { PG8_STAGE(bufoff, (kptr) + (half) * hstepA, voffA); } } while (0)
; #define PG8_LDA(dst, b, h) do { _Pragma("unroll") for (int m = 0; m < 4; ++m) _Pragma("unroll") for (int k = 0; k < 2; ++k) dst[m][k] = *(const LAS bf16x8*)(lds + PG8_SA(b, h) + aoff + m * 2048 + k * 1024); } while (0)
; #define PG8_LDB(dst, b, h) do { _Pragma("unroll") for (int n = 0; n < 2; ++n) _Pragma("unroll") for (int k = 0; k < 2; ++k) dst[n][k] = *(const LAS bf16x8*)(lds + PG8_SB(b, h) + boff + n * 2048 + k * 1024); } while (0)
; #define PG8_WAIT_V(n) asm volatile("s_waitcnt vmcnt(" #n ")" ::: "memory")
; #define PG8_WAIT_L(n) asm volatile("s_waitcnt lgkmcnt(" #n ")" ::: "memory")
;     ...
;         for (int t = 0; t < nt; t += 2) {
;             const bool last = (t == nt - 2);
;             const char* a1 = cA + (size_t)(t + 1) * kstep;
;             const char* a2 = last ? nA : cA + (size_t)(t + 2) * kstep; const char* b2 = last ? nB : cB + (size_t)(t + 2) * kstep;
;             const char* a3 = a2 + kstep; const char* b3 = b2 + kstep;
;             unsigned g2[2][2];
;             if constexpr (GATHER) {
; #pragma unroll
;                 for (int _h = 0; _h < 2; ++_h)
; #pragma unroll
;                     for (int _i = 0; _i < 2; ++_i) g2[_h][_i] = last ? gN[_h][_i] : gC[_h][_i]; }
;             if constexpr (SP2) {
;             PG8_LDB(B0, 0, 0); PG8_LDB(B1, 0, 1); PG8_SCHED; PG8_LDA(At, 0, 0); PG8_STAGE_A(PG8_SA(1, 1), a1, 1, gC);
;             PG8_WAIT_V(8); PG8_WAIT_L(0); PG8_BAR; PG8_MMA(0, 0, At, B0); PG8_MMA(0, 1, At, B1); PG8_BAR; PG8_SCHED;
;             PG8_LDA(At, 0, 1); PG8_STAGE(PG8_SB(0, 0), b2, voffB); PG8_STAGE(PG8_SB(0, 1), b2 + hstepB, voffB); PG8_STAGE_A(PG8_SA(0, 0), a2, 0, g2);
;             PG8_WAIT_V(8); PG8_WAIT_L(0); PG8_BAR; PG8_MMA(1, 0, At, B0); PG8_MMA(1, 1, At, B1); PG8_BAR; PG8_SCHED;
.LBB0_1443:
	s_add_u32 s0, s24, 0xfffe0080
	s_addc_u32 s1, s25, -1
	s_add_i32 s15, 0, 0x10000
	s_cmp_eq_u32 s14, 4
	s_cselect_b32 s31, s49, s1
	s_cselect_b32 s30, s48, s0
	s_cselect_b32 s1, s51, s13
	s_cselect_b32 s0, s50, s12
	s_add_i32 s18, 0, 0x14000
	v_add_u32_e32 v62, s15, v199
	v_add_u32_e32 v150, s18, v199
	ds_read_b128 v[38:41], v62
	ds_read_b128 v[46:49], v62 offset:1024
	ds_read_b128 v[54:57], v62 offset:2048
	ds_read_b128 v[62:65], v62 offset:3072
	ds_read_b128 v[122:125], v150
	ds_read_b128 v[130:133], v150 offset:1024
	ds_read_b128 v[142:145], v150 offset:2048
	ds_read_b128 v[150:153], v150 offset:3072
	v_lshl_add_u64 v[196:197], s[24:25], 0, v[180:181]
	s_add_i32 m0, s55, 0xc000
	ds_read_b128 v[154:157], v201
	ds_read_b128 v[158:161], v201 offset:1024
	ds_read_b128 v[166:169], v201 offset:2048
	ds_read_b128 v[184:187], v201 offset:3072
	ds_read_b128 v[188:191], v201 offset:4096
	ds_read_b128 v[192:195], v201 offset:5120
	ds_read_b128 v[202:205], v201 offset:6144
	ds_read_b128 v[216:219], v201 offset:7168
	global_load_lds_dwordx4 v[196:197], off
	v_lshl_add_u64 v[196:197], s[24:25], 0, v[182:183]
	s_add_i32 m0, s55, 0xe000
	s_nop 0
	global_load_lds_dwordx4 v[196:197], off
	s_waitcnt vmcnt(8)
	s_waitcnt lgkmcnt(0)
	s_barrier
	s_setprio 1
	s_waitcnt lgkmcnt(0)
	v_mfma_f32_16x16x32_bf16 v[170:173], v[38:41], v[154:157], v[170:173]
	v_mfma_f32_16x16x32_bf16 v[162:165], v[54:57], v[154:157], v[162:165]
	v_mfma_f32_16x16x32_bf16 v[134:137], v[38:41], v[166:169], v[134:137]
	v_mfma_f32_16x16x32_bf16 v[126:129], v[54:57], v[166:169], v[126:129]
	v_mfma_f32_16x16x32_bf16 v[110:113], v[38:41], v[188:191], v[110:113]
	v_mfma_f32_16x16x32_bf16 v[106:109], v[54:57], v[188:191], v[106:109]
	v_mfma_f32_16x16x32_bf16 v[94:97], v[38:41], v[202:205], v[94:97]
	v_mfma_f32_16x16x32_bf16 v[90:93], v[54:57], v[202:205], v[90:93]
	v_mfma_f32_16x16x32_bf16 v[170:173], v[46:49], v[158:161], v[170:173]
	v_mfma_f32_16x16x32_bf16 v[162:165], v[62:65], v[158:161], v[162:165]
	v_mfma_f32_16x16x32_bf16 v[134:137], v[46:49], v[184:187], v[134:137]
	v_mfma_f32_16x16x32_bf16 v[126:129], v[62:65], v[184:187], v[126:129]
	v_mfma_f32_16x16x32_bf16 v[110:113], v[46:49], v[192:195], v[110:113]
	v_mfma_f32_16x16x32_bf16 v[106:109], v[62:65], v[192:195], v[106:109]
	v_mfma_f32_16x16x32_bf16 v[94:97], v[46:49], v[216:219], v[94:97]
	v_mfma_f32_16x16x32_bf16 v[90:93], v[62:65], v[216:219], v[90:93]
	s_setprio 0
	s_setprio 1
	v_mfma_f32_16x16x32_bf16 v[146:149], v[122:125], v[154:157], v[146:149]
	v_mfma_f32_16x16x32_bf16 v[138:141], v[142:145], v[154:157], v[138:141]
	v_mfma_f32_16x16x32_bf16 v[118:121], v[122:125], v[166:169], v[118:121]
	v_mfma_f32_16x16x32_bf16 v[114:117], v[142:145], v[166:169], v[114:117]
	v_mfma_f32_16x16x32_bf16 v[102:105], v[122:125], v[188:191], v[102:105]
	v_mfma_f32_16x16x32_bf16 v[98:101], v[142:145], v[188:191], v[98:101]
	v_mfma_f32_16x16x32_bf16 v[86:89], v[122:125], v[202:205], v[86:89]
	v_mfma_f32_16x16x32_bf16 v[82:85], v[142:145], v[202:205], v[82:85]
	v_mfma_f32_16x16x32_bf16 v[146:149], v[130:133], v[158:161], v[146:149]
	v_mfma_f32_16x16x32_bf16 v[138:141], v[150:153], v[158:161], v[138:141]
	v_mfma_f32_16x16x32_bf16 v[118:121], v[130:133], v[184:187], v[118:121]
	v_mfma_f32_16x16x32_bf16 v[114:117], v[150:153], v[184:187], v[114:117]
	v_mfma_f32_16x16x32_bf16 v[102:105], v[130:133], v[192:195], v[102:105]
	v_mfma_f32_16x16x32_bf16 v[98:101], v[150:153], v[192:195], v[98:101]
	v_mfma_f32_16x16x32_bf16 v[86:89], v[130:133], v[216:219], v[86:89]
	v_mfma_f32_16x16x32_bf16 v[82:85], v[150:153], v[216:219], v[82:85]
	s_setprio 0
	s_barrier
	s_add_i32 s15, s15, s57
	v_lshl_add_u64 v[196:197], s[0:1], 0, v[206:207]
	s_mov_b32 m0, s15
	ds_read_b128 v[154:157], v201 offset:16384
	ds_read_b128 v[158:161], v201 offset:17408
	ds_read_b128 v[166:169], v201 offset:18432
	ds_read_b128 v[184:187], v201 offset:19456
	ds_read_b128 v[188:191], v201 offset:20480
	ds_read_b128 v[192:195], v201 offset:21504
	ds_read_b128 v[202:205], v201 offset:22528
	ds_read_b128 v[216:219], v201 offset:23552
	global_load_lds_dwordx4 v[196:197], off
	s_add_i32 m0, s15, 0x2000
	s_add_u32 s16, s0, 0x20000
	v_lshl_add_u64 v[208:209], s[0:1], 0, v[174:175]
	s_addc_u32 s17, s1, 0
	s_add_i32 s15, s18, s57
	global_load_lds_dwordx4 v[208:209], off
	v_lshl_add_u64 v[210:211], s[16:17], 0, v[206:207]
	s_mov_b32 m0, s15
	v_lshl_add_u64 v[212:213], s[30:31], 0, v[176:177]
	global_load_lds_dwordx4 v[210:211], off
	v_lshl_add_u64 v[210:211], s[16:17], 0, v[174:175]
	s_add_i32 m0, s15, 0x2000
	s_nop 0
	global_load_lds_dwordx4 v[210:211], off
	v_lshl_add_u64 v[210:211], s[30:31], 0, v[178:179]
	s_mov_b32 m0, s55
	s_nop 0
	global_load_lds_dwordx4 v[210:211], off
	s_mov_b32 m0, s63
	s_nop 0
	global_load_lds_dwordx4 v[212:213], off
	s_waitcnt vmcnt(8)
	s_waitcnt lgkmcnt(0)
	s_barrier
; #define PG8_STAGE_A(bufoff, kptr, half, VO) do { if constexpr (GATHER) { _Pragma("unroll") for (int _i = 0; _i < 2; ++_i) \
;         __builtin_amdgcn_global_load_lds((const unsigned*)((const char*)(kptr) + (VO)[half][_i]), (LAS unsigned*)(lds + (bufoff) + ldsw + _i * 8192), 16, 0, 0); } \
;         else { PG8_STAGE(bufoff, (kptr) + (half) * hstepA, voffA); } } while (0)
; #define PG8_LDA(dst, b, h) do { _Pragma("unroll") for (int m = 0; m < 4; ++m) _Pragma("unroll") for (int k = 0; k < 2; ++k) dst[m][k] = *(const LAS bf16x8*)(lds + PG8_SA(b, h) + aoff + m * 2048 + k * 1024); } while (0)
; #define PG8_LDB(dst, b, h) do { _Pragma("unroll") for (int n = 0; n < 2; ++n) _Pragma("unroll") for (int k = 0; k < 2; ++k) dst[n][k] = *(const LAS bf16x8*)(lds + PG8_SB(b, h) + boff + n * 2048 + k * 1024); } while (0)
; #define PG8_MMA(ai, bj, At, Bt) do { __builtin_amdgcn_s_setprio(1); _Pragma("unroll") for (int m = 0; m < 4; ++m) _Pragma("unroll") for (int n = 0; n < 2; ++n) _Pragma("unroll") for (int k = 0; k < 2; ++k) \
;         acc[ai][bj][m][n] = __builtin_amdgcn_mfma_f32_16x16x32_bf16(Bt[n][k], At[m][k], acc[ai][bj][m][n], 0, 0, 0); __builtin_amdgcn_s_setprio(0); } while (0)
; #define PG8_WAIT_V(n) asm volatile("s_waitcnt vmcnt(" #n ")" ::: "memory")
; #define PG8_WAIT_L(n) asm volatile("s_waitcnt lgkmcnt(" #n ")" ::: "memory")
; #define PG8_BAR __builtin_amdgcn_s_barrier()
; #define PG8_SCHED __builtin_amdgcn_sched_barrier(0)
;     ...
;             PG8_WAIT_V(8); PG8_WAIT_L(0); PG8_BAR; PG8_MMA(1, 0, At, B0); PG8_MMA(1, 1, At, B1); PG8_BAR; PG8_SCHED;
;             PG8_LDB(B0, 1, 0); PG8_LDB(B1, 1, 1); PG8_SCHED; PG8_LDA(At, 1, 0); PG8_STAGE_A(PG8_SA(0, 1), a2, 1, g2);
;             PG8_WAIT_V(8); PG8_WAIT_L(0); PG8_BAR; PG8_MMA(0, 0, At, B0); PG8_MMA(0, 1, At, B1); PG8_BAR; PG8_SCHED;
	s_setprio 1
	s_waitcnt lgkmcnt(0)
	v_mfma_f32_16x16x32_bf16 v[78:81], v[38:41], v[154:157], v[78:81]
	v_mfma_f32_16x16x32_bf16 v[74:77], v[54:57], v[154:157], v[74:77]
	v_mfma_f32_16x16x32_bf16 v[58:61], v[38:41], v[166:169], v[58:61]
	v_mfma_f32_16x16x32_bf16 v[50:53], v[54:57], v[166:169], v[50:53]
	v_mfma_f32_16x16x32_bf16 v[30:33], v[38:41], v[188:191], v[30:33]
	v_mfma_f32_16x16x32_bf16 v[26:29], v[54:57], v[188:191], v[26:29]
	v_mfma_f32_16x16x32_bf16 v[14:17], v[38:41], v[202:205], v[14:17]
	v_mfma_f32_16x16x32_bf16 v[10:13], v[54:57], v[202:205], v[10:13]
	v_mfma_f32_16x16x32_bf16 v[78:81], v[46:49], v[158:161], v[78:81]
	v_mfma_f32_16x16x32_bf16 v[74:77], v[62:65], v[158:161], v[74:77]
	v_mfma_f32_16x16x32_bf16 v[58:61], v[46:49], v[184:187], v[58:61]
	v_mfma_f32_16x16x32_bf16 v[50:53], v[62:65], v[184:187], v[50:53]
	v_mfma_f32_16x16x32_bf16 v[30:33], v[46:49], v[192:195], v[30:33]
	v_mfma_f32_16x16x32_bf16 v[26:29], v[62:65], v[192:195], v[26:29]
	v_mfma_f32_16x16x32_bf16 v[14:17], v[46:49], v[216:219], v[14:17]
	v_mfma_f32_16x16x32_bf16 v[10:13], v[62:65], v[216:219], v[10:13]
	s_setprio 0
	s_setprio 1
	v_mfma_f32_16x16x32_bf16 v[42:45], v[122:125], v[166:169], v[42:45]
	v_mfma_f32_16x16x32_bf16 v[34:37], v[142:145], v[166:169], v[34:37]
	v_mfma_f32_16x16x32_bf16 v[22:25], v[122:125], v[188:191], v[22:25]
	v_mfma_f32_16x16x32_bf16 v[18:21], v[142:145], v[188:191], v[18:21]
	v_mfma_f32_16x16x32_bf16 v[6:9], v[122:125], v[202:205], v[6:9]
	v_mfma_f32_16x16x32_bf16 v[2:5], v[142:145], v[202:205], v[2:5]
	v_mfma_f32_16x16x32_bf16 v[38:41], v[122:125], v[154:157], v[70:73]
	v_mfma_f32_16x16x32_bf16 v[46:49], v[142:145], v[154:157], v[66:69]
	v_mfma_f32_16x16x32_bf16 v[42:45], v[130:133], v[184:187], v[42:45]
	v_mfma_f32_16x16x32_bf16 v[34:37], v[150:153], v[184:187], v[34:37]
	v_mfma_f32_16x16x32_bf16 v[22:25], v[130:133], v[192:195], v[22:25]
	v_mfma_f32_16x16x32_bf16 v[18:21], v[150:153], v[192:195], v[18:21]
	v_mfma_f32_16x16x32_bf16 v[6:9], v[130:133], v[216:219], v[6:9]
	v_mfma_f32_16x16x32_bf16 v[2:5], v[150:153], v[216:219], v[2:5]
	v_mfma_f32_16x16x32_bf16 v[38:41], v[130:133], v[158:161], v[38:41]
	v_mfma_f32_16x16x32_bf16 v[46:49], v[150:153], v[158:161], v[46:49]
	s_setprio 0
	s_barrier
	s_add_i32 s15, 0, 0x18000
	s_add_i32 s18, 0, 0x1c000
	v_add_u32_e32 v70, s15, v199
	v_add_u32_e32 v150, s18, v199
	ds_read_b128 v[54:57], v70
	ds_read_b128 v[62:65], v70 offset:1024
	ds_read_b128 v[66:69], v70 offset:2048
	ds_read_b128 v[70:73], v70 offset:3072
	ds_read_b128 v[122:125], v150
	ds_read_b128 v[130:133], v150 offset:1024
	ds_read_b128 v[142:145], v150 offset:2048
	ds_read_b128 v[150:153], v150 offset:3072
	s_add_u32 s16, s30, 0x20000
	s_addc_u32 s17, s31, 0
	s_mov_b32 m0, s64
	v_lshl_add_u64 v[220:221], s[16:17], 0, v[178:179]
	ds_read_b128 v[154:157], v201 offset:32768
	ds_read_b128 v[158:161], v201 offset:33792
	ds_read_b128 v[166:169], v201 offset:34816
	ds_read_b128 v[184:187], v201 offset:35840
	ds_read_b128 v[188:191], v201 offset:36864
	ds_read_b128 v[192:195], v201 offset:37888
	ds_read_b128 v[202:205], v201 offset:38912
	ds_read_b128 v[216:219], v201 offset:39936
	global_load_lds_dwordx4 v[220:221], off
	v_lshl_add_u64 v[220:221], s[16:17], 0, v[176:177]
	s_mov_b32 m0, s65
	s_nop 0
	global_load_lds_dwordx4 v[220:221], off
	s_waitcnt vmcnt(8)
	s_waitcnt lgkmcnt(0)
	s_barrier
	s_setprio 1
	s_waitcnt lgkmcnt(0)
	v_mfma_f32_16x16x32_bf16 v[170:173], v[54:57], v[154:157], v[170:173]
	v_mfma_f32_16x16x32_bf16 v[162:165], v[66:69], v[154:157], v[162:165]
	v_mfma_f32_16x16x32_bf16 v[134:137], v[54:57], v[166:169], v[134:137]
	v_mfma_f32_16x16x32_bf16 v[126:129], v[66:69], v[166:169], v[126:129]
	v_mfma_f32_16x16x32_bf16 v[110:113], v[54:57], v[188:191], v[110:113]
	v_mfma_f32_16x16x32_bf16 v[106:109], v[66:69], v[188:191], v[106:109]
	v_mfma_f32_16x16x32_bf16 v[94:97], v[54:57], v[202:205], v[94:97]
	v_mfma_f32_16x16x32_bf16 v[90:93], v[66:69], v[202:205], v[90:93]
	v_mfma_f32_16x16x32_bf16 v[170:173], v[62:65], v[158:161], v[170:173]
	v_mfma_f32_16x16x32_bf16 v[162:165], v[70:73], v[158:161], v[162:165]
	v_mfma_f32_16x16x32_bf16 v[134:137], v[62:65], v[184:187], v[134:137]
	v_mfma_f32_16x16x32_bf16 v[126:129], v[70:73], v[184:187], v[126:129]
	v_mfma_f32_16x16x32_bf16 v[110:113], v[62:65], v[192:195], v[110:113]
	v_mfma_f32_16x16x32_bf16 v[106:109], v[70:73], v[192:195], v[106:109]
	v_mfma_f32_16x16x32_bf16 v[94:97], v[62:65], v[216:219], v[94:97]
	v_mfma_f32_16x16x32_bf16 v[90:93], v[70:73], v[216:219], v[90:93]
	s_setprio 0
	s_setprio 1
	v_mfma_f32_16x16x32_bf16 v[146:149], v[122:125], v[154:157], v[146:149]
	v_mfma_f32_16x16x32_bf16 v[138:141], v[142:145], v[154:157], v[138:141]
	v_mfma_f32_16x16x32_bf16 v[118:121], v[122:125], v[166:169], v[118:121]
	v_mfma_f32_16x16x32_bf16 v[114:117], v[142:145], v[166:169], v[114:117]
	v_mfma_f32_16x16x32_bf16 v[102:105], v[122:125], v[188:191], v[102:105]
	v_mfma_f32_16x16x32_bf16 v[98:101], v[142:145], v[188:191], v[98:101]
	v_mfma_f32_16x16x32_bf16 v[86:89], v[122:125], v[202:205], v[86:89]
	v_mfma_f32_16x16x32_bf16 v[82:85], v[142:145], v[202:205], v[82:85]
	v_mfma_f32_16x16x32_bf16 v[146:149], v[130:133], v[158:161], v[146:149]
	v_mfma_f32_16x16x32_bf16 v[138:141], v[150:153], v[158:161], v[138:141]
	v_mfma_f32_16x16x32_bf16 v[118:121], v[130:133], v[184:187], v[118:121]
	v_mfma_f32_16x16x32_bf16 v[114:117], v[150:153], v[184:187], v[114:117]
	v_mfma_f32_16x16x32_bf16 v[102:105], v[130:133], v[192:195], v[102:105]
	v_mfma_f32_16x16x32_bf16 v[98:101], v[150:153], v[192:195], v[98:101]
	v_mfma_f32_16x16x32_bf16 v[86:89], v[130:133], v[216:219], v[86:89]
	v_mfma_f32_16x16x32_bf16 v[82:85], v[150:153], v[216:219], v[82:85]
	s_setprio 0
	s_barrier
; #define PG8_STAGE(bufoff, gbase, voff) do { _Pragma("unroll") for (int _i = 0; _i < 2; ++_i) \
;         __builtin_amdgcn_global_load_lds((const unsigned*)((const char*)(gbase) + (voff)[_i]), (LAS unsigned*)(lds + (bufoff) + ldsw + _i * 8192), 16, 0, 0); } while (0)
; #define PG8_STAGE_A(bufoff, kptr, half, VO) do { if constexpr (GATHER) { _Pragma("unroll") for (int _i = 0; _i < 2; ++_i) \
;         __builtin_amdgcn_global_load_lds((const unsigned*)((const char*)(kptr) + (VO)[half][_i]), (LAS unsigned*)(lds + (bufoff) + ldsw + _i * 8192), 16, 0, 0); } \
;         else { PG8_STAGE(bufoff, (kptr) + (half) * hstepA, voffA); } } while (0)
; #define PG8_LDA(dst, b, h) do { _Pragma("unroll") for (int m = 0; m < 4; ++m) _Pragma("unroll") for (int k = 0; k < 2; ++k) dst[m][k] = *(const LAS bf16x8*)(lds + PG8_SA(b, h) + aoff + m * 2048 + k * 1024); } while (0)
; #define PG8_MMA(ai, bj, At, Bt) do { __builtin_amdgcn_s_setprio(1); _Pragma("unroll") for (int m = 0; m < 4; ++m) _Pragma("unroll") for (int n = 0; n < 2; ++n) _Pragma("unroll") for (int k = 0; k < 2; ++k) \
;         acc[ai][bj][m][n] = __builtin_amdgcn_mfma_f32_16x16x32_bf16(Bt[n][k], At[m][k], acc[ai][bj][m][n], 0, 0, 0); __builtin_amdgcn_s_setprio(0); } while (0)
; #define PG8_WAIT_V(n) asm volatile("s_waitcnt vmcnt(" #n ")" ::: "memory")
; #define PG8_WAIT_L(n) asm volatile("s_waitcnt lgkmcnt(" #n ")" ::: "memory")
; #define PG8_BAR __builtin_amdgcn_s_barrier()
; #define PG8_SCHED __builtin_amdgcn_sched_barrier(0)
;     ...
;         for (int t = 0; t < nt; t += 2) {
;     ...
;             PG8_LDA(At, 1, 1); PG8_STAGE(PG8_SB(1, 0), b3, voffB); PG8_STAGE(PG8_SB(1, 1), b3 + hstepB, voffB); PG8_STAGE_A(PG8_SA(1, 0), a3, 0, g2);
;             PG8_WAIT_V(8); PG8_WAIT_L(0); PG8_BAR; PG8_MMA(1, 0, At, B0); PG8_MMA(1, 1, At, B1); PG8_BAR; PG8_SCHED;
	s_add_i32 s15, s15, s57
	v_lshl_add_u64 v[196:197], v[196:197], 0, s[8:9]
	s_mov_b32 m0, s15
	ds_read_b128 v[154:157], v201 offset:49152
	ds_read_b128 v[158:161], v201 offset:50176
	ds_read_b128 v[166:169], v201 offset:51200
	ds_read_b128 v[184:187], v201 offset:52224
	ds_read_b128 v[188:191], v201 offset:53248
	ds_read_b128 v[192:195], v201 offset:54272
	ds_read_b128 v[202:205], v201 offset:55296
	ds_read_b128 v[216:219], v201 offset:56320
	global_load_lds_dwordx4 v[196:197], off
	s_add_i32 m0, s15, 0x2000
	s_add_u32 s0, s0, 0x20080
	v_lshl_add_u64 v[196:197], v[208:209], 0, s[8:9]
	s_addc_u32 s1, s1, 0
	s_add_i32 s15, s18, s57
	global_load_lds_dwordx4 v[196:197], off
	v_lshl_add_u64 v[196:197], s[0:1], 0, v[206:207]
	s_mov_b32 m0, s15
	s_nop 0
	global_load_lds_dwordx4 v[196:197], off
	v_lshl_add_u64 v[196:197], s[0:1], 0, v[174:175]
	s_add_i32 m0, s15, 0x2000
	s_nop 0
	global_load_lds_dwordx4 v[196:197], off
	v_lshl_add_u64 v[196:197], v[210:211], 0, s[8:9]
	s_mov_b32 m0, s4
	s_nop 0
	global_load_lds_dwordx4 v[196:197], off
	v_lshl_add_u64 v[196:197], v[212:213], 0, s[8:9]
	s_mov_b32 m0, s66
	s_nop 0
	global_load_lds_dwordx4 v[196:197], off
	s_waitcnt vmcnt(8)
	s_waitcnt lgkmcnt(0)
	s_barrier
	s_setprio 1
	s_waitcnt lgkmcnt(0)
	v_mfma_f32_16x16x32_bf16 v[78:81], v[54:57], v[154:157], v[78:81]
	v_mfma_f32_16x16x32_bf16 v[74:77], v[66:69], v[154:157], v[74:77]
	v_mfma_f32_16x16x32_bf16 v[58:61], v[54:57], v[166:169], v[58:61]
	v_mfma_f32_16x16x32_bf16 v[50:53], v[66:69], v[166:169], v[50:53]
	v_mfma_f32_16x16x32_bf16 v[30:33], v[54:57], v[188:191], v[30:33]
	v_mfma_f32_16x16x32_bf16 v[26:29], v[66:69], v[188:191], v[26:29]
	v_mfma_f32_16x16x32_bf16 v[14:17], v[54:57], v[202:205], v[14:17]
	v_mfma_f32_16x16x32_bf16 v[10:13], v[66:69], v[202:205], v[10:13]
	v_mfma_f32_16x16x32_bf16 v[78:81], v[62:65], v[158:161], v[78:81]
	v_mfma_f32_16x16x32_bf16 v[74:77], v[70:73], v[158:161], v[74:77]
	v_mfma_f32_16x16x32_bf16 v[58:61], v[62:65], v[184:187], v[58:61]
	v_mfma_f32_16x16x32_bf16 v[50:53], v[70:73], v[184:187], v[50:53]
	v_mfma_f32_16x16x32_bf16 v[30:33], v[62:65], v[192:195], v[30:33]
	v_mfma_f32_16x16x32_bf16 v[26:29], v[70:73], v[192:195], v[26:29]
	v_mfma_f32_16x16x32_bf16 v[14:17], v[62:65], v[216:219], v[14:17]
	v_mfma_f32_16x16x32_bf16 v[10:13], v[70:73], v[216:219], v[10:13]
	s_setprio 0
	s_setprio 1
	v_mfma_f32_16x16x32_bf16 v[38:41], v[122:125], v[154:157], v[38:41]
	v_mfma_f32_16x16x32_bf16 v[70:73], v[130:133], v[158:161], v[38:41]
	v_mfma_f32_16x16x32_bf16 v[38:41], v[142:145], v[154:157], v[46:49]
	v_mfma_f32_16x16x32_bf16 v[66:69], v[150:153], v[158:161], v[38:41]
	v_mfma_f32_16x16x32_bf16 v[38:41], v[122:125], v[166:169], v[42:45]
	v_mfma_f32_16x16x32_bf16 v[34:37], v[142:145], v[166:169], v[34:37]
	v_mfma_f32_16x16x32_bf16 v[22:25], v[122:125], v[188:191], v[22:25]
	v_mfma_f32_16x16x32_bf16 v[18:21], v[142:145], v[188:191], v[18:21]
	v_mfma_f32_16x16x32_bf16 v[6:9], v[122:125], v[202:205], v[6:9]
	v_mfma_f32_16x16x32_bf16 v[2:5], v[142:145], v[202:205], v[2:5]
	v_mfma_f32_16x16x32_bf16 v[42:45], v[130:133], v[184:187], v[38:41]
	v_mfma_f32_16x16x32_bf16 v[34:37], v[150:153], v[184:187], v[34:37]
	v_mfma_f32_16x16x32_bf16 v[22:25], v[130:133], v[192:195], v[22:25]
	v_mfma_f32_16x16x32_bf16 v[18:21], v[150:153], v[192:195], v[18:21]
	v_mfma_f32_16x16x32_bf16 v[6:9], v[130:133], v[216:219], v[6:9]
	v_mfma_f32_16x16x32_bf16 v[2:5], v[150:153], v[216:219], v[2:5]
	s_add_i32 s14, s14, 2
	s_add_u32 s24, s24, 0x100
	s_addc_u32 s25, s25, 0
	s_add_u32 s12, s12, 0x100
	s_addc_u32 s13, s13, 0
	s_cmp_gt_u32 s14, 5
	s_setprio 0
	s_barrier
	s_cbranch_scc0 .LBB0_1443
	s_and_b64 vcc, exec, s[42:43]
	s_cbranch_vccz .LBB0_1446
	s_barrier

; #define PG8_STAGE(bufoff, gbase, voff) do { _Pragma("unroll") for (int _i = 0; _i < 2; ++_i) \
;         __builtin_amdgcn_global_load_lds((const unsigned*)((const char*)(gbase) + (voff)[_i]), (LAS unsigned*)(lds + (bufoff) + ldsw + _i * 8192), 16, 0, 0); } while (0)
; #define PG8_STAGE_A(bufoff, kptr, half, VO) do { if constexpr (GATHER) { _Pragma("unroll") for (int _i = 0; _i < 2; ++_i) \
;         __builtin_amdgcn_global_load_lds((const unsigned*)((const char*)(kptr) + (VO)[half][_i]), (LAS unsigned*)(lds + (bufoff) + ldsw + _i * 8192), 16, 0, 0); } \
;         else { PG8_STAGE(bufoff, (kptr) + (half) * hstepA, voffA); } } while (0)
; #define PG8_LDA(dst, b, h) do { _Pragma("unroll") for (int m = 0; m < 4; ++m) _Pragma("unroll") for (int k = 0; k < 2; ++k) dst[m][k] = *(const LAS bf16x8*)(lds + PG8_SA(b, h) + aoff + m * 2048 + k * 1024); } while (0)
; #define PG8_LDB(dst, b, h) do { _Pragma("unroll") for (int n = 0; n < 2; ++n) _Pragma("unroll") for (int k = 0; k < 2; ++k) dst[n][k] = *(const LAS bf16x8*)(lds + PG8_SB(b, h) + boff + n * 2048 + k * 1024); } while (0)
; #define PG8_WAIT_V(n) asm volatile("s_waitcnt vmcnt(" #n ")" ::: "memory")
; #define PG8_WAIT_L(n) asm volatile("s_waitcnt lgkmcnt(" #n ")" ::: "memory")
;     ...
;         for (int t = 0; t < nt; t += 2) {
;             const bool last = (t == nt - 2);
;             const char* a1 = cA + (size_t)(t + 1) * kstep;
;             const char* a2 = last ? nA : cA + (size_t)(t + 2) * kstep; const char* b2 = last ? nB : cB + (size_t)(t + 2) * kstep;
;             const char* a3 = a2 + kstep; const char* b3 = b2 + kstep;
;             unsigned g2[2][2];
;             if constexpr (GATHER) {
; #pragma unroll
;                 for (int _h = 0; _h < 2; ++_h)
; #pragma unroll
;                     for (int _i = 0; _i < 2; ++_i) g2[_h][_i] = last ? gN[_h][_i] : gC[_h][_i]; }
;             if constexpr (SP2) {
;             PG8_LDB(B0, 0, 0); PG8_LDB(B1, 0, 1); PG8_SCHED; PG8_LDA(At, 0, 0); PG8_STAGE_A(PG8_SA(1, 1), a1, 1, gC);
;             PG8_WAIT_V(8); PG8_WAIT_L(0); PG8_BAR; PG8_MMA(0, 0, At, B0); PG8_MMA(0, 1, At, B1); PG8_BAR; PG8_SCHED;
;             PG8_LDA(At, 0, 1); PG8_STAGE(PG8_SB(0, 0), b2, voffB); PG8_STAGE(PG8_SB(0, 1), b2 + hstepB, voffB); PG8_STAGE_A(PG8_SA(0, 0), a2, 0, g2);
;             PG8_WAIT_V(8); PG8_WAIT_L(0); PG8_BAR; PG8_MMA(1, 0, At, B0); PG8_MMA(1, 1, At, B1); PG8_BAR; PG8_SCHED;
.LBB0_1669:
	s_add_u32 s0, s24, 0xfff80080
	s_addc_u32 s1, s25, -1
	s_add_i32 s15, 0, 0x10000
	s_cmp_eq_u32 s14, 28
	s_cselect_b32 s31, s45, s1
	s_cselect_b32 s30, s44, s0
	v_add_u32_e32 v158, s15, v161
	s_cselect_b32 s1, s47, s13
	s_cselect_b32 s0, s46, s12
	s_add_i32 s18, 0, 0x14000
	ds_read_b128 v[164:167], v158
	ds_read_b128 v[168:171], v158 offset:1024
	ds_read_b128 v[172:175], v158 offset:2048
	ds_read_b128 v[176:179], v158 offset:3072
	v_add_u32_e32 v158, s18, v161
	ds_read_b128 v[180:183], v158
	ds_read_b128 v[184:187], v158 offset:1024
	ds_read_b128 v[188:191], v158 offset:2048
	ds_read_b128 v[192:195], v158 offset:3072
	v_lshl_add_u64 v[158:159], s[24:25], 0, v[154:155]
	s_add_i32 m0, s49, 0xc000
	ds_read_b128 v[196:199], v163
	ds_read_b128 v[200:203], v163 offset:1024
	ds_read_b128 v[216:219], v163 offset:2048
	ds_read_b128 v[220:223], v163 offset:3072
	ds_read_b128 v[224:227], v163 offset:4096
	ds_read_b128 v[228:231], v163 offset:5120
	ds_read_b128 v[232:235], v163 offset:6144
	ds_read_b128 v[236:239], v163 offset:7168
	global_load_lds_dwordx4 v[158:159], off
	v_lshl_add_u64 v[158:159], s[24:25], 0, v[156:157]
	s_add_i32 m0, s49, 0xe000
	s_nop 0
	global_load_lds_dwordx4 v[158:159], off
	s_waitcnt vmcnt(8)
	s_waitcnt lgkmcnt(0)
	s_barrier
	s_setprio 1
	s_waitcnt lgkmcnt(0)
	v_mfma_f32_16x16x32_bf16 v[126:129], v[164:167], v[196:199], v[126:129]
	v_mfma_f32_16x16x32_bf16 v[122:125], v[172:175], v[196:199], v[122:125]
	v_mfma_f32_16x16x32_bf16 v[118:121], v[164:167], v[216:219], v[118:121]
	v_mfma_f32_16x16x32_bf16 v[114:117], v[172:175], v[216:219], v[114:117]
	v_mfma_f32_16x16x32_bf16 v[102:105], v[164:167], v[224:227], v[102:105]
	v_mfma_f32_16x16x32_bf16 v[98:101], v[172:175], v[224:227], v[98:101]
	v_mfma_f32_16x16x32_bf16 v[86:89], v[164:167], v[232:235], v[86:89]
	v_mfma_f32_16x16x32_bf16 v[82:85], v[172:175], v[232:235], v[82:85]
	v_mfma_f32_16x16x32_bf16 v[126:129], v[168:171], v[200:203], v[126:129]
	v_mfma_f32_16x16x32_bf16 v[122:125], v[176:179], v[200:203], v[122:125]
	v_mfma_f32_16x16x32_bf16 v[118:121], v[168:171], v[220:223], v[118:121]
	v_mfma_f32_16x16x32_bf16 v[114:117], v[176:179], v[220:223], v[114:117]
	v_mfma_f32_16x16x32_bf16 v[102:105], v[168:171], v[228:231], v[102:105]
	v_mfma_f32_16x16x32_bf16 v[98:101], v[176:179], v[228:231], v[98:101]
	v_mfma_f32_16x16x32_bf16 v[86:89], v[168:171], v[236:239], v[86:89]
	v_mfma_f32_16x16x32_bf16 v[82:85], v[176:179], v[236:239], v[82:85]
	s_setprio 0
	s_setprio 1
	v_mfma_f32_16x16x32_bf16 v[110:113], v[180:183], v[196:199], v[110:113]
	v_mfma_f32_16x16x32_bf16 v[106:109], v[188:191], v[196:199], v[106:109]
	v_mfma_f32_16x16x32_bf16 v[94:97], v[180:183], v[216:219], v[94:97]
	v_mfma_f32_16x16x32_bf16 v[90:93], v[188:191], v[216:219], v[90:93]
	v_mfma_f32_16x16x32_bf16 v[78:81], v[180:183], v[224:227], v[78:81]
	v_mfma_f32_16x16x32_bf16 v[74:77], v[188:191], v[224:227], v[74:77]
	v_mfma_f32_16x16x32_bf16 v[70:73], v[180:183], v[232:235], v[70:73]
	v_mfma_f32_16x16x32_bf16 v[66:69], v[188:191], v[232:235], v[66:69]
	v_mfma_f32_16x16x32_bf16 v[110:113], v[184:187], v[200:203], v[110:113]
	v_mfma_f32_16x16x32_bf16 v[106:109], v[192:195], v[200:203], v[106:109]
	v_mfma_f32_16x16x32_bf16 v[94:97], v[184:187], v[220:223], v[94:97]
	v_mfma_f32_16x16x32_bf16 v[90:93], v[192:195], v[220:223], v[90:93]
	v_mfma_f32_16x16x32_bf16 v[78:81], v[184:187], v[228:231], v[78:81]
	v_mfma_f32_16x16x32_bf16 v[74:77], v[192:195], v[228:231], v[74:77]
	v_mfma_f32_16x16x32_bf16 v[70:73], v[184:187], v[236:239], v[70:73]
	v_mfma_f32_16x16x32_bf16 v[66:69], v[192:195], v[236:239], v[66:69]
	s_setprio 0
	s_barrier
	s_add_i32 s15, s15, s52
	v_lshl_add_u64 v[158:159], s[0:1], 0, v[206:207]
	s_mov_b32 m0, s15
	ds_read_b128 v[196:199], v163 offset:16384
	ds_read_b128 v[200:203], v163 offset:17408
	ds_read_b128 v[216:219], v163 offset:18432
	ds_read_b128 v[220:223], v163 offset:19456
	ds_read_b128 v[224:227], v163 offset:20480
	ds_read_b128 v[228:231], v163 offset:21504
	ds_read_b128 v[232:235], v163 offset:22528
	ds_read_b128 v[236:239], v163 offset:23552
	global_load_lds_dwordx4 v[158:159], off
	s_add_i32 m0, s15, 0x2000
	s_add_u32 s16, s0, 0x80000
	v_lshl_add_u64 v[204:205], s[0:1], 0, v[130:131]
	s_addc_u32 s17, s1, 0
	s_add_i32 s15, s18, s52
	global_load_lds_dwordx4 v[204:205], off
	v_lshl_add_u64 v[208:209], s[16:17], 0, v[206:207]
	s_mov_b32 m0, s15
	v_lshl_add_u64 v[210:211], s[30:31], 0, v[132:133]
	global_load_lds_dwordx4 v[208:209], off
	v_lshl_add_u64 v[208:209], s[16:17], 0, v[130:131]
	s_add_i32 m0, s15, 0x2000
	s_nop 0
	global_load_lds_dwordx4 v[208:209], off
	v_lshl_add_u64 v[208:209], s[30:31], 0, v[134:135]
	s_mov_b32 m0, s49
	s_nop 0
	global_load_lds_dwordx4 v[208:209], off
	s_mov_b32 m0, s53
	s_nop 0
	global_load_lds_dwordx4 v[210:211], off
	s_waitcnt vmcnt(8)
	s_waitcnt lgkmcnt(0)
	s_barrier
; #define PG8_STAGE_A(bufoff, kptr, half, VO) do { if constexpr (GATHER) { _Pragma("unroll") for (int _i = 0; _i < 2; ++_i) \
;         __builtin_amdgcn_global_load_lds((const unsigned*)((const char*)(kptr) + (VO)[half][_i]), (LAS unsigned*)(lds + (bufoff) + ldsw + _i * 8192), 16, 0, 0); } \
;         else { PG8_STAGE(bufoff, (kptr) + (half) * hstepA, voffA); } } while (0)
; #define PG8_LDA(dst, b, h) do { _Pragma("unroll") for (int m = 0; m < 4; ++m) _Pragma("unroll") for (int k = 0; k < 2; ++k) dst[m][k] = *(const LAS bf16x8*)(lds + PG8_SA(b, h) + aoff + m * 2048 + k * 1024); } while (0)
; #define PG8_LDB(dst, b, h) do { _Pragma("unroll") for (int n = 0; n < 2; ++n) _Pragma("unroll") for (int k = 0; k < 2; ++k) dst[n][k] = *(const LAS bf16x8*)(lds + PG8_SB(b, h) + boff + n * 2048 + k * 1024); } while (0)
; #define PG8_MMA(ai, bj, At, Bt) do { __builtin_amdgcn_s_setprio(1); _Pragma("unroll") for (int m = 0; m < 4; ++m) _Pragma("unroll") for (int n = 0; n < 2; ++n) _Pragma("unroll") for (int k = 0; k < 2; ++k) \
;         acc[ai][bj][m][n] = __builtin_amdgcn_mfma_f32_16x16x32_bf16(Bt[n][k], At[m][k], acc[ai][bj][m][n], 0, 0, 0); __builtin_amdgcn_s_setprio(0); } while (0)
; #define PG8_WAIT_V(n) asm volatile("s_waitcnt vmcnt(" #n ")" ::: "memory")
; #define PG8_WAIT_L(n) asm volatile("s_waitcnt lgkmcnt(" #n ")" ::: "memory")
; #define PG8_BAR __builtin_amdgcn_s_barrier()
; #define PG8_SCHED __builtin_amdgcn_sched_barrier(0)
;     ...
;             PG8_WAIT_V(8); PG8_WAIT_L(0); PG8_BAR; PG8_MMA(1, 0, At, B0); PG8_MMA(1, 1, At, B1); PG8_BAR; PG8_SCHED;
;             PG8_LDB(B0, 1, 0); PG8_LDB(B1, 1, 1); PG8_SCHED; PG8_LDA(At, 1, 0); PG8_STAGE_A(PG8_SA(0, 1), a2, 1, g2);
;             PG8_WAIT_V(8); PG8_WAIT_L(0); PG8_BAR; PG8_MMA(0, 0, At, B0); PG8_MMA(0, 1, At, B1); PG8_BAR; PG8_SCHED;
	s_setprio 1
	s_waitcnt lgkmcnt(0)
	v_mfma_f32_16x16x32_bf16 v[62:65], v[164:167], v[196:199], v[62:65]
	v_mfma_f32_16x16x32_bf16 v[58:61], v[172:175], v[196:199], v[58:61]
	v_mfma_f32_16x16x32_bf16 v[54:57], v[164:167], v[216:219], v[54:57]
	v_mfma_f32_16x16x32_bf16 v[50:53], v[172:175], v[216:219], v[50:53]
	v_mfma_f32_16x16x32_bf16 v[38:41], v[164:167], v[224:227], v[38:41]
	v_mfma_f32_16x16x32_bf16 v[34:37], v[172:175], v[224:227], v[34:37]
	v_mfma_f32_16x16x32_bf16 v[22:25], v[164:167], v[232:235], v[22:25]
	v_mfma_f32_16x16x32_bf16 v[18:21], v[172:175], v[232:235], v[18:21]
	v_mfma_f32_16x16x32_bf16 v[62:65], v[168:171], v[200:203], v[62:65]
	v_mfma_f32_16x16x32_bf16 v[58:61], v[176:179], v[200:203], v[58:61]
	v_mfma_f32_16x16x32_bf16 v[54:57], v[168:171], v[220:223], v[54:57]
	v_mfma_f32_16x16x32_bf16 v[50:53], v[176:179], v[220:223], v[50:53]
	v_mfma_f32_16x16x32_bf16 v[38:41], v[168:171], v[228:231], v[38:41]
	v_mfma_f32_16x16x32_bf16 v[34:37], v[176:179], v[228:231], v[34:37]
	v_mfma_f32_16x16x32_bf16 v[22:25], v[168:171], v[236:239], v[22:25]
	v_mfma_f32_16x16x32_bf16 v[18:21], v[176:179], v[236:239], v[18:21]
	s_setprio 0
	s_setprio 1
	v_mfma_f32_16x16x32_bf16 v[46:49], v[180:183], v[196:199], v[46:49]
	v_mfma_f32_16x16x32_bf16 v[42:45], v[188:191], v[196:199], v[42:45]
	v_mfma_f32_16x16x32_bf16 v[30:33], v[180:183], v[216:219], v[30:33]
	v_mfma_f32_16x16x32_bf16 v[26:29], v[188:191], v[216:219], v[26:29]
	v_mfma_f32_16x16x32_bf16 v[14:17], v[180:183], v[224:227], v[14:17]
	v_mfma_f32_16x16x32_bf16 v[10:13], v[188:191], v[224:227], v[10:13]
	v_mfma_f32_16x16x32_bf16 v[6:9], v[180:183], v[232:235], v[6:9]
	v_mfma_f32_16x16x32_bf16 v[2:5], v[188:191], v[232:235], v[2:5]
	v_mfma_f32_16x16x32_bf16 v[46:49], v[184:187], v[200:203], v[46:49]
	v_mfma_f32_16x16x32_bf16 v[42:45], v[192:195], v[200:203], v[42:45]
	v_mfma_f32_16x16x32_bf16 v[30:33], v[184:187], v[220:223], v[30:33]
	v_mfma_f32_16x16x32_bf16 v[26:29], v[192:195], v[220:223], v[26:29]
	v_mfma_f32_16x16x32_bf16 v[14:17], v[184:187], v[228:231], v[14:17]
	v_mfma_f32_16x16x32_bf16 v[10:13], v[192:195], v[228:231], v[10:13]
	v_mfma_f32_16x16x32_bf16 v[6:9], v[184:187], v[236:239], v[6:9]
	v_mfma_f32_16x16x32_bf16 v[2:5], v[192:195], v[236:239], v[2:5]
	s_setprio 0
	s_barrier
	s_add_i32 s15, 0, 0x18000
	s_add_i32 s18, 0, 0x1c000
	v_add_u32_e32 v176, s15, v161
	v_add_u32_e32 v192, s18, v161
	ds_read_b128 v[164:167], v176
	ds_read_b128 v[168:171], v176 offset:1024
	ds_read_b128 v[172:175], v176 offset:2048
	ds_read_b128 v[176:179], v176 offset:3072
	ds_read_b128 v[180:183], v192
	ds_read_b128 v[184:187], v192 offset:1024
	ds_read_b128 v[188:191], v192 offset:2048
	ds_read_b128 v[192:195], v192 offset:3072
	s_add_u32 s16, s30, 0x80000
	s_addc_u32 s17, s31, 0
	s_mov_b32 m0, s59
	v_lshl_add_u64 v[212:213], s[16:17], 0, v[134:135]
	ds_read_b128 v[196:199], v163 offset:32768
	ds_read_b128 v[200:203], v163 offset:33792
	ds_read_b128 v[216:219], v163 offset:34816
	ds_read_b128 v[220:223], v163 offset:35840
	ds_read_b128 v[224:227], v163 offset:36864
	ds_read_b128 v[228:231], v163 offset:37888
	ds_read_b128 v[232:235], v163 offset:38912
	ds_read_b128 v[236:239], v163 offset:39936
	global_load_lds_dwordx4 v[212:213], off
	v_lshl_add_u64 v[212:213], s[16:17], 0, v[132:133]
	s_mov_b32 m0, s60
	s_nop 0
	global_load_lds_dwordx4 v[212:213], off
	s_waitcnt vmcnt(8)
	s_waitcnt lgkmcnt(0)
	s_barrier
	s_setprio 1
	s_waitcnt lgkmcnt(0)
	v_mfma_f32_16x16x32_bf16 v[126:129], v[164:167], v[196:199], v[126:129]
	v_mfma_f32_16x16x32_bf16 v[122:125], v[172:175], v[196:199], v[122:125]
	v_mfma_f32_16x16x32_bf16 v[118:121], v[164:167], v[216:219], v[118:121]
	v_mfma_f32_16x16x32_bf16 v[114:117], v[172:175], v[216:219], v[114:117]
	v_mfma_f32_16x16x32_bf16 v[102:105], v[164:167], v[224:227], v[102:105]
	v_mfma_f32_16x16x32_bf16 v[98:101], v[172:175], v[224:227], v[98:101]
	v_mfma_f32_16x16x32_bf16 v[86:89], v[164:167], v[232:235], v[86:89]
	v_mfma_f32_16x16x32_bf16 v[82:85], v[172:175], v[232:235], v[82:85]
	v_mfma_f32_16x16x32_bf16 v[126:129], v[168:171], v[200:203], v[126:129]
	v_mfma_f32_16x16x32_bf16 v[122:125], v[176:179], v[200:203], v[122:125]
	v_mfma_f32_16x16x32_bf16 v[118:121], v[168:171], v[220:223], v[118:121]
	v_mfma_f32_16x16x32_bf16 v[114:117], v[176:179], v[220:223], v[114:117]
	v_mfma_f32_16x16x32_bf16 v[102:105], v[168:171], v[228:231], v[102:105]
	v_mfma_f32_16x16x32_bf16 v[98:101], v[176:179], v[228:231], v[98:101]
	v_mfma_f32_16x16x32_bf16 v[86:89], v[168:171], v[236:239], v[86:89]
	v_mfma_f32_16x16x32_bf16 v[82:85], v[176:179], v[236:239], v[82:85]
	s_setprio 0
	s_setprio 1
	v_mfma_f32_16x16x32_bf16 v[110:113], v[180:183], v[196:199], v[110:113]
	v_mfma_f32_16x16x32_bf16 v[106:109], v[188:191], v[196:199], v[106:109]
	v_mfma_f32_16x16x32_bf16 v[94:97], v[180:183], v[216:219], v[94:97]
	v_mfma_f32_16x16x32_bf16 v[90:93], v[188:191], v[216:219], v[90:93]
	v_mfma_f32_16x16x32_bf16 v[78:81], v[180:183], v[224:227], v[78:81]
	v_mfma_f32_16x16x32_bf16 v[74:77], v[188:191], v[224:227], v[74:77]
	v_mfma_f32_16x16x32_bf16 v[70:73], v[180:183], v[232:235], v[70:73]
	v_mfma_f32_16x16x32_bf16 v[66:69], v[188:191], v[232:235], v[66:69]
	v_mfma_f32_16x16x32_bf16 v[110:113], v[184:187], v[200:203], v[110:113]
	v_mfma_f32_16x16x32_bf16 v[106:109], v[192:195], v[200:203], v[106:109]
	v_mfma_f32_16x16x32_bf16 v[94:97], v[184:187], v[220:223], v[94:97]
	v_mfma_f32_16x16x32_bf16 v[90:93], v[192:195], v[220:223], v[90:93]
	v_mfma_f32_16x16x32_bf16 v[78:81], v[184:187], v[228:231], v[78:81]
	v_mfma_f32_16x16x32_bf16 v[74:77], v[192:195], v[228:231], v[74:77]
	v_mfma_f32_16x16x32_bf16 v[70:73], v[184:187], v[236:239], v[70:73]
	v_mfma_f32_16x16x32_bf16 v[66:69], v[192:195], v[236:239], v[66:69]
	s_setprio 0
	s_barrier
; #define PG8_STAGE(bufoff, gbase, voff) do { _Pragma("unroll") for (int _i = 0; _i < 2; ++_i) \
;         __builtin_amdgcn_global_load_lds((const unsigned*)((const char*)(gbase) + (voff)[_i]), (LAS unsigned*)(lds + (bufoff) + ldsw + _i * 8192), 16, 0, 0); } while (0)
; #define PG8_STAGE_A(bufoff, kptr, half, VO) do { if constexpr (GATHER) { _Pragma("unroll") for (int _i = 0; _i < 2; ++_i) \
;         __builtin_amdgcn_global_load_lds((const unsigned*)((const char*)(kptr) + (VO)[half][_i]), (LAS unsigned*)(lds + (bufoff) + ldsw + _i * 8192), 16, 0, 0); } \
;         else { PG8_STAGE(bufoff, (kptr) + (half) * hstepA, voffA); } } while (0)
; #define PG8_LDA(dst, b, h) do { _Pragma("unroll") for (int m = 0; m < 4; ++m) _Pragma("unroll") for (int k = 0; k < 2; ++k) dst[m][k] = *(const LAS bf16x8*)(lds + PG8_SA(b, h) + aoff + m * 2048 + k * 1024); } while (0)
; #define PG8_MMA(ai, bj, At, Bt) do { __builtin_amdgcn_s_setprio(1); _Pragma("unroll") for (int m = 0; m < 4; ++m) _Pragma("unroll") for (int n = 0; n < 2; ++n) _Pragma("unroll") for (int k = 0; k < 2; ++k) \
;         acc[ai][bj][m][n] = __builtin_amdgcn_mfma_f32_16x16x32_bf16(Bt[n][k], At[m][k], acc[ai][bj][m][n], 0, 0, 0); __builtin_amdgcn_s_setprio(0); } while (0)
; #define PG8_WAIT_V(n) asm volatile("s_waitcnt vmcnt(" #n ")" ::: "memory")
; #define PG8_WAIT_L(n) asm volatile("s_waitcnt lgkmcnt(" #n ")" ::: "memory")
; #define PG8_BAR __builtin_amdgcn_s_barrier()
; #define PG8_SCHED __builtin_amdgcn_sched_barrier(0)
;     ...
;         for (int t = 0; t < nt; t += 2) {
;     ...
;             PG8_LDA(At, 1, 1); PG8_STAGE(PG8_SB(1, 0), b3, voffB); PG8_STAGE(PG8_SB(1, 1), b3 + hstepB, voffB); PG8_STAGE_A(PG8_SA(1, 0), a3, 0, g2);
;             PG8_WAIT_V(8); PG8_WAIT_L(0); PG8_BAR; PG8_MMA(1, 0, At, B0); PG8_MMA(1, 1, At, B1); PG8_BAR; PG8_SCHED;
	s_add_i32 s15, s15, s52
	v_lshl_add_u64 v[158:159], v[158:159], 0, s[8:9]
	s_mov_b32 m0, s15
	ds_read_b128 v[196:199], v163 offset:49152
	ds_read_b128 v[200:203], v163 offset:50176
	ds_read_b128 v[216:219], v163 offset:51200
	ds_read_b128 v[220:223], v163 offset:52224
	ds_read_b128 v[224:227], v163 offset:53248
	ds_read_b128 v[228:231], v163 offset:54272
	ds_read_b128 v[232:235], v163 offset:55296
	ds_read_b128 v[236:239], v163 offset:56320
	global_load_lds_dwordx4 v[158:159], off
	s_add_i32 m0, s15, 0x2000
	s_add_u32 s0, s0, 0x80080
	v_lshl_add_u64 v[158:159], v[204:205], 0, s[8:9]
	s_addc_u32 s1, s1, 0
	s_add_i32 s15, s18, s52
	global_load_lds_dwordx4 v[158:159], off
	v_lshl_add_u64 v[158:159], s[0:1], 0, v[206:207]
	s_mov_b32 m0, s15
	s_nop 0
	global_load_lds_dwordx4 v[158:159], off
	v_lshl_add_u64 v[158:159], s[0:1], 0, v[130:131]
	s_add_i32 m0, s15, 0x2000
	s_nop 0
	global_load_lds_dwordx4 v[158:159], off
	v_lshl_add_u64 v[158:159], v[208:209], 0, s[8:9]
	s_mov_b32 m0, s61
	s_nop 0
	global_load_lds_dwordx4 v[158:159], off
	v_lshl_add_u64 v[158:159], v[210:211], 0, s[8:9]
	s_mov_b32 m0, s62
	s_nop 0
	global_load_lds_dwordx4 v[158:159], off
	s_waitcnt vmcnt(8)
	s_waitcnt lgkmcnt(0)
	s_barrier
	s_setprio 1
	s_waitcnt lgkmcnt(0)
	v_mfma_f32_16x16x32_bf16 v[62:65], v[164:167], v[196:199], v[62:65]
	v_mfma_f32_16x16x32_bf16 v[58:61], v[172:175], v[196:199], v[58:61]
	v_mfma_f32_16x16x32_bf16 v[54:57], v[164:167], v[216:219], v[54:57]
	v_mfma_f32_16x16x32_bf16 v[50:53], v[172:175], v[216:219], v[50:53]
	v_mfma_f32_16x16x32_bf16 v[38:41], v[164:167], v[224:227], v[38:41]
	v_mfma_f32_16x16x32_bf16 v[34:37], v[172:175], v[224:227], v[34:37]
	v_mfma_f32_16x16x32_bf16 v[22:25], v[164:167], v[232:235], v[22:25]
	v_mfma_f32_16x16x32_bf16 v[18:21], v[172:175], v[232:235], v[18:21]
	v_mfma_f32_16x16x32_bf16 v[62:65], v[168:171], v[200:203], v[62:65]
	v_mfma_f32_16x16x32_bf16 v[58:61], v[176:179], v[200:203], v[58:61]
	v_mfma_f32_16x16x32_bf16 v[54:57], v[168:171], v[220:223], v[54:57]
	v_mfma_f32_16x16x32_bf16 v[50:53], v[176:179], v[220:223], v[50:53]
	v_mfma_f32_16x16x32_bf16 v[38:41], v[168:171], v[228:231], v[38:41]
	v_mfma_f32_16x16x32_bf16 v[34:37], v[176:179], v[228:231], v[34:37]
	v_mfma_f32_16x16x32_bf16 v[22:25], v[168:171], v[236:239], v[22:25]
	v_mfma_f32_16x16x32_bf16 v[18:21], v[176:179], v[236:239], v[18:21]
	s_setprio 0
	s_setprio 1
	v_mfma_f32_16x16x32_bf16 v[46:49], v[180:183], v[196:199], v[46:49]
	v_mfma_f32_16x16x32_bf16 v[42:45], v[188:191], v[196:199], v[42:45]
	v_mfma_f32_16x16x32_bf16 v[30:33], v[180:183], v[216:219], v[30:33]
	v_mfma_f32_16x16x32_bf16 v[26:29], v[188:191], v[216:219], v[26:29]
	v_mfma_f32_16x16x32_bf16 v[14:17], v[180:183], v[224:227], v[14:17]
	v_mfma_f32_16x16x32_bf16 v[10:13], v[188:191], v[224:227], v[10:13]
	v_mfma_f32_16x16x32_bf16 v[6:9], v[180:183], v[232:235], v[6:9]
	v_mfma_f32_16x16x32_bf16 v[2:5], v[188:191], v[232:235], v[2:5]
	v_mfma_f32_16x16x32_bf16 v[46:49], v[184:187], v[200:203], v[46:49]
	v_mfma_f32_16x16x32_bf16 v[42:45], v[192:195], v[200:203], v[42:45]
	v_mfma_f32_16x16x32_bf16 v[30:33], v[184:187], v[220:223], v[30:33]
	v_mfma_f32_16x16x32_bf16 v[26:29], v[192:195], v[220:223], v[26:29]
	v_mfma_f32_16x16x32_bf16 v[14:17], v[184:187], v[228:231], v[14:17]
	v_mfma_f32_16x16x32_bf16 v[10:13], v[192:195], v[228:231], v[10:13]
	v_mfma_f32_16x16x32_bf16 v[6:9], v[184:187], v[236:239], v[6:9]
	v_mfma_f32_16x16x32_bf16 v[2:5], v[192:195], v[236:239], v[2:5]
	s_add_i32 s14, s14, 2
	s_add_u32 s24, s24, 0x100
	s_addc_u32 s25, s25, 0
	s_add_u32 s12, s12, 0x100
	s_addc_u32 s13, s13, 0
	s_cmp_gt_u32 s14, 29
	s_setprio 0
	s_barrier
	s_cbranch_scc0 .LBB0_1669
	s_and_b64 vcc, exec, s[38:39]
	s_cbranch_vccz .LBB0_1672
	s_barrier

; #define PG8_STAGE(bufoff, gbase, voff) do { _Pragma("unroll") for (int _i = 0; _i < 2; ++_i) \
;         __builtin_amdgcn_global_load_lds((const unsigned*)((const char*)(gbase) + (voff)[_i]), (LAS unsigned*)(lds + (bufoff) + ldsw + _i * 8192), 16, 0, 0); } while (0)
; #define PG8_STAGE_A(bufoff, kptr, half, VO) do { if constexpr (GATHER) { _Pragma("unroll") for (int _i = 0; _i < 2; ++_i) \
;         __builtin_amdgcn_global_load_lds((const unsigned*)((const char*)(kptr) + (VO)[half][_i]), (LAS unsigned*)(lds + (bufoff) + ldsw + _i * 8192), 16, 0, 0); } \
;         else { PG8_STAGE(bufoff, (kptr) + (half) * hstepA, voffA); } } while (0)
; #define PG8_LDA(dst, b, h) do { _Pragma("unroll") for (int m = 0; m < 4; ++m) _Pragma("unroll") for (int k = 0; k < 2; ++k) dst[m][k] = *(const LAS bf16x8*)(lds + PG8_SA(b, h) + aoff + m * 2048 + k * 1024); } while (0)
; #define PG8_LDB(dst, b, h) do { _Pragma("unroll") for (int n = 0; n < 2; ++n) _Pragma("unroll") for (int k = 0; k < 2; ++k) dst[n][k] = *(const LAS bf16x8*)(lds + PG8_SB(b, h) + boff + n * 2048 + k * 1024); } while (0)
; #define PG8_WAIT_V(n) asm volatile("s_waitcnt vmcnt(" #n ")" ::: "memory")
; #define PG8_WAIT_L(n) asm volatile("s_waitcnt lgkmcnt(" #n ")" ::: "memory")
;     ...
;         for (int t = 0; t < nt; t += 2) {
;             const bool last = (t == nt - 2);
;             const char* a1 = cA + (size_t)(t + 1) * kstep;
;             const char* a2 = last ? nA : cA + (size_t)(t + 2) * kstep; const char* b2 = last ? nB : cB + (size_t)(t + 2) * kstep;
;             const char* a3 = a2 + kstep; const char* b3 = b2 + kstep;
;             unsigned g2[2][2];
;             if constexpr (GATHER) {
; #pragma unroll
;                 for (int _h = 0; _h < 2; ++_h)
; #pragma unroll
;                     for (int _i = 0; _i < 2; ++_i) g2[_h][_i] = last ? gN[_h][_i] : gC[_h][_i]; }
;             if constexpr (SP2) {
;             PG8_LDB(B0, 0, 0); PG8_LDB(B1, 0, 1); PG8_SCHED; PG8_LDA(At, 0, 0); PG8_STAGE_A(PG8_SA(1, 1), a1, 1, gC);
;             PG8_WAIT_V(8); PG8_WAIT_L(0); PG8_BAR; PG8_MMA(0, 0, At, B0); PG8_MMA(0, 1, At, B1); PG8_BAR; PG8_SCHED;
;             PG8_LDA(At, 0, 1); PG8_STAGE(PG8_SB(0, 0), b2, voffB); PG8_STAGE(PG8_SB(0, 1), b2 + hstepB, voffB); PG8_STAGE_A(PG8_SA(0, 0), a2, 0, g2);
;             PG8_WAIT_V(8); PG8_WAIT_L(0); PG8_BAR; PG8_MMA(1, 0, At, B0); PG8_MMA(1, 1, At, B1); PG8_BAR; PG8_SCHED;
.LBB0_1693:
	s_add_u32 s0, s24, 0xfff80080
	s_addc_u32 s1, s25, -1
	s_add_i32 s15, 0, 0x10000
	s_cmp_eq_u32 s14, 28
	s_cselect_b32 s31, s45, s1
	s_cselect_b32 s30, s44, s0
	s_cselect_b32 s1, s47, s13
	s_cselect_b32 s0, s46, s12
	s_add_i32 s18, 0, 0x14000
	v_add_u32_e32 v142, s15, v244
	v_add_u32_e32 v158, s18, v244
	ds_read_b128 v[122:125], v142
	ds_read_b128 v[126:129], v142 offset:1024
	ds_read_b128 v[134:137], v142 offset:2048
	ds_read_b128 v[142:145], v142 offset:3072
	ds_read_b128 v[146:149], v158
	ds_read_b128 v[150:153], v158 offset:1024
	ds_read_b128 v[154:157], v158 offset:2048
	ds_read_b128 v[158:161], v158 offset:3072
	v_lshl_add_u64 v[194:195], s[24:25], 0, v[222:223]
	s_add_i32 m0, s49, 0xc000
	ds_read_b128 v[162:165], v209
	ds_read_b128 v[166:169], v209 offset:1024
	ds_read_b128 v[170:173], v209 offset:2048
	ds_read_b128 v[174:177], v209 offset:3072
	ds_read_b128 v[178:181], v209 offset:4096
	ds_read_b128 v[182:185], v209 offset:5120
	ds_read_b128 v[186:189], v209 offset:6144
	ds_read_b128 v[190:193], v209 offset:7168
	global_load_lds_dwordx4 v[194:195], off
	v_lshl_add_u64 v[194:195], s[24:25], 0, v[224:225]
	s_add_i32 m0, s49, 0xe000
	s_nop 0
	global_load_lds_dwordx4 v[194:195], off
	s_waitcnt vmcnt(8)
	s_waitcnt lgkmcnt(0)
	s_barrier
	s_setprio 1
	s_waitcnt lgkmcnt(0)
	v_mfma_f32_16x16x32_bf16 v[138:141], v[122:125], v[162:165], v[138:141]
	v_mfma_f32_16x16x32_bf16 v[130:133], v[134:137], v[162:165], v[130:133]
	v_mfma_f32_16x16x32_bf16 v[114:117], v[122:125], v[170:173], v[114:117]
	v_mfma_f32_16x16x32_bf16 v[106:109], v[134:137], v[170:173], v[106:109]
	v_mfma_f32_16x16x32_bf16 v[98:101], v[122:125], v[178:181], v[98:101]
	v_mfma_f32_16x16x32_bf16 v[90:93], v[134:137], v[178:181], v[90:93]
	v_mfma_f32_16x16x32_bf16 v[82:85], v[122:125], v[186:189], v[82:85]
	v_mfma_f32_16x16x32_bf16 v[74:77], v[134:137], v[186:189], v[74:77]
	v_mfma_f32_16x16x32_bf16 v[138:141], v[126:129], v[166:169], v[138:141]
	v_mfma_f32_16x16x32_bf16 v[130:133], v[142:145], v[166:169], v[130:133]
	v_mfma_f32_16x16x32_bf16 v[114:117], v[126:129], v[174:177], v[114:117]
	v_mfma_f32_16x16x32_bf16 v[106:109], v[142:145], v[174:177], v[106:109]
	v_mfma_f32_16x16x32_bf16 v[98:101], v[126:129], v[182:185], v[98:101]
	v_mfma_f32_16x16x32_bf16 v[90:93], v[142:145], v[182:185], v[90:93]
	v_mfma_f32_16x16x32_bf16 v[82:85], v[126:129], v[190:193], v[82:85]
	v_mfma_f32_16x16x32_bf16 v[74:77], v[142:145], v[190:193], v[74:77]
	s_setprio 0
	s_setprio 1
	v_mfma_f32_16x16x32_bf16 v[118:121], v[146:149], v[162:165], v[118:121]
	v_mfma_f32_16x16x32_bf16 v[110:113], v[154:157], v[162:165], v[110:113]
	v_mfma_f32_16x16x32_bf16 v[102:105], v[146:149], v[170:173], v[102:105]
	v_mfma_f32_16x16x32_bf16 v[94:97], v[154:157], v[170:173], v[94:97]
	v_mfma_f32_16x16x32_bf16 v[86:89], v[146:149], v[178:181], v[86:89]
	v_mfma_f32_16x16x32_bf16 v[78:81], v[154:157], v[178:181], v[78:81]
	v_mfma_f32_16x16x32_bf16 v[70:73], v[146:149], v[186:189], v[70:73]
	v_mfma_f32_16x16x32_bf16 v[66:69], v[154:157], v[186:189], v[66:69]
	v_mfma_f32_16x16x32_bf16 v[118:121], v[150:153], v[166:169], v[118:121]
	v_mfma_f32_16x16x32_bf16 v[110:113], v[158:161], v[166:169], v[110:113]
	v_mfma_f32_16x16x32_bf16 v[102:105], v[150:153], v[174:177], v[102:105]
	v_mfma_f32_16x16x32_bf16 v[94:97], v[158:161], v[174:177], v[94:97]
	v_mfma_f32_16x16x32_bf16 v[86:89], v[150:153], v[182:185], v[86:89]
	v_mfma_f32_16x16x32_bf16 v[78:81], v[158:161], v[182:185], v[78:81]
	v_mfma_f32_16x16x32_bf16 v[70:73], v[150:153], v[190:193], v[70:73]
	v_mfma_f32_16x16x32_bf16 v[66:69], v[158:161], v[190:193], v[66:69]
	s_setprio 0
	s_barrier
	s_add_i32 s15, s15, s52
	v_lshl_add_u64 v[194:195], s[0:1], 0, v[206:207]
	s_mov_b32 m0, s15
	ds_read_b128 v[162:165], v209 offset:16384
	ds_read_b128 v[166:169], v209 offset:17408
	ds_read_b128 v[170:173], v209 offset:18432
	ds_read_b128 v[174:177], v209 offset:19456
	ds_read_b128 v[178:181], v209 offset:20480
	ds_read_b128 v[182:185], v209 offset:21504
	ds_read_b128 v[186:189], v209 offset:22528
	ds_read_b128 v[190:193], v209 offset:23552
	global_load_lds_dwordx4 v[194:195], off
	s_add_i32 m0, s15, 0x2000
	s_add_u32 s16, s0, 0x80000
	v_lshl_add_u64 v[196:197], s[0:1], 0, v[216:217]
	s_addc_u32 s17, s1, 0
	s_add_i32 s15, s18, s52
	global_load_lds_dwordx4 v[196:197], off
	v_lshl_add_u64 v[198:199], s[16:17], 0, v[206:207]
	s_mov_b32 m0, s15
	v_lshl_add_u64 v[200:201], s[30:31], 0, v[218:219]
	global_load_lds_dwordx4 v[198:199], off
	v_lshl_add_u64 v[198:199], s[16:17], 0, v[216:217]
	s_add_i32 m0, s15, 0x2000
	s_nop 0
	global_load_lds_dwordx4 v[198:199], off
	v_lshl_add_u64 v[198:199], s[30:31], 0, v[220:221]
	s_mov_b32 m0, s49
	s_nop 0
	global_load_lds_dwordx4 v[198:199], off
	s_mov_b32 m0, s53
	s_nop 0
	global_load_lds_dwordx4 v[200:201], off
	s_waitcnt vmcnt(8)
	s_waitcnt lgkmcnt(0)
	s_barrier
; #define PG8_STAGE_A(bufoff, kptr, half, VO) do { if constexpr (GATHER) { _Pragma("unroll") for (int _i = 0; _i < 2; ++_i) \
;         __builtin_amdgcn_global_load_lds((const unsigned*)((const char*)(kptr) + (VO)[half][_i]), (LAS unsigned*)(lds + (bufoff) + ldsw + _i * 8192), 16, 0, 0); } \
;         else { PG8_STAGE(bufoff, (kptr) + (half) * hstepA, voffA); } } while (0)
; #define PG8_LDA(dst, b, h) do { _Pragma("unroll") for (int m = 0; m < 4; ++m) _Pragma("unroll") for (int k = 0; k < 2; ++k) dst[m][k] = *(const LAS bf16x8*)(lds + PG8_SA(b, h) + aoff + m * 2048 + k * 1024); } while (0)
; #define PG8_LDB(dst, b, h) do { _Pragma("unroll") for (int n = 0; n < 2; ++n) _Pragma("unroll") for (int k = 0; k < 2; ++k) dst[n][k] = *(const LAS bf16x8*)(lds + PG8_SB(b, h) + boff + n * 2048 + k * 1024); } while (0)
; #define PG8_MMA(ai, bj, At, Bt) do { __builtin_amdgcn_s_setprio(1); _Pragma("unroll") for (int m = 0; m < 4; ++m) _Pragma("unroll") for (int n = 0; n < 2; ++n) _Pragma("unroll") for (int k = 0; k < 2; ++k) \
;         acc[ai][bj][m][n] = __builtin_amdgcn_mfma_f32_16x16x32_bf16(Bt[n][k], At[m][k], acc[ai][bj][m][n], 0, 0, 0); __builtin_amdgcn_s_setprio(0); } while (0)
; #define PG8_WAIT_V(n) asm volatile("s_waitcnt vmcnt(" #n ")" ::: "memory")
; #define PG8_WAIT_L(n) asm volatile("s_waitcnt lgkmcnt(" #n ")" ::: "memory")
; #define PG8_BAR __builtin_amdgcn_s_barrier()
; #define PG8_SCHED __builtin_amdgcn_sched_barrier(0)
;     ...
;             PG8_WAIT_V(8); PG8_WAIT_L(0); PG8_BAR; PG8_MMA(1, 0, At, B0); PG8_MMA(1, 1, At, B1); PG8_BAR; PG8_SCHED;
;             PG8_LDB(B0, 1, 0); PG8_LDB(B1, 1, 1); PG8_SCHED; PG8_LDA(At, 1, 0); PG8_STAGE_A(PG8_SA(0, 1), a2, 1, g2);
;             PG8_WAIT_V(8); PG8_WAIT_L(0); PG8_BAR; PG8_MMA(0, 0, At, B0); PG8_MMA(0, 1, At, B1); PG8_BAR; PG8_SCHED;
	s_setprio 1
	s_waitcnt lgkmcnt(0)
	v_mfma_f32_16x16x32_bf16 v[62:65], v[122:125], v[162:165], v[62:65]
	v_mfma_f32_16x16x32_bf16 v[58:61], v[134:137], v[162:165], v[58:61]
	v_mfma_f32_16x16x32_bf16 v[50:53], v[122:125], v[170:173], v[50:53]
	v_mfma_f32_16x16x32_bf16 v[42:45], v[134:137], v[170:173], v[42:45]
	v_mfma_f32_16x16x32_bf16 v[34:37], v[122:125], v[178:181], v[34:37]
	v_mfma_f32_16x16x32_bf16 v[26:29], v[134:137], v[178:181], v[26:29]
	v_mfma_f32_16x16x32_bf16 v[18:21], v[122:125], v[186:189], v[18:21]
	v_mfma_f32_16x16x32_bf16 v[10:13], v[134:137], v[186:189], v[10:13]
	v_mfma_f32_16x16x32_bf16 v[62:65], v[126:129], v[166:169], v[62:65]
	v_mfma_f32_16x16x32_bf16 v[58:61], v[142:145], v[166:169], v[58:61]
	v_mfma_f32_16x16x32_bf16 v[50:53], v[126:129], v[174:177], v[50:53]
	v_mfma_f32_16x16x32_bf16 v[42:45], v[142:145], v[174:177], v[42:45]
	v_mfma_f32_16x16x32_bf16 v[34:37], v[126:129], v[182:185], v[34:37]
	v_mfma_f32_16x16x32_bf16 v[26:29], v[142:145], v[182:185], v[26:29]
	v_mfma_f32_16x16x32_bf16 v[18:21], v[126:129], v[190:193], v[18:21]
	v_mfma_f32_16x16x32_bf16 v[10:13], v[142:145], v[190:193], v[10:13]
	s_setprio 0
	s_setprio 1
	v_mfma_f32_16x16x32_bf16 v[54:57], v[146:149], v[162:165], v[54:57]
	v_mfma_f32_16x16x32_bf16 v[46:49], v[154:157], v[162:165], v[46:49]
	v_mfma_f32_16x16x32_bf16 v[38:41], v[146:149], v[170:173], v[38:41]
	v_mfma_f32_16x16x32_bf16 v[30:33], v[154:157], v[170:173], v[30:33]
	v_mfma_f32_16x16x32_bf16 v[22:25], v[146:149], v[178:181], v[22:25]
	v_mfma_f32_16x16x32_bf16 v[14:17], v[154:157], v[178:181], v[14:17]
	v_mfma_f32_16x16x32_bf16 v[6:9], v[146:149], v[186:189], v[6:9]
	v_mfma_f32_16x16x32_bf16 v[2:5], v[154:157], v[186:189], v[2:5]
	v_mfma_f32_16x16x32_bf16 v[54:57], v[150:153], v[166:169], v[54:57]
	v_mfma_f32_16x16x32_bf16 v[46:49], v[158:161], v[166:169], v[46:49]
	v_mfma_f32_16x16x32_bf16 v[38:41], v[150:153], v[174:177], v[38:41]
	v_mfma_f32_16x16x32_bf16 v[30:33], v[158:161], v[174:177], v[30:33]
	v_mfma_f32_16x16x32_bf16 v[22:25], v[150:153], v[182:185], v[22:25]
	v_mfma_f32_16x16x32_bf16 v[14:17], v[158:161], v[182:185], v[14:17]
	v_mfma_f32_16x16x32_bf16 v[6:9], v[150:153], v[190:193], v[6:9]
	v_mfma_f32_16x16x32_bf16 v[2:5], v[158:161], v[190:193], v[2:5]
	s_setprio 0
	s_barrier
	s_add_i32 s15, 0, 0x18000
	s_add_i32 s18, 0, 0x1c000
	v_add_u32_e32 v142, s15, v244
	v_add_u32_e32 v158, s18, v244
	ds_read_b128 v[122:125], v142
	ds_read_b128 v[126:129], v142 offset:1024
	ds_read_b128 v[134:137], v142 offset:2048
	ds_read_b128 v[142:145], v142 offset:3072
	ds_read_b128 v[146:149], v158
	ds_read_b128 v[150:153], v158 offset:1024
	ds_read_b128 v[154:157], v158 offset:2048
	ds_read_b128 v[158:161], v158 offset:3072
	s_add_u32 s16, s30, 0x80000
	s_addc_u32 s17, s31, 0
	s_mov_b32 m0, s59
	v_lshl_add_u64 v[202:203], s[16:17], 0, v[220:221]
	ds_read_b128 v[162:165], v209 offset:32768
	ds_read_b128 v[166:169], v209 offset:33792
	ds_read_b128 v[170:173], v209 offset:34816
	ds_read_b128 v[174:177], v209 offset:35840
	ds_read_b128 v[178:181], v209 offset:36864
	ds_read_b128 v[182:185], v209 offset:37888
	ds_read_b128 v[186:189], v209 offset:38912
	ds_read_b128 v[190:193], v209 offset:39936
	global_load_lds_dwordx4 v[202:203], off
	v_lshl_add_u64 v[202:203], s[16:17], 0, v[218:219]
	s_mov_b32 m0, s60
	s_nop 0
	global_load_lds_dwordx4 v[202:203], off
	s_waitcnt vmcnt(8)
	s_waitcnt lgkmcnt(0)
	s_barrier
	s_setprio 1
	s_waitcnt lgkmcnt(0)
	v_mfma_f32_16x16x32_bf16 v[138:141], v[122:125], v[162:165], v[138:141]
	v_mfma_f32_16x16x32_bf16 v[130:133], v[134:137], v[162:165], v[130:133]
	v_mfma_f32_16x16x32_bf16 v[114:117], v[122:125], v[170:173], v[114:117]
	v_mfma_f32_16x16x32_bf16 v[106:109], v[134:137], v[170:173], v[106:109]
	v_mfma_f32_16x16x32_bf16 v[98:101], v[122:125], v[178:181], v[98:101]
	v_mfma_f32_16x16x32_bf16 v[90:93], v[134:137], v[178:181], v[90:93]
	v_mfma_f32_16x16x32_bf16 v[82:85], v[122:125], v[186:189], v[82:85]
	v_mfma_f32_16x16x32_bf16 v[74:77], v[134:137], v[186:189], v[74:77]
	v_mfma_f32_16x16x32_bf16 v[138:141], v[126:129], v[166:169], v[138:141]
	v_mfma_f32_16x16x32_bf16 v[130:133], v[142:145], v[166:169], v[130:133]
	v_mfma_f32_16x16x32_bf16 v[114:117], v[126:129], v[174:177], v[114:117]
	v_mfma_f32_16x16x32_bf16 v[106:109], v[142:145], v[174:177], v[106:109]
	v_mfma_f32_16x16x32_bf16 v[98:101], v[126:129], v[182:185], v[98:101]
	v_mfma_f32_16x16x32_bf16 v[90:93], v[142:145], v[182:185], v[90:93]
	v_mfma_f32_16x16x32_bf16 v[82:85], v[126:129], v[190:193], v[82:85]
	v_mfma_f32_16x16x32_bf16 v[74:77], v[142:145], v[190:193], v[74:77]
	s_setprio 0
	s_setprio 1
	v_mfma_f32_16x16x32_bf16 v[118:121], v[146:149], v[162:165], v[118:121]
	v_mfma_f32_16x16x32_bf16 v[110:113], v[154:157], v[162:165], v[110:113]
	v_mfma_f32_16x16x32_bf16 v[102:105], v[146:149], v[170:173], v[102:105]
	v_mfma_f32_16x16x32_bf16 v[94:97], v[154:157], v[170:173], v[94:97]
	v_mfma_f32_16x16x32_bf16 v[86:89], v[146:149], v[178:181], v[86:89]
	v_mfma_f32_16x16x32_bf16 v[78:81], v[154:157], v[178:181], v[78:81]
	v_mfma_f32_16x16x32_bf16 v[70:73], v[146:149], v[186:189], v[70:73]
	v_mfma_f32_16x16x32_bf16 v[66:69], v[154:157], v[186:189], v[66:69]
	v_mfma_f32_16x16x32_bf16 v[118:121], v[150:153], v[166:169], v[118:121]
	v_mfma_f32_16x16x32_bf16 v[110:113], v[158:161], v[166:169], v[110:113]
	v_mfma_f32_16x16x32_bf16 v[102:105], v[150:153], v[174:177], v[102:105]
	v_mfma_f32_16x16x32_bf16 v[94:97], v[158:161], v[174:177], v[94:97]
	v_mfma_f32_16x16x32_bf16 v[86:89], v[150:153], v[182:185], v[86:89]
	v_mfma_f32_16x16x32_bf16 v[78:81], v[158:161], v[182:185], v[78:81]
	v_mfma_f32_16x16x32_bf16 v[70:73], v[150:153], v[190:193], v[70:73]
	v_mfma_f32_16x16x32_bf16 v[66:69], v[158:161], v[190:193], v[66:69]
	s_setprio 0
	s_barrier
; #define PG8_STAGE(bufoff, gbase, voff) do { _Pragma("unroll") for (int _i = 0; _i < 2; ++_i) \
;         __builtin_amdgcn_global_load_lds((const unsigned*)((const char*)(gbase) + (voff)[_i]), (LAS unsigned*)(lds + (bufoff) + ldsw + _i * 8192), 16, 0, 0); } while (0)
; #define PG8_STAGE_A(bufoff, kptr, half, VO) do { if constexpr (GATHER) { _Pragma("unroll") for (int _i = 0; _i < 2; ++_i) \
;         __builtin_amdgcn_global_load_lds((const unsigned*)((const char*)(kptr) + (VO)[half][_i]), (LAS unsigned*)(lds + (bufoff) + ldsw + _i * 8192), 16, 0, 0); } \
;         else { PG8_STAGE(bufoff, (kptr) + (half) * hstepA, voffA); } } while (0)
; #define PG8_LDA(dst, b, h) do { _Pragma("unroll") for (int m = 0; m < 4; ++m) _Pragma("unroll") for (int k = 0; k < 2; ++k) dst[m][k] = *(const LAS bf16x8*)(lds + PG8_SA(b, h) + aoff + m * 2048 + k * 1024); } while (0)
; #define PG8_MMA(ai, bj, At, Bt) do { __builtin_amdgcn_s_setprio(1); _Pragma("unroll") for (int m = 0; m < 4; ++m) _Pragma("unroll") for (int n = 0; n < 2; ++n) _Pragma("unroll") for (int k = 0; k < 2; ++k) \
;         acc[ai][bj][m][n] = __builtin_amdgcn_mfma_f32_16x16x32_bf16(Bt[n][k], At[m][k], acc[ai][bj][m][n], 0, 0, 0); __builtin_amdgcn_s_setprio(0); } while (0)
; #define PG8_WAIT_V(n) asm volatile("s_waitcnt vmcnt(" #n ")" ::: "memory")
; #define PG8_WAIT_L(n) asm volatile("s_waitcnt lgkmcnt(" #n ")" ::: "memory")
; #define PG8_BAR __builtin_amdgcn_s_barrier()
; #define PG8_SCHED __builtin_amdgcn_sched_barrier(0)
;     ...
;         for (int t = 0; t < nt; t += 2) {
;     ...
;             PG8_LDA(At, 1, 1); PG8_STAGE(PG8_SB(1, 0), b3, voffB); PG8_STAGE(PG8_SB(1, 1), b3 + hstepB, voffB); PG8_STAGE_A(PG8_SA(1, 0), a3, 0, g2);
;             PG8_WAIT_V(8); PG8_WAIT_L(0); PG8_BAR; PG8_MMA(1, 0, At, B0); PG8_MMA(1, 1, At, B1); PG8_BAR; PG8_SCHED;
	s_add_i32 s15, s15, s52
	v_lshl_add_u64 v[194:195], v[194:195], 0, s[8:9]
	s_mov_b32 m0, s15
	ds_read_b128 v[162:165], v209 offset:49152
	ds_read_b128 v[166:169], v209 offset:50176
	ds_read_b128 v[170:173], v209 offset:51200
	ds_read_b128 v[174:177], v209 offset:52224
	ds_read_b128 v[178:181], v209 offset:53248
	ds_read_b128 v[182:185], v209 offset:54272
	ds_read_b128 v[186:189], v209 offset:55296
	ds_read_b128 v[190:193], v209 offset:56320
	global_load_lds_dwordx4 v[194:195], off
	s_add_i32 m0, s15, 0x2000
	s_add_u32 s0, s0, 0x80080
	v_lshl_add_u64 v[194:195], v[196:197], 0, s[8:9]
	s_addc_u32 s1, s1, 0
	s_add_i32 s15, s18, s52
	global_load_lds_dwordx4 v[194:195], off
	v_lshl_add_u64 v[194:195], s[0:1], 0, v[206:207]
	s_mov_b32 m0, s15
	s_nop 0
	global_load_lds_dwordx4 v[194:195], off
	v_lshl_add_u64 v[194:195], s[0:1], 0, v[216:217]
	s_add_i32 m0, s15, 0x2000
	s_nop 0
	global_load_lds_dwordx4 v[194:195], off
	v_lshl_add_u64 v[194:195], v[198:199], 0, s[8:9]
	s_mov_b32 m0, s61
	s_nop 0
	global_load_lds_dwordx4 v[194:195], off
	v_lshl_add_u64 v[194:195], v[200:201], 0, s[8:9]
	s_mov_b32 m0, s62
	s_nop 0
	global_load_lds_dwordx4 v[194:195], off
	s_waitcnt vmcnt(8)
	s_waitcnt lgkmcnt(0)
	s_barrier
	s_setprio 1
	s_waitcnt lgkmcnt(0)
	v_mfma_f32_16x16x32_bf16 v[62:65], v[122:125], v[162:165], v[62:65]
	v_mfma_f32_16x16x32_bf16 v[58:61], v[134:137], v[162:165], v[58:61]
	v_mfma_f32_16x16x32_bf16 v[50:53], v[122:125], v[170:173], v[50:53]
	v_mfma_f32_16x16x32_bf16 v[42:45], v[134:137], v[170:173], v[42:45]
	v_mfma_f32_16x16x32_bf16 v[34:37], v[122:125], v[178:181], v[34:37]
	v_mfma_f32_16x16x32_bf16 v[26:29], v[134:137], v[178:181], v[26:29]
	v_mfma_f32_16x16x32_bf16 v[18:21], v[122:125], v[186:189], v[18:21]
	v_mfma_f32_16x16x32_bf16 v[10:13], v[134:137], v[186:189], v[10:13]
	v_mfma_f32_16x16x32_bf16 v[62:65], v[126:129], v[166:169], v[62:65]
	v_mfma_f32_16x16x32_bf16 v[58:61], v[142:145], v[166:169], v[58:61]
	v_mfma_f32_16x16x32_bf16 v[50:53], v[126:129], v[174:177], v[50:53]
	v_mfma_f32_16x16x32_bf16 v[42:45], v[142:145], v[174:177], v[42:45]
	v_mfma_f32_16x16x32_bf16 v[34:37], v[126:129], v[182:185], v[34:37]
	v_mfma_f32_16x16x32_bf16 v[26:29], v[142:145], v[182:185], v[26:29]
	v_mfma_f32_16x16x32_bf16 v[18:21], v[126:129], v[190:193], v[18:21]
	v_mfma_f32_16x16x32_bf16 v[10:13], v[142:145], v[190:193], v[10:13]
	s_setprio 0
	s_setprio 1
	v_mfma_f32_16x16x32_bf16 v[54:57], v[146:149], v[162:165], v[54:57]
	v_mfma_f32_16x16x32_bf16 v[46:49], v[154:157], v[162:165], v[46:49]
	v_mfma_f32_16x16x32_bf16 v[38:41], v[146:149], v[170:173], v[38:41]
	v_mfma_f32_16x16x32_bf16 v[30:33], v[154:157], v[170:173], v[30:33]
	v_mfma_f32_16x16x32_bf16 v[22:25], v[146:149], v[178:181], v[22:25]
	v_mfma_f32_16x16x32_bf16 v[14:17], v[154:157], v[178:181], v[14:17]
	v_mfma_f32_16x16x32_bf16 v[6:9], v[146:149], v[186:189], v[6:9]
	v_mfma_f32_16x16x32_bf16 v[2:5], v[154:157], v[186:189], v[2:5]
	v_mfma_f32_16x16x32_bf16 v[54:57], v[150:153], v[166:169], v[54:57]
	v_mfma_f32_16x16x32_bf16 v[46:49], v[158:161], v[166:169], v[46:49]
	v_mfma_f32_16x16x32_bf16 v[38:41], v[150:153], v[174:177], v[38:41]
	v_mfma_f32_16x16x32_bf16 v[30:33], v[158:161], v[174:177], v[30:33]
	v_mfma_f32_16x16x32_bf16 v[22:25], v[150:153], v[182:185], v[22:25]
	v_mfma_f32_16x16x32_bf16 v[14:17], v[158:161], v[182:185], v[14:17]
	v_mfma_f32_16x16x32_bf16 v[6:9], v[150:153], v[190:193], v[6:9]
	v_mfma_f32_16x16x32_bf16 v[2:5], v[158:161], v[190:193], v[2:5]
	s_add_i32 s14, s14, 2
	s_add_u32 s24, s24, 0x100
	s_addc_u32 s25, s25, 0
	s_add_u32 s12, s12, 0x100
	s_addc_u32 s13, s13, 0
	s_cmp_gt_u32 s14, 29
	s_setprio 0
	s_barrier
	s_cbranch_scc0 .LBB0_1693
	s_and_b64 vcc, exec, s[38:39]
	s_cbranch_vccz .LBB0_1696
	s_barrier

; #define PG8_STAGE(bufoff, gbase, voff) do { _Pragma("unroll") for (int _i = 0; _i < 2; ++_i) \
;         __builtin_amdgcn_global_load_lds((const unsigned*)((const char*)(gbase) + (voff)[_i]), (LAS unsigned*)(lds + (bufoff) + ldsw + _i * 8192), 16, 0, 0); } while (0)
; #define PG8_STAGE_A(bufoff, kptr, half, VO) do { if constexpr (GATHER) { _Pragma("unroll") for (int _i = 0; _i < 2; ++_i) \
;         __builtin_amdgcn_global_load_lds((const unsigned*)((const char*)(kptr) + (VO)[half][_i]), (LAS unsigned*)(lds + (bufoff) + ldsw + _i * 8192), 16, 0, 0); } \
;         else { PG8_STAGE(bufoff, (kptr) + (half) * hstepA, voffA); } } while (0)
; #define PG8_LDA(dst, b, h) do { _Pragma("unroll") for (int m = 0; m < 4; ++m) _Pragma("unroll") for (int k = 0; k < 2; ++k) dst[m][k] = *(const LAS bf16x8*)(lds + PG8_SA(b, h) + aoff + m * 2048 + k * 1024); } while (0)
; #define PG8_LDB(dst, b, h) do { _Pragma("unroll") for (int n = 0; n < 2; ++n) _Pragma("unroll") for (int k = 0; k < 2; ++k) dst[n][k] = *(const LAS bf16x8*)(lds + PG8_SB(b, h) + boff + n * 2048 + k * 1024); } while (0)
; #define PG8_WAIT_V(n) asm volatile("s_waitcnt vmcnt(" #n ")" ::: "memory")
; #define PG8_WAIT_L(n) asm volatile("s_waitcnt lgkmcnt(" #n ")" ::: "memory")
;     ...
;         for (int t = 0; t < nt; t += 2) {
;             const bool last = (t == nt - 2);
;             const char* a1 = cA + (size_t)(t + 1) * kstep;
;             const char* a2 = last ? nA : cA + (size_t)(t + 2) * kstep; const char* b2 = last ? nB : cB + (size_t)(t + 2) * kstep;
;             const char* a3 = a2 + kstep; const char* b3 = b2 + kstep;
;             unsigned g2[2][2];
;             if constexpr (GATHER) {
; #pragma unroll
;                 for (int _h = 0; _h < 2; ++_h)
; #pragma unroll
;                     for (int _i = 0; _i < 2; ++_i) g2[_h][_i] = last ? gN[_h][_i] : gC[_h][_i]; }
;             if constexpr (SP2) {
;             PG8_LDB(B0, 0, 0); PG8_LDB(B1, 0, 1); PG8_SCHED; PG8_LDA(At, 0, 0); PG8_STAGE_A(PG8_SA(1, 1), a1, 1, gC);
;             PG8_WAIT_V(8); PG8_WAIT_L(0); PG8_BAR; PG8_MMA(0, 0, At, B0); PG8_MMA(0, 1, At, B1); PG8_BAR; PG8_SCHED;
;             PG8_LDA(At, 0, 1); PG8_STAGE(PG8_SB(0, 0), b2, voffB); PG8_STAGE(PG8_SB(0, 1), b2 + hstepB, voffB); PG8_STAGE_A(PG8_SA(0, 0), a2, 0, g2);
;             PG8_WAIT_V(8); PG8_WAIT_L(0); PG8_BAR; PG8_MMA(1, 0, At, B0); PG8_MMA(1, 1, At, B1); PG8_BAR; PG8_SCHED;
.LBB0_2265:
	s_add_u32 s0, s34, s24
	s_addc_u32 s1, s35, s25
	s_add_u32 s19, s0, 0x100
	s_addc_u32 s20, s1, 0
	s_add_u32 s21, s16, s24
	s_addc_u32 s22, s17, s25
	s_cmpk_eq_i32 s24, 0xf00
	s_cselect_b64 vcc, -1, 0
	s_and_b64 s[0:1], vcc, exec
	s_cselect_b32 s31, s12, s20
	s_cselect_b32 s30, s13, s19
	s_cselect_b32 s1, s14, s22
	s_cselect_b32 s0, s15, s21
	s_add_i32 s19, 0, 0x10000
	v_add_u32_e32 v161, s19, v139
	s_add_i32 s22, 0, 0x14000
	ds_read_b128 v[162:165], v161
	ds_read_b128 v[166:169], v161 offset:1024
	ds_read_b128 v[170:173], v161 offset:2048
	ds_read_b128 v[174:177], v161 offset:3072
	v_add_u32_e32 v161, s22, v139
	ds_read_b128 v[178:181], v161
	ds_read_b128 v[182:185], v161 offset:1024
	ds_read_b128 v[186:189], v161 offset:2048
	ds_read_b128 v[190:193], v161 offset:3072
	v_cndmask_b32_e32 v206, v138, v160, vcc
	v_cndmask_b32_e32 v212, v136, v159, vcc
	v_cndmask_b32_e32 v135, v134, v157, vcc
	v_cndmask_b32_e32 v141, v140, v158, vcc
	v_lshl_add_u64 v[214:215], v[144:145], 0, s[24:25]
	s_add_i32 m0, s57, 0xc000
	ds_read_b128 v[194:197], v156
	ds_read_b128 v[198:201], v156 offset:1024
	ds_read_b128 v[202:205], v156 offset:2048
	ds_read_b128 v[208:211], v156 offset:3072
	ds_read_b128 v[216:219], v156 offset:4096
	ds_read_b128 v[220:223], v156 offset:5120
	ds_read_b128 v[224:227], v156 offset:6144
	ds_read_b128 v[228:231], v156 offset:7168
	global_load_lds_dwordx4 v[214:215], off
	v_lshl_add_u64 v[214:215], v[142:143], 0, s[24:25]
	s_add_i32 m0, s57, 0xe000
	s_nop 0
	global_load_lds_dwordx4 v[214:215], off
	s_waitcnt vmcnt(8)
	s_waitcnt lgkmcnt(0)
	s_barrier
	s_setprio 1
	s_waitcnt lgkmcnt(0)
	v_mfma_f32_16x16x32_bf16 v[126:129], v[162:165], v[194:197], v[126:129]
	v_mfma_f32_16x16x32_bf16 v[122:125], v[170:173], v[194:197], v[122:125]
	v_mfma_f32_16x16x32_bf16 v[110:113], v[162:165], v[202:205], v[110:113]
	v_mfma_f32_16x16x32_bf16 v[106:109], v[170:173], v[202:205], v[106:109]
	v_mfma_f32_16x16x32_bf16 v[94:97], v[162:165], v[216:219], v[94:97]
	v_mfma_f32_16x16x32_bf16 v[90:93], v[170:173], v[216:219], v[90:93]
	v_mfma_f32_16x16x32_bf16 v[78:81], v[162:165], v[224:227], v[78:81]
	v_mfma_f32_16x16x32_bf16 v[74:77], v[170:173], v[224:227], v[74:77]
	v_mfma_f32_16x16x32_bf16 v[126:129], v[166:169], v[198:201], v[126:129]
	v_mfma_f32_16x16x32_bf16 v[122:125], v[174:177], v[198:201], v[122:125]
	v_mfma_f32_16x16x32_bf16 v[110:113], v[166:169], v[208:211], v[110:113]
	v_mfma_f32_16x16x32_bf16 v[106:109], v[174:177], v[208:211], v[106:109]
	v_mfma_f32_16x16x32_bf16 v[94:97], v[166:169], v[220:223], v[94:97]
	v_mfma_f32_16x16x32_bf16 v[90:93], v[174:177], v[220:223], v[90:93]
	v_mfma_f32_16x16x32_bf16 v[78:81], v[166:169], v[228:231], v[78:81]
	v_mfma_f32_16x16x32_bf16 v[74:77], v[174:177], v[228:231], v[74:77]
	s_setprio 0
	s_setprio 1
	v_mfma_f32_16x16x32_bf16 v[118:121], v[178:181], v[194:197], v[118:121]
	v_mfma_f32_16x16x32_bf16 v[114:117], v[186:189], v[194:197], v[114:117]
	v_mfma_f32_16x16x32_bf16 v[102:105], v[178:181], v[202:205], v[102:105]
	v_mfma_f32_16x16x32_bf16 v[98:101], v[186:189], v[202:205], v[98:101]
	v_mfma_f32_16x16x32_bf16 v[86:89], v[178:181], v[216:219], v[86:89]
	v_mfma_f32_16x16x32_bf16 v[82:85], v[186:189], v[216:219], v[82:85]
	v_mfma_f32_16x16x32_bf16 v[70:73], v[178:181], v[224:227], v[70:73]
	v_mfma_f32_16x16x32_bf16 v[66:69], v[186:189], v[224:227], v[66:69]
	v_mfma_f32_16x16x32_bf16 v[118:121], v[182:185], v[198:201], v[118:121]
	v_mfma_f32_16x16x32_bf16 v[114:117], v[190:193], v[198:201], v[114:117]
	v_mfma_f32_16x16x32_bf16 v[102:105], v[182:185], v[208:211], v[102:105]
	v_mfma_f32_16x16x32_bf16 v[98:101], v[190:193], v[208:211], v[98:101]
	v_mfma_f32_16x16x32_bf16 v[86:89], v[182:185], v[220:223], v[86:89]
	v_mfma_f32_16x16x32_bf16 v[82:85], v[190:193], v[220:223], v[82:85]
	v_mfma_f32_16x16x32_bf16 v[70:73], v[182:185], v[228:231], v[70:73]
	v_mfma_f32_16x16x32_bf16 v[66:69], v[190:193], v[228:231], v[66:69]
	s_setprio 0
	s_barrier
	s_add_i32 s19, s19, s56
	v_lshl_add_u64 v[214:215], s[0:1], 0, v[130:131]
	s_mov_b32 m0, s19
	ds_read_b128 v[194:197], v156 offset:16384
	ds_read_b128 v[198:201], v156 offset:17408
	ds_read_b128 v[202:205], v156 offset:18432
	ds_read_b128 v[208:211], v156 offset:19456
	ds_read_b128 v[216:219], v156 offset:20480
	ds_read_b128 v[220:223], v156 offset:21504
	ds_read_b128 v[224:227], v156 offset:22528
	ds_read_b128 v[228:231], v156 offset:23552
	global_load_lds_dwordx4 v[214:215], off
	s_add_i32 m0, s19, 0x2000
	s_add_u32 s20, s0, 0x80000
	v_lshl_add_u64 v[232:233], s[0:1], 0, v[132:133]
	s_addc_u32 s21, s1, 0
	s_add_i32 s19, s22, s56
	global_load_lds_dwordx4 v[232:233], off
	v_lshl_add_u64 v[234:235], s[20:21], 0, v[130:131]
	s_mov_b32 m0, s19
	v_mov_b32_e32 v213, v207
	global_load_lds_dwordx4 v[234:235], off
	v_lshl_add_u64 v[234:235], s[20:21], 0, v[132:133]
	s_add_i32 m0, s19, 0x2000
	s_nop 0
	global_load_lds_dwordx4 v[234:235], off
	s_mov_b32 m0, s57
	v_lshl_add_u64 v[234:235], s[30:31], 0, v[206:207]
	global_load_lds_dwordx4 v206, s[30:31]
	s_mov_b32 m0, s58
	s_nop 0
	global_load_lds_dwordx4 v212, s[30:31]
	s_waitcnt vmcnt(8)
	s_waitcnt lgkmcnt(0)
	v_lshl_add_u64 v[212:213], s[30:31], 0, v[212:213]
	s_barrier
; #define PG8_STAGE_A(bufoff, kptr, half, VO) do { if constexpr (GATHER) { _Pragma("unroll") for (int _i = 0; _i < 2; ++_i) \
;         __builtin_amdgcn_global_load_lds((const unsigned*)((const char*)(kptr) + (VO)[half][_i]), (LAS unsigned*)(lds + (bufoff) + ldsw + _i * 8192), 16, 0, 0); } \
;         else { PG8_STAGE(bufoff, (kptr) + (half) * hstepA, voffA); } } while (0)
; #define PG8_LDA(dst, b, h) do { _Pragma("unroll") for (int m = 0; m < 4; ++m) _Pragma("unroll") for (int k = 0; k < 2; ++k) dst[m][k] = *(const LAS bf16x8*)(lds + PG8_SA(b, h) + aoff + m * 2048 + k * 1024); } while (0)
; #define PG8_LDB(dst, b, h) do { _Pragma("unroll") for (int n = 0; n < 2; ++n) _Pragma("unroll") for (int k = 0; k < 2; ++k) dst[n][k] = *(const LAS bf16x8*)(lds + PG8_SB(b, h) + boff + n * 2048 + k * 1024); } while (0)
; #define PG8_MMA(ai, bj, At, Bt) do { __builtin_amdgcn_s_setprio(1); _Pragma("unroll") for (int m = 0; m < 4; ++m) _Pragma("unroll") for (int n = 0; n < 2; ++n) _Pragma("unroll") for (int k = 0; k < 2; ++k) \
;         acc[ai][bj][m][n] = __builtin_amdgcn_mfma_f32_16x16x32_bf16(Bt[n][k], At[m][k], acc[ai][bj][m][n], 0, 0, 0); __builtin_amdgcn_s_setprio(0); } while (0)
; #define PG8_WAIT_V(n) asm volatile("s_waitcnt vmcnt(" #n ")" ::: "memory")
; #define PG8_WAIT_L(n) asm volatile("s_waitcnt lgkmcnt(" #n ")" ::: "memory")
; #define PG8_BAR __builtin_amdgcn_s_barrier()
; #define PG8_SCHED __builtin_amdgcn_sched_barrier(0)
;     ...
;             PG8_WAIT_V(8); PG8_WAIT_L(0); PG8_BAR; PG8_MMA(1, 0, At, B0); PG8_MMA(1, 1, At, B1); PG8_BAR; PG8_SCHED;
;             PG8_LDB(B0, 1, 0); PG8_LDB(B1, 1, 1); PG8_SCHED; PG8_LDA(At, 1, 0); PG8_STAGE_A(PG8_SA(0, 1), a2, 1, g2);
;             PG8_WAIT_V(8); PG8_WAIT_L(0); PG8_BAR; PG8_MMA(0, 0, At, B0); PG8_MMA(0, 1, At, B1); PG8_BAR; PG8_SCHED;
	s_setprio 1
	s_waitcnt lgkmcnt(0)
	v_mfma_f32_16x16x32_bf16 v[62:65], v[162:165], v[194:197], v[62:65]
	v_mfma_f32_16x16x32_bf16 v[58:61], v[170:173], v[194:197], v[58:61]
	v_mfma_f32_16x16x32_bf16 v[46:49], v[162:165], v[202:205], v[46:49]
	v_mfma_f32_16x16x32_bf16 v[42:45], v[170:173], v[202:205], v[42:45]
	v_mfma_f32_16x16x32_bf16 v[30:33], v[162:165], v[216:219], v[30:33]
	v_mfma_f32_16x16x32_bf16 v[26:29], v[170:173], v[216:219], v[26:29]
	v_mfma_f32_16x16x32_bf16 v[14:17], v[162:165], v[224:227], v[14:17]
	v_mfma_f32_16x16x32_bf16 v[10:13], v[170:173], v[224:227], v[10:13]
	v_mfma_f32_16x16x32_bf16 v[62:65], v[166:169], v[198:201], v[62:65]
	v_mfma_f32_16x16x32_bf16 v[58:61], v[174:177], v[198:201], v[58:61]
	v_mfma_f32_16x16x32_bf16 v[46:49], v[166:169], v[208:211], v[46:49]
	v_mfma_f32_16x16x32_bf16 v[42:45], v[174:177], v[208:211], v[42:45]
	v_mfma_f32_16x16x32_bf16 v[30:33], v[166:169], v[220:223], v[30:33]
	v_mfma_f32_16x16x32_bf16 v[26:29], v[174:177], v[220:223], v[26:29]
	v_mfma_f32_16x16x32_bf16 v[14:17], v[166:169], v[228:231], v[14:17]
	v_mfma_f32_16x16x32_bf16 v[10:13], v[174:177], v[228:231], v[10:13]
	s_setprio 0
	s_setprio 1
	v_mfma_f32_16x16x32_bf16 v[54:57], v[178:181], v[194:197], v[54:57]
	v_mfma_f32_16x16x32_bf16 v[50:53], v[186:189], v[194:197], v[50:53]
	v_mfma_f32_16x16x32_bf16 v[38:41], v[178:181], v[202:205], v[38:41]
	v_mfma_f32_16x16x32_bf16 v[34:37], v[186:189], v[202:205], v[34:37]
	v_mfma_f32_16x16x32_bf16 v[22:25], v[178:181], v[216:219], v[22:25]
	v_mfma_f32_16x16x32_bf16 v[18:21], v[186:189], v[216:219], v[18:21]
	v_mfma_f32_16x16x32_bf16 v[6:9], v[178:181], v[224:227], v[6:9]
	v_mfma_f32_16x16x32_bf16 v[2:5], v[186:189], v[224:227], v[2:5]
	v_mfma_f32_16x16x32_bf16 v[54:57], v[182:185], v[198:201], v[54:57]
	v_mfma_f32_16x16x32_bf16 v[50:53], v[190:193], v[198:201], v[50:53]
	v_mfma_f32_16x16x32_bf16 v[38:41], v[182:185], v[208:211], v[38:41]
	v_mfma_f32_16x16x32_bf16 v[34:37], v[190:193], v[208:211], v[34:37]
	v_mfma_f32_16x16x32_bf16 v[22:25], v[182:185], v[220:223], v[22:25]
	v_mfma_f32_16x16x32_bf16 v[18:21], v[190:193], v[220:223], v[18:21]
	v_mfma_f32_16x16x32_bf16 v[6:9], v[182:185], v[228:231], v[6:9]
	v_mfma_f32_16x16x32_bf16 v[2:5], v[190:193], v[228:231], v[2:5]
	s_setprio 0
	s_barrier
	s_add_i32 s19, 0, 0x18000
	v_add_u32_e32 v161, s19, v139
	s_add_i32 s20, 0, 0x1c000
	ds_read_b128 v[162:165], v161
	ds_read_b128 v[166:169], v161 offset:1024
	ds_read_b128 v[170:173], v161 offset:2048
	ds_read_b128 v[174:177], v161 offset:3072
	v_add_u32_e32 v161, s20, v139
	ds_read_b128 v[178:181], v161
	ds_read_b128 v[182:185], v161 offset:1024
	ds_read_b128 v[186:189], v161 offset:2048
	ds_read_b128 v[190:193], v161 offset:3072
	s_mov_b32 m0, s59
	ds_read_b128 v[194:197], v156 offset:32768
	ds_read_b128 v[198:201], v156 offset:33792
	ds_read_b128 v[202:205], v156 offset:34816
	ds_read_b128 v[208:211], v156 offset:35840
	ds_read_b128 v[216:219], v156 offset:36864
	ds_read_b128 v[220:223], v156 offset:37888
	ds_read_b128 v[224:227], v156 offset:38912
	ds_read_b128 v[228:231], v156 offset:39936
	global_load_lds_dwordx4 v135, s[30:31]
	s_mov_b32 m0, s60
	s_nop 0
	global_load_lds_dwordx4 v141, s[30:31]
	s_waitcnt vmcnt(8)
	s_waitcnt lgkmcnt(0)
	s_barrier
	s_setprio 1
	s_waitcnt lgkmcnt(0)
	v_mfma_f32_16x16x32_bf16 v[126:129], v[162:165], v[194:197], v[126:129]
	v_mfma_f32_16x16x32_bf16 v[122:125], v[170:173], v[194:197], v[122:125]
	v_mfma_f32_16x16x32_bf16 v[110:113], v[162:165], v[202:205], v[110:113]
	v_mfma_f32_16x16x32_bf16 v[106:109], v[170:173], v[202:205], v[106:109]
	v_mfma_f32_16x16x32_bf16 v[94:97], v[162:165], v[216:219], v[94:97]
	v_mfma_f32_16x16x32_bf16 v[90:93], v[170:173], v[216:219], v[90:93]
	v_mfma_f32_16x16x32_bf16 v[78:81], v[162:165], v[224:227], v[78:81]
	v_mfma_f32_16x16x32_bf16 v[74:77], v[170:173], v[224:227], v[74:77]
	v_mfma_f32_16x16x32_bf16 v[126:129], v[166:169], v[198:201], v[126:129]
	v_mfma_f32_16x16x32_bf16 v[122:125], v[174:177], v[198:201], v[122:125]
	v_mfma_f32_16x16x32_bf16 v[110:113], v[166:169], v[208:211], v[110:113]
	v_mfma_f32_16x16x32_bf16 v[106:109], v[174:177], v[208:211], v[106:109]
	v_mfma_f32_16x16x32_bf16 v[94:97], v[166:169], v[220:223], v[94:97]
	v_mfma_f32_16x16x32_bf16 v[90:93], v[174:177], v[220:223], v[90:93]
	v_mfma_f32_16x16x32_bf16 v[78:81], v[166:169], v[228:231], v[78:81]
	v_mfma_f32_16x16x32_bf16 v[74:77], v[174:177], v[228:231], v[74:77]
	s_setprio 0
	s_setprio 1
	v_mfma_f32_16x16x32_bf16 v[118:121], v[178:181], v[194:197], v[118:121]
	v_mfma_f32_16x16x32_bf16 v[114:117], v[186:189], v[194:197], v[114:117]
	v_mfma_f32_16x16x32_bf16 v[102:105], v[178:181], v[202:205], v[102:105]
	v_mfma_f32_16x16x32_bf16 v[98:101], v[186:189], v[202:205], v[98:101]
	v_mfma_f32_16x16x32_bf16 v[86:89], v[178:181], v[216:219], v[86:89]
	v_mfma_f32_16x16x32_bf16 v[82:85], v[186:189], v[216:219], v[82:85]
	v_mfma_f32_16x16x32_bf16 v[70:73], v[178:181], v[224:227], v[70:73]
	v_mfma_f32_16x16x32_bf16 v[66:69], v[186:189], v[224:227], v[66:69]
	v_mfma_f32_16x16x32_bf16 v[118:121], v[182:185], v[198:201], v[118:121]
	v_mfma_f32_16x16x32_bf16 v[114:117], v[190:193], v[198:201], v[114:117]
	v_mfma_f32_16x16x32_bf16 v[102:105], v[182:185], v[208:211], v[102:105]
	v_mfma_f32_16x16x32_bf16 v[98:101], v[190:193], v[208:211], v[98:101]
	v_mfma_f32_16x16x32_bf16 v[86:89], v[182:185], v[220:223], v[86:89]
	v_mfma_f32_16x16x32_bf16 v[82:85], v[190:193], v[220:223], v[82:85]
	v_mfma_f32_16x16x32_bf16 v[70:73], v[182:185], v[228:231], v[70:73]
	v_mfma_f32_16x16x32_bf16 v[66:69], v[190:193], v[228:231], v[66:69]
	s_setprio 0
	s_barrier
; #define PG8_STAGE(bufoff, gbase, voff) do { _Pragma("unroll") for (int _i = 0; _i < 2; ++_i) \
;         __builtin_amdgcn_global_load_lds((const unsigned*)((const char*)(gbase) + (voff)[_i]), (LAS unsigned*)(lds + (bufoff) + ldsw + _i * 8192), 16, 0, 0); } while (0)
; #define PG8_STAGE_A(bufoff, kptr, half, VO) do { if constexpr (GATHER) { _Pragma("unroll") for (int _i = 0; _i < 2; ++_i) \
;         __builtin_amdgcn_global_load_lds((const unsigned*)((const char*)(kptr) + (VO)[half][_i]), (LAS unsigned*)(lds + (bufoff) + ldsw + _i * 8192), 16, 0, 0); } \
;         else { PG8_STAGE(bufoff, (kptr) + (half) * hstepA, voffA); } } while (0)
; #define PG8_LDA(dst, b, h) do { _Pragma("unroll") for (int m = 0; m < 4; ++m) _Pragma("unroll") for (int k = 0; k < 2; ++k) dst[m][k] = *(const LAS bf16x8*)(lds + PG8_SA(b, h) + aoff + m * 2048 + k * 1024); } while (0)
; #define PG8_MMA(ai, bj, At, Bt) do { __builtin_amdgcn_s_setprio(1); _Pragma("unroll") for (int m = 0; m < 4; ++m) _Pragma("unroll") for (int n = 0; n < 2; ++n) _Pragma("unroll") for (int k = 0; k < 2; ++k) \
;         acc[ai][bj][m][n] = __builtin_amdgcn_mfma_f32_16x16x32_bf16(Bt[n][k], At[m][k], acc[ai][bj][m][n], 0, 0, 0); __builtin_amdgcn_s_setprio(0); } while (0)
; #define PG8_WAIT_V(n) asm volatile("s_waitcnt vmcnt(" #n ")" ::: "memory")
; #define PG8_WAIT_L(n) asm volatile("s_waitcnt lgkmcnt(" #n ")" ::: "memory")
; #define PG8_BAR __builtin_amdgcn_s_barrier()
; #define PG8_SCHED __builtin_amdgcn_sched_barrier(0)
;     ...
;         for (int t = 0; t < nt; t += 2) {
;             const bool last = (t == nt - 2);
;     ...
;             PG8_LDA(At, 1, 1); PG8_STAGE(PG8_SB(1, 0), b3, voffB); PG8_STAGE(PG8_SB(1, 1), b3 + hstepB, voffB); PG8_STAGE_A(PG8_SA(1, 0), a3, 0, g2);
;             PG8_WAIT_V(8); PG8_WAIT_L(0); PG8_BAR; PG8_MMA(1, 0, At, B0); PG8_MMA(1, 1, At, B1); PG8_BAR; PG8_SCHED;
	s_add_i32 s19, s19, s56
	v_lshl_add_u64 v[214:215], v[214:215], 0, s[8:9]
	s_mov_b32 m0, s19
	ds_read_b128 v[194:197], v156 offset:49152
	ds_read_b128 v[198:201], v156 offset:50176
	ds_read_b128 v[202:205], v156 offset:51200
	ds_read_b128 v[208:211], v156 offset:52224
	ds_read_b128 v[216:219], v156 offset:53248
	ds_read_b128 v[220:223], v156 offset:54272
	ds_read_b128 v[224:227], v156 offset:55296
	ds_read_b128 v[228:231], v156 offset:56320
	global_load_lds_dwordx4 v[214:215], off
	s_add_i32 m0, s19, 0x2000
	s_add_u32 s0, s0, 0x80080
	v_lshl_add_u64 v[214:215], v[232:233], 0, s[8:9]
	s_addc_u32 s1, s1, 0
	s_add_i32 s19, s20, s56
	global_load_lds_dwordx4 v[214:215], off
	v_lshl_add_u64 v[214:215], s[0:1], 0, v[130:131]
	s_mov_b32 m0, s19
	v_lshl_add_u64 v[212:213], v[212:213], 0, s[8:9]
	global_load_lds_dwordx4 v[214:215], off
	v_lshl_add_u64 v[214:215], s[0:1], 0, v[132:133]
	s_add_i32 m0, s19, 0x2000
	s_nop 0
	global_load_lds_dwordx4 v[214:215], off
	v_lshl_add_u64 v[214:215], v[234:235], 0, s[8:9]
	s_mov_b32 m0, s63
	s_nop 0
	global_load_lds_dwordx4 v[214:215], off
	s_mov_b32 m0, s64
	s_nop 0
	global_load_lds_dwordx4 v[212:213], off
	s_waitcnt vmcnt(8)
	s_waitcnt lgkmcnt(0)
	s_barrier
	s_setprio 1
	s_waitcnt lgkmcnt(0)
	v_mfma_f32_16x16x32_bf16 v[62:65], v[162:165], v[194:197], v[62:65]
	v_mfma_f32_16x16x32_bf16 v[58:61], v[170:173], v[194:197], v[58:61]
	v_mfma_f32_16x16x32_bf16 v[46:49], v[162:165], v[202:205], v[46:49]
	v_mfma_f32_16x16x32_bf16 v[42:45], v[170:173], v[202:205], v[42:45]
	v_mfma_f32_16x16x32_bf16 v[30:33], v[162:165], v[216:219], v[30:33]
	v_mfma_f32_16x16x32_bf16 v[26:29], v[170:173], v[216:219], v[26:29]
	v_mfma_f32_16x16x32_bf16 v[14:17], v[162:165], v[224:227], v[14:17]
	v_mfma_f32_16x16x32_bf16 v[10:13], v[170:173], v[224:227], v[10:13]
	v_mfma_f32_16x16x32_bf16 v[62:65], v[166:169], v[198:201], v[62:65]
	v_mfma_f32_16x16x32_bf16 v[58:61], v[174:177], v[198:201], v[58:61]
	v_mfma_f32_16x16x32_bf16 v[46:49], v[166:169], v[208:211], v[46:49]
	v_mfma_f32_16x16x32_bf16 v[42:45], v[174:177], v[208:211], v[42:45]
	v_mfma_f32_16x16x32_bf16 v[30:33], v[166:169], v[220:223], v[30:33]
	v_mfma_f32_16x16x32_bf16 v[26:29], v[174:177], v[220:223], v[26:29]
	v_mfma_f32_16x16x32_bf16 v[14:17], v[166:169], v[228:231], v[14:17]
	v_mfma_f32_16x16x32_bf16 v[10:13], v[174:177], v[228:231], v[10:13]
	s_setprio 0
	s_setprio 1
	v_mfma_f32_16x16x32_bf16 v[54:57], v[178:181], v[194:197], v[54:57]
	v_mfma_f32_16x16x32_bf16 v[50:53], v[186:189], v[194:197], v[50:53]
	v_mfma_f32_16x16x32_bf16 v[38:41], v[178:181], v[202:205], v[38:41]
	v_mfma_f32_16x16x32_bf16 v[34:37], v[186:189], v[202:205], v[34:37]
	v_mfma_f32_16x16x32_bf16 v[22:25], v[178:181], v[216:219], v[22:25]
	v_mfma_f32_16x16x32_bf16 v[18:21], v[186:189], v[216:219], v[18:21]
	v_mfma_f32_16x16x32_bf16 v[6:9], v[178:181], v[224:227], v[6:9]
	v_mfma_f32_16x16x32_bf16 v[2:5], v[186:189], v[224:227], v[2:5]
	v_mfma_f32_16x16x32_bf16 v[54:57], v[182:185], v[198:201], v[54:57]
	v_mfma_f32_16x16x32_bf16 v[50:53], v[190:193], v[198:201], v[50:53]
	v_mfma_f32_16x16x32_bf16 v[38:41], v[182:185], v[208:211], v[38:41]
	v_mfma_f32_16x16x32_bf16 v[34:37], v[190:193], v[208:211], v[34:37]
	v_mfma_f32_16x16x32_bf16 v[22:25], v[182:185], v[220:223], v[22:25]
	v_mfma_f32_16x16x32_bf16 v[18:21], v[190:193], v[220:223], v[18:21]
	v_mfma_f32_16x16x32_bf16 v[6:9], v[182:185], v[228:231], v[6:9]
	v_mfma_f32_16x16x32_bf16 v[2:5], v[190:193], v[228:231], v[2:5]
	s_add_i32 s18, s18, 2
	s_add_u32 s24, s24, 0x100
	s_addc_u32 s25, s25, 0
	s_cmp_gt_u32 s18, 29
	s_setprio 0
	s_barrier
	s_cbranch_scc0 .LBB0_2265
	s_and_b64 vcc, exec, s[42:43]
	s_cbranch_vccz .LBB0_2268
	s_barrier

; #define PG8_STAGE(bufoff, gbase, voff) do { _Pragma("unroll") for (int _i = 0; _i < 2; ++_i) \
;         __builtin_amdgcn_global_load_lds((const unsigned*)((const char*)(gbase) + (voff)[_i]), (LAS unsigned*)(lds + (bufoff) + ldsw + _i * 8192), 16, 0, 0); } while (0)
; #define PG8_STAGE_A(bufoff, kptr, half, VO) do { if constexpr (GATHER) { _Pragma("unroll") for (int _i = 0; _i < 2; ++_i) \
;         __builtin_amdgcn_global_load_lds((const unsigned*)((const char*)(kptr) + (VO)[half][_i]), (LAS unsigned*)(lds + (bufoff) + ldsw + _i * 8192), 16, 0, 0); } \
;         else { PG8_STAGE(bufoff, (kptr) + (half) * hstepA, voffA); } } while (0)
; #define PG8_LDA(dst, b, h) do { _Pragma("unroll") for (int m = 0; m < 4; ++m) _Pragma("unroll") for (int k = 0; k < 2; ++k) dst[m][k] = *(const LAS bf16x8*)(lds + PG8_SA(b, h) + aoff + m * 2048 + k * 1024); } while (0)
; #define PG8_LDB(dst, b, h) do { _Pragma("unroll") for (int n = 0; n < 2; ++n) _Pragma("unroll") for (int k = 0; k < 2; ++k) dst[n][k] = *(const LAS bf16x8*)(lds + PG8_SB(b, h) + boff + n * 2048 + k * 1024); } while (0)
; #define PG8_MMA(ai, bj, At, Bt) do { __builtin_amdgcn_s_setprio(1); _Pragma("unroll") for (int m = 0; m < 4; ++m) _Pragma("unroll") for (int n = 0; n < 2; ++n) _Pragma("unroll") for (int k = 0; k < 2; ++k) \
;         acc[ai][bj][m][n] = __builtin_amdgcn_mfma_f32_16x16x32_bf16(Bt[n][k], At[m][k], acc[ai][bj][m][n], 0, 0, 0); __builtin_amdgcn_s_setprio(0); } while (0)
; #define PG8_WAIT_V(n) asm volatile("s_waitcnt vmcnt(" #n ")" ::: "memory")
; #define PG8_WAIT_L(n) asm volatile("s_waitcnt lgkmcnt(" #n ")" ::: "memory")
; #define PG8_BAR __builtin_amdgcn_s_barrier()
; #define PG8_SCHED __builtin_amdgcn_sched_barrier(0)
;     ...
;             PG8_LDB(B0, 0, 0); PG8_LDB(B1, 0, 1); PG8_SCHED; PG8_LDA(At, 0, 0); PG8_STAGE_A(PG8_SA(1, 1), a1, 1, gC);
;             PG8_WAIT_V(8); PG8_WAIT_L(0); PG8_BAR; PG8_MMA(0, 0, At, B0); PG8_MMA(0, 1, At, B1); PG8_BAR; PG8_SCHED;
;             PG8_LDA(At, 0, 1); PG8_STAGE(PG8_SB(0, 0), b2, voffB); PG8_STAGE(PG8_SB(0, 1), b2 + hstepB, voffB); PG8_STAGE_A(PG8_SA(0, 0), a2, 0, g2);
;             PG8_WAIT_V(8); PG8_WAIT_L(0); PG8_BAR; PG8_MMA(1, 0, At, B0); PG8_MMA(1, 1, At, B1); PG8_BAR; PG8_SCHED;
.LBB0_2458:
	s_add_u32 s0, s24, 0xfffc0080
	s_addc_u32 s1, s25, -1
	s_add_i32 s19, 0, 0x10000
	s_cmp_eq_u32 s18, 12
	s_cselect_b32 s31, s12, s1
	s_cselect_b32 s30, s13, s0
	v_add_u32_e32 v140, s19, v145
	s_cselect_b32 s1, s14, s17
	s_cselect_b32 s0, s15, s16
	s_add_i32 s22, 0, 0x14000
	ds_read_b128 v[156:159], v140
	ds_read_b128 v[160:163], v140 offset:1024
	ds_read_b128 v[164:167], v140 offset:2048
	ds_read_b128 v[168:171], v140 offset:3072
	v_add_u32_e32 v140, s22, v145
	ds_read_b128 v[172:175], v140
	ds_read_b128 v[176:179], v140 offset:1024
	ds_read_b128 v[180:183], v140 offset:2048
	ds_read_b128 v[184:187], v140 offset:3072
	v_lshl_add_u64 v[142:143], s[24:25], 0, v[136:137]
	s_add_i32 m0, s37, 0xc000
	ds_read_b128 v[188:191], v155
	ds_read_b128 v[192:195], v155 offset:1024
	ds_read_b128 v[196:199], v155 offset:2048
	ds_read_b128 v[200:203], v155 offset:3072
	ds_read_b128 v[208:211], v155 offset:4096
	ds_read_b128 v[216:219], v155 offset:5120
	ds_read_b128 v[220:223], v155 offset:6144
	ds_read_b128 v[224:227], v155 offset:7168
	global_load_lds_dwordx4 v[142:143], off
	v_lshl_add_u64 v[142:143], s[24:25], 0, v[138:139]
	s_add_i32 m0, s37, 0xe000
	s_nop 0
	global_load_lds_dwordx4 v[142:143], off
	s_waitcnt vmcnt(8)
	s_waitcnt lgkmcnt(0)
	s_barrier
	s_setprio 1
	s_waitcnt lgkmcnt(0)
	v_mfma_f32_16x16x32_bf16 v[126:129], v[156:159], v[188:191], v[126:129]
	v_mfma_f32_16x16x32_bf16 v[122:125], v[164:167], v[188:191], v[122:125]
	v_mfma_f32_16x16x32_bf16 v[110:113], v[156:159], v[196:199], v[110:113]
	v_mfma_f32_16x16x32_bf16 v[106:109], v[164:167], v[196:199], v[106:109]
	v_mfma_f32_16x16x32_bf16 v[94:97], v[156:159], v[208:211], v[94:97]
	v_mfma_f32_16x16x32_bf16 v[90:93], v[164:167], v[208:211], v[90:93]
	v_mfma_f32_16x16x32_bf16 v[86:89], v[156:159], v[220:223], v[86:89]
	v_mfma_f32_16x16x32_bf16 v[78:81], v[164:167], v[220:223], v[78:81]
	v_mfma_f32_16x16x32_bf16 v[126:129], v[160:163], v[192:195], v[126:129]
	v_mfma_f32_16x16x32_bf16 v[122:125], v[168:171], v[192:195], v[122:125]
	v_mfma_f32_16x16x32_bf16 v[110:113], v[160:163], v[200:203], v[110:113]
	v_mfma_f32_16x16x32_bf16 v[106:109], v[168:171], v[200:203], v[106:109]
	v_mfma_f32_16x16x32_bf16 v[94:97], v[160:163], v[216:219], v[94:97]
	v_mfma_f32_16x16x32_bf16 v[90:93], v[168:171], v[216:219], v[90:93]
	v_mfma_f32_16x16x32_bf16 v[86:89], v[160:163], v[224:227], v[86:89]
	v_mfma_f32_16x16x32_bf16 v[78:81], v[168:171], v[224:227], v[78:81]
	s_setprio 0
	s_setprio 1
	v_mfma_f32_16x16x32_bf16 v[118:121], v[172:175], v[188:191], v[118:121]
	v_mfma_f32_16x16x32_bf16 v[114:117], v[180:183], v[188:191], v[114:117]
	v_mfma_f32_16x16x32_bf16 v[102:105], v[172:175], v[196:199], v[102:105]
	v_mfma_f32_16x16x32_bf16 v[98:101], v[180:183], v[196:199], v[98:101]
	v_mfma_f32_16x16x32_bf16 v[82:85], v[172:175], v[208:211], v[82:85]
	v_mfma_f32_16x16x32_bf16 v[74:77], v[180:183], v[208:211], v[74:77]
	v_mfma_f32_16x16x32_bf16 v[70:73], v[172:175], v[220:223], v[70:73]
	v_mfma_f32_16x16x32_bf16 v[66:69], v[180:183], v[220:223], v[66:69]
	v_mfma_f32_16x16x32_bf16 v[118:121], v[176:179], v[192:195], v[118:121]
	v_mfma_f32_16x16x32_bf16 v[114:117], v[184:187], v[192:195], v[114:117]
	v_mfma_f32_16x16x32_bf16 v[102:105], v[176:179], v[200:203], v[102:105]
	v_mfma_f32_16x16x32_bf16 v[98:101], v[184:187], v[200:203], v[98:101]
	v_mfma_f32_16x16x32_bf16 v[82:85], v[176:179], v[216:219], v[82:85]
	v_mfma_f32_16x16x32_bf16 v[74:77], v[184:187], v[216:219], v[74:77]
	v_mfma_f32_16x16x32_bf16 v[70:73], v[176:179], v[224:227], v[70:73]
	v_mfma_f32_16x16x32_bf16 v[66:69], v[184:187], v[224:227], v[66:69]
	s_setprio 0
	s_barrier
	s_add_i32 s19, s19, s62
	v_lshl_add_u64 v[142:143], s[0:1], 0, v[206:207]
	s_mov_b32 m0, s19
	ds_read_b128 v[188:191], v155 offset:16384
	ds_read_b128 v[192:195], v155 offset:17408
	ds_read_b128 v[196:199], v155 offset:18432
	ds_read_b128 v[200:203], v155 offset:19456
	ds_read_b128 v[208:211], v155 offset:20480
	ds_read_b128 v[216:219], v155 offset:21504
	ds_read_b128 v[220:223], v155 offset:22528
	ds_read_b128 v[224:227], v155 offset:23552
	global_load_lds_dwordx4 v[142:143], off
	s_add_i32 m0, s19, 0x2000
	s_add_u32 s20, s0, 0x40000
	v_lshl_add_u64 v[204:205], s[0:1], 0, v[134:135]
	s_addc_u32 s21, s1, 0
	s_add_i32 s19, s22, s62
	global_load_lds_dwordx4 v[204:205], off
	v_lshl_add_u64 v[212:213], s[20:21], 0, v[206:207]
	s_mov_b32 m0, s19
	v_lshl_add_u64 v[214:215], s[30:31], 0, v[132:133]
	global_load_lds_dwordx4 v[212:213], off
	v_lshl_add_u64 v[212:213], s[20:21], 0, v[134:135]
	s_add_i32 m0, s19, 0x2000
	s_nop 0
	global_load_lds_dwordx4 v[212:213], off
	v_lshl_add_u64 v[212:213], s[30:31], 0, v[130:131]
	s_mov_b32 m0, s37
	s_nop 0
	global_load_lds_dwordx4 v[212:213], off
	s_mov_b32 m0, s65
	s_nop 0
	global_load_lds_dwordx4 v[214:215], off
	s_waitcnt vmcnt(8)
	s_waitcnt lgkmcnt(0)
	s_barrier
; #define PG8_STAGE_A(bufoff, kptr, half, VO) do { if constexpr (GATHER) { _Pragma("unroll") for (int _i = 0; _i < 2; ++_i) \
;         __builtin_amdgcn_global_load_lds((const unsigned*)((const char*)(kptr) + (VO)[half][_i]), (LAS unsigned*)(lds + (bufoff) + ldsw + _i * 8192), 16, 0, 0); } \
;         else { PG8_STAGE(bufoff, (kptr) + (half) * hstepA, voffA); } } while (0)
; #define PG8_LDA(dst, b, h) do { _Pragma("unroll") for (int m = 0; m < 4; ++m) _Pragma("unroll") for (int k = 0; k < 2; ++k) dst[m][k] = *(const LAS bf16x8*)(lds + PG8_SA(b, h) + aoff + m * 2048 + k * 1024); } while (0)
; #define PG8_LDB(dst, b, h) do { _Pragma("unroll") for (int n = 0; n < 2; ++n) _Pragma("unroll") for (int k = 0; k < 2; ++k) dst[n][k] = *(const LAS bf16x8*)(lds + PG8_SB(b, h) + boff + n * 2048 + k * 1024); } while (0)
; #define PG8_MMA(ai, bj, At, Bt) do { __builtin_amdgcn_s_setprio(1); _Pragma("unroll") for (int m = 0; m < 4; ++m) _Pragma("unroll") for (int n = 0; n < 2; ++n) _Pragma("unroll") for (int k = 0; k < 2; ++k) \
;         acc[ai][bj][m][n] = __builtin_amdgcn_mfma_f32_16x16x32_bf16(Bt[n][k], At[m][k], acc[ai][bj][m][n], 0, 0, 0); __builtin_amdgcn_s_setprio(0); } while (0)
; #define PG8_WAIT_V(n) asm volatile("s_waitcnt vmcnt(" #n ")" ::: "memory")
; #define PG8_WAIT_L(n) asm volatile("s_waitcnt lgkmcnt(" #n ")" ::: "memory")
; #define PG8_BAR __builtin_amdgcn_s_barrier()
; #define PG8_SCHED __builtin_amdgcn_sched_barrier(0)
;     ...
;             PG8_WAIT_V(8); PG8_WAIT_L(0); PG8_BAR; PG8_MMA(1, 0, At, B0); PG8_MMA(1, 1, At, B1); PG8_BAR; PG8_SCHED;
;             PG8_LDB(B0, 1, 0); PG8_LDB(B1, 1, 1); PG8_SCHED; PG8_LDA(At, 1, 0); PG8_STAGE_A(PG8_SA(0, 1), a2, 1, g2);
;             PG8_WAIT_V(8); PG8_WAIT_L(0); PG8_BAR; PG8_MMA(0, 0, At, B0); PG8_MMA(0, 1, At, B1); PG8_BAR; PG8_SCHED;
	s_setprio 1
	s_waitcnt lgkmcnt(0)
	v_mfma_f32_16x16x32_bf16 v[62:65], v[156:159], v[188:191], v[62:65]
	v_mfma_f32_16x16x32_bf16 v[58:61], v[164:167], v[188:191], v[58:61]
	v_mfma_f32_16x16x32_bf16 v[54:57], v[156:159], v[196:199], v[54:57]
	v_mfma_f32_16x16x32_bf16 v[46:49], v[164:167], v[196:199], v[46:49]
	v_mfma_f32_16x16x32_bf16 v[38:41], v[156:159], v[208:211], v[38:41]
	v_mfma_f32_16x16x32_bf16 v[30:33], v[164:167], v[208:211], v[30:33]
	v_mfma_f32_16x16x32_bf16 v[22:25], v[156:159], v[220:223], v[22:25]
	v_mfma_f32_16x16x32_bf16 v[14:17], v[164:167], v[220:223], v[14:17]
	v_mfma_f32_16x16x32_bf16 v[62:65], v[160:163], v[192:195], v[62:65]
	v_mfma_f32_16x16x32_bf16 v[58:61], v[168:171], v[192:195], v[58:61]
	v_mfma_f32_16x16x32_bf16 v[54:57], v[160:163], v[200:203], v[54:57]
	v_mfma_f32_16x16x32_bf16 v[46:49], v[168:171], v[200:203], v[46:49]
	v_mfma_f32_16x16x32_bf16 v[38:41], v[160:163], v[216:219], v[38:41]
	v_mfma_f32_16x16x32_bf16 v[30:33], v[168:171], v[216:219], v[30:33]
	v_mfma_f32_16x16x32_bf16 v[22:25], v[160:163], v[224:227], v[22:25]
	v_mfma_f32_16x16x32_bf16 v[14:17], v[168:171], v[224:227], v[14:17]
	s_setprio 0
	s_setprio 1
	v_mfma_f32_16x16x32_bf16 v[50:53], v[172:175], v[188:191], v[50:53]
	v_mfma_f32_16x16x32_bf16 v[42:45], v[180:183], v[188:191], v[42:45]
	v_mfma_f32_16x16x32_bf16 v[34:37], v[172:175], v[196:199], v[34:37]
	v_mfma_f32_16x16x32_bf16 v[26:29], v[180:183], v[196:199], v[26:29]
	v_mfma_f32_16x16x32_bf16 v[18:21], v[172:175], v[208:211], v[18:21]
	v_mfma_f32_16x16x32_bf16 v[10:13], v[180:183], v[208:211], v[10:13]
	v_mfma_f32_16x16x32_bf16 v[6:9], v[172:175], v[220:223], v[6:9]
	v_mfma_f32_16x16x32_bf16 v[2:5], v[180:183], v[220:223], v[2:5]
	v_mfma_f32_16x16x32_bf16 v[50:53], v[176:179], v[192:195], v[50:53]
	v_mfma_f32_16x16x32_bf16 v[42:45], v[184:187], v[192:195], v[42:45]
	v_mfma_f32_16x16x32_bf16 v[34:37], v[176:179], v[200:203], v[34:37]
	v_mfma_f32_16x16x32_bf16 v[26:29], v[184:187], v[200:203], v[26:29]
	v_mfma_f32_16x16x32_bf16 v[18:21], v[176:179], v[216:219], v[18:21]
	v_mfma_f32_16x16x32_bf16 v[10:13], v[184:187], v[216:219], v[10:13]
	v_mfma_f32_16x16x32_bf16 v[6:9], v[176:179], v[224:227], v[6:9]
	v_mfma_f32_16x16x32_bf16 v[2:5], v[184:187], v[224:227], v[2:5]
	s_setprio 0
	s_barrier
	s_add_i32 s19, 0, 0x18000
	v_add_u32_e32 v140, s19, v145
	s_add_i32 s22, 0, 0x1c000
	ds_read_b128 v[156:159], v140
	ds_read_b128 v[160:163], v140 offset:1024
	ds_read_b128 v[164:167], v140 offset:2048
	ds_read_b128 v[168:171], v140 offset:3072
	v_add_u32_e32 v140, s22, v145
	ds_read_b128 v[172:175], v140
	ds_read_b128 v[176:179], v140 offset:1024
	ds_read_b128 v[180:183], v140 offset:2048
	ds_read_b128 v[184:187], v140 offset:3072
	s_add_u32 s20, s30, 0x40000
	s_addc_u32 s21, s31, 0
	s_mov_b32 m0, s66
	v_lshl_add_u64 v[228:229], s[20:21], 0, v[130:131]
	ds_read_b128 v[188:191], v155 offset:32768
	ds_read_b128 v[192:195], v155 offset:33792
	ds_read_b128 v[196:199], v155 offset:34816
	ds_read_b128 v[200:203], v155 offset:35840
	ds_read_b128 v[208:211], v155 offset:36864
	ds_read_b128 v[216:219], v155 offset:37888
	ds_read_b128 v[220:223], v155 offset:38912
	ds_read_b128 v[224:227], v155 offset:39936
	global_load_lds_dwordx4 v[228:229], off
	v_lshl_add_u64 v[228:229], s[20:21], 0, v[132:133]
	s_mov_b32 m0, s67
	s_nop 0
	global_load_lds_dwordx4 v[228:229], off
	s_waitcnt vmcnt(8)
	s_waitcnt lgkmcnt(0)
	s_barrier
	s_setprio 1
	s_waitcnt lgkmcnt(0)
	v_mfma_f32_16x16x32_bf16 v[126:129], v[156:159], v[188:191], v[126:129]
	v_mfma_f32_16x16x32_bf16 v[122:125], v[164:167], v[188:191], v[122:125]
	v_mfma_f32_16x16x32_bf16 v[110:113], v[156:159], v[196:199], v[110:113]
	v_mfma_f32_16x16x32_bf16 v[106:109], v[164:167], v[196:199], v[106:109]
	v_mfma_f32_16x16x32_bf16 v[94:97], v[156:159], v[208:211], v[94:97]
	v_mfma_f32_16x16x32_bf16 v[90:93], v[164:167], v[208:211], v[90:93]
	v_mfma_f32_16x16x32_bf16 v[86:89], v[156:159], v[220:223], v[86:89]
	v_mfma_f32_16x16x32_bf16 v[78:81], v[164:167], v[220:223], v[78:81]
	v_mfma_f32_16x16x32_bf16 v[126:129], v[160:163], v[192:195], v[126:129]
	v_mfma_f32_16x16x32_bf16 v[122:125], v[168:171], v[192:195], v[122:125]
	v_mfma_f32_16x16x32_bf16 v[110:113], v[160:163], v[200:203], v[110:113]
	v_mfma_f32_16x16x32_bf16 v[106:109], v[168:171], v[200:203], v[106:109]
	v_mfma_f32_16x16x32_bf16 v[94:97], v[160:163], v[216:219], v[94:97]
	v_mfma_f32_16x16x32_bf16 v[90:93], v[168:171], v[216:219], v[90:93]
	v_mfma_f32_16x16x32_bf16 v[86:89], v[160:163], v[224:227], v[86:89]
	v_mfma_f32_16x16x32_bf16 v[78:81], v[168:171], v[224:227], v[78:81]
	s_setprio 0
	s_setprio 1
	v_mfma_f32_16x16x32_bf16 v[118:121], v[172:175], v[188:191], v[118:121]
	v_mfma_f32_16x16x32_bf16 v[114:117], v[180:183], v[188:191], v[114:117]
	v_mfma_f32_16x16x32_bf16 v[102:105], v[172:175], v[196:199], v[102:105]
	v_mfma_f32_16x16x32_bf16 v[98:101], v[180:183], v[196:199], v[98:101]
	v_mfma_f32_16x16x32_bf16 v[82:85], v[172:175], v[208:211], v[82:85]
	v_mfma_f32_16x16x32_bf16 v[74:77], v[180:183], v[208:211], v[74:77]
	v_mfma_f32_16x16x32_bf16 v[70:73], v[172:175], v[220:223], v[70:73]
	v_mfma_f32_16x16x32_bf16 v[66:69], v[180:183], v[220:223], v[66:69]
	v_mfma_f32_16x16x32_bf16 v[118:121], v[176:179], v[192:195], v[118:121]
	v_mfma_f32_16x16x32_bf16 v[114:117], v[184:187], v[192:195], v[114:117]
	v_mfma_f32_16x16x32_bf16 v[102:105], v[176:179], v[200:203], v[102:105]
	v_mfma_f32_16x16x32_bf16 v[98:101], v[184:187], v[200:203], v[98:101]
	v_mfma_f32_16x16x32_bf16 v[82:85], v[176:179], v[216:219], v[82:85]
	v_mfma_f32_16x16x32_bf16 v[74:77], v[184:187], v[216:219], v[74:77]
	v_mfma_f32_16x16x32_bf16 v[70:73], v[176:179], v[224:227], v[70:73]
	v_mfma_f32_16x16x32_bf16 v[66:69], v[184:187], v[224:227], v[66:69]
	s_setprio 0
	s_barrier
; #define PG8_STAGE(bufoff, gbase, voff) do { _Pragma("unroll") for (int _i = 0; _i < 2; ++_i) \
;         __builtin_amdgcn_global_load_lds((const unsigned*)((const char*)(gbase) + (voff)[_i]), (LAS unsigned*)(lds + (bufoff) + ldsw + _i * 8192), 16, 0, 0); } while (0)
; #define PG8_STAGE_A(bufoff, kptr, half, VO) do { if constexpr (GATHER) { _Pragma("unroll") for (int _i = 0; _i < 2; ++_i) \
;         __builtin_amdgcn_global_load_lds((const unsigned*)((const char*)(kptr) + (VO)[half][_i]), (LAS unsigned*)(lds + (bufoff) + ldsw + _i * 8192), 16, 0, 0); } \
;         else { PG8_STAGE(bufoff, (kptr) + (half) * hstepA, voffA); } } while (0)
; #define PG8_LDA(dst, b, h) do { _Pragma("unroll") for (int m = 0; m < 4; ++m) _Pragma("unroll") for (int k = 0; k < 2; ++k) dst[m][k] = *(const LAS bf16x8*)(lds + PG8_SA(b, h) + aoff + m * 2048 + k * 1024); } while (0)
; #define PG8_MMA(ai, bj, At, Bt) do { __builtin_amdgcn_s_setprio(1); _Pragma("unroll") for (int m = 0; m < 4; ++m) _Pragma("unroll") for (int n = 0; n < 2; ++n) _Pragma("unroll") for (int k = 0; k < 2; ++k) \
;         acc[ai][bj][m][n] = __builtin_amdgcn_mfma_f32_16x16x32_bf16(Bt[n][k], At[m][k], acc[ai][bj][m][n], 0, 0, 0); __builtin_amdgcn_s_setprio(0); } while (0)
; #define PG8_WAIT_V(n) asm volatile("s_waitcnt vmcnt(" #n ")" ::: "memory")
; #define PG8_WAIT_L(n) asm volatile("s_waitcnt lgkmcnt(" #n ")" ::: "memory")
; #define PG8_BAR __builtin_amdgcn_s_barrier()
; #define PG8_SCHED __builtin_amdgcn_sched_barrier(0)
;     ...
;         for (int t = 0; t < nt; t += 2) {
;             const bool last = (t == nt - 2);
;     ...
;             PG8_LDA(At, 1, 1); PG8_STAGE(PG8_SB(1, 0), b3, voffB); PG8_STAGE(PG8_SB(1, 1), b3 + hstepB, voffB); PG8_STAGE_A(PG8_SA(1, 0), a3, 0, g2);
;             PG8_WAIT_V(8); PG8_WAIT_L(0); PG8_BAR; PG8_MMA(1, 0, At, B0); PG8_MMA(1, 1, At, B1); PG8_BAR; PG8_SCHED;
	s_add_i32 s19, s19, s62
	v_lshl_add_u64 v[142:143], v[142:143], 0, s[8:9]
	s_mov_b32 m0, s19
	ds_read_b128 v[188:191], v155 offset:49152
	ds_read_b128 v[192:195], v155 offset:50176
	ds_read_b128 v[196:199], v155 offset:51200
	ds_read_b128 v[200:203], v155 offset:52224
	ds_read_b128 v[208:211], v155 offset:53248
	ds_read_b128 v[216:219], v155 offset:54272
	ds_read_b128 v[220:223], v155 offset:55296
	ds_read_b128 v[224:227], v155 offset:56320
	global_load_lds_dwordx4 v[142:143], off
	s_add_i32 m0, s19, 0x2000
	s_add_u32 s0, s0, 0x40080
	v_lshl_add_u64 v[142:143], v[204:205], 0, s[8:9]
	s_addc_u32 s1, s1, 0
	s_add_i32 s19, s22, s62
	global_load_lds_dwordx4 v[142:143], off
	v_lshl_add_u64 v[142:143], s[0:1], 0, v[206:207]
	s_mov_b32 m0, s19
	s_nop 0
	global_load_lds_dwordx4 v[142:143], off
	v_lshl_add_u64 v[142:143], s[0:1], 0, v[134:135]
	s_add_i32 m0, s19, 0x2000
	s_nop 0
	global_load_lds_dwordx4 v[142:143], off
	v_lshl_add_u64 v[142:143], v[212:213], 0, s[8:9]
	s_mov_b32 m0, s70
	s_nop 0
	global_load_lds_dwordx4 v[142:143], off
	v_lshl_add_u64 v[142:143], v[214:215], 0, s[8:9]
	s_mov_b32 m0, s71
	s_nop 0
	global_load_lds_dwordx4 v[142:143], off
	s_waitcnt vmcnt(8)
	s_waitcnt lgkmcnt(0)
	s_barrier
	s_setprio 1
	s_waitcnt lgkmcnt(0)
	v_mfma_f32_16x16x32_bf16 v[62:65], v[156:159], v[188:191], v[62:65]
	v_mfma_f32_16x16x32_bf16 v[58:61], v[164:167], v[188:191], v[58:61]
	v_mfma_f32_16x16x32_bf16 v[54:57], v[156:159], v[196:199], v[54:57]
	v_mfma_f32_16x16x32_bf16 v[46:49], v[164:167], v[196:199], v[46:49]
	v_mfma_f32_16x16x32_bf16 v[38:41], v[156:159], v[208:211], v[38:41]
	v_mfma_f32_16x16x32_bf16 v[30:33], v[164:167], v[208:211], v[30:33]
	v_mfma_f32_16x16x32_bf16 v[22:25], v[156:159], v[220:223], v[22:25]
	v_mfma_f32_16x16x32_bf16 v[14:17], v[164:167], v[220:223], v[14:17]
	v_mfma_f32_16x16x32_bf16 v[62:65], v[160:163], v[192:195], v[62:65]
	v_mfma_f32_16x16x32_bf16 v[58:61], v[168:171], v[192:195], v[58:61]
	v_mfma_f32_16x16x32_bf16 v[54:57], v[160:163], v[200:203], v[54:57]
	v_mfma_f32_16x16x32_bf16 v[46:49], v[168:171], v[200:203], v[46:49]
	v_mfma_f32_16x16x32_bf16 v[38:41], v[160:163], v[216:219], v[38:41]
	v_mfma_f32_16x16x32_bf16 v[30:33], v[168:171], v[216:219], v[30:33]
	v_mfma_f32_16x16x32_bf16 v[22:25], v[160:163], v[224:227], v[22:25]
	v_mfma_f32_16x16x32_bf16 v[14:17], v[168:171], v[224:227], v[14:17]
	s_setprio 0
	s_setprio 1
	v_mfma_f32_16x16x32_bf16 v[50:53], v[172:175], v[188:191], v[50:53]
	v_mfma_f32_16x16x32_bf16 v[42:45], v[180:183], v[188:191], v[42:45]
	v_mfma_f32_16x16x32_bf16 v[34:37], v[172:175], v[196:199], v[34:37]
	v_mfma_f32_16x16x32_bf16 v[26:29], v[180:183], v[196:199], v[26:29]
	v_mfma_f32_16x16x32_bf16 v[18:21], v[172:175], v[208:211], v[18:21]
	v_mfma_f32_16x16x32_bf16 v[10:13], v[180:183], v[208:211], v[10:13]
	v_mfma_f32_16x16x32_bf16 v[6:9], v[172:175], v[220:223], v[6:9]
	v_mfma_f32_16x16x32_bf16 v[2:5], v[180:183], v[220:223], v[2:5]
	v_mfma_f32_16x16x32_bf16 v[50:53], v[176:179], v[192:195], v[50:53]
	v_mfma_f32_16x16x32_bf16 v[42:45], v[184:187], v[192:195], v[42:45]
	v_mfma_f32_16x16x32_bf16 v[34:37], v[176:179], v[200:203], v[34:37]
	v_mfma_f32_16x16x32_bf16 v[26:29], v[184:187], v[200:203], v[26:29]
	v_mfma_f32_16x16x32_bf16 v[18:21], v[176:179], v[216:219], v[18:21]
	v_mfma_f32_16x16x32_bf16 v[10:13], v[184:187], v[216:219], v[10:13]
	v_mfma_f32_16x16x32_bf16 v[6:9], v[176:179], v[224:227], v[6:9]
	v_mfma_f32_16x16x32_bf16 v[2:5], v[184:187], v[224:227], v[2:5]
	s_add_i32 s18, s18, 2
	s_add_u32 s24, s24, 0x100
	s_addc_u32 s25, s25, 0
	s_add_u32 s16, s16, 0x100
	s_addc_u32 s17, s17, 0
	s_cmp_gt_u32 s18, 13
	s_setprio 0
	s_barrier
	s_cbranch_scc0 .LBB0_2458
	s_and_b64 vcc, exec, s[42:43]
	s_cbranch_vccz .LBB0_2461
	s_barrier
